# nt (non-temporal) cache hint on the read-once f32 loads: weight-conversion tile loads, ada_w GEMV loads, norm_in x loads
# baseline (speedup 1.0000x reference)
.LBB0_14:
	v_lshl_add_u64 v[26:27], v[16:17], 0, s[30:31]
	v_add_co_u32_e64 v28, s[8:9], s4, v26
	global_load_dwordx4 v[22:25], v[26:27], off nt
	s_nop 0
	v_addc_co_u32_e64 v29, s[8:9], 0, v27, s[8:9]
	v_add_co_u32_e64 v30, s[8:9], s5, v26
	v_add_u32_e32 v68, 0x2000, v21
	s_nop 0
	v_addc_co_u32_e64 v31, s[8:9], 0, v27, s[8:9]
	v_add_co_u32_e64 v34, s[8:9], s33, v26
	s_add_u32 s30, s30, 0x600000
	s_nop 0
	v_addc_co_u32_e64 v35, s[8:9], 0, v27, s[8:9]
	v_add_co_u32_e64 v38, s[8:9], s34, v26
	s_addc_u32 s31, s31, 0
	s_nop 0
	v_addc_co_u32_e64 v39, s[8:9], 0, v27, s[8:9]
	v_add_co_u32_e64 v42, s[8:9], s35, v26
	s_cmp_eq_u32 s30, 0x6000000
	s_nop 0
	v_addc_co_u32_e64 v43, s[8:9], 0, v27, s[8:9]
	v_add_co_u32_e64 v46, s[8:9], s36, v26
	s_nop 1
	v_addc_co_u32_e64 v47, s[8:9], 0, v27, s[8:9]
	v_add_co_u32_e64 v50, s[8:9], s37, v26
	s_nop 1
	v_addc_co_u32_e64 v51, s[8:9], 0, v27, s[8:9]
	global_load_dwordx4 v[26:29], v[28:29], off nt
	s_nop 0
	global_load_dwordx4 v[30:33], v[30:31], off nt
	s_nop 0
	global_load_dwordx4 v[34:37], v[34:35], off nt
	s_nop 0
	global_load_dwordx4 v[38:41], v[38:39], off nt
	s_nop 0
	global_load_dwordx4 v[42:45], v[42:43], off nt
	s_nop 0
	global_load_dwordx4 v[46:49], v[46:47], off nt
	s_nop 0
	global_load_dwordx4 v[50:53], v[50:51], off nt
	ds_read2_b32 v[54:55], v21 offset1:16
	ds_read2_b32 v[56:57], v21 offset0:32 offset1:48
	ds_read2_b32 v[58:59], v21 offset0:64 offset1:80
	ds_read2_b32 v[60:61], v21 offset0:96 offset1:112
	ds_read2_b32 v[62:63], v68 offset1:16
	ds_read2_b32 v[64:65], v68 offset0:32 offset1:48
	ds_read2_b32 v[66:67], v68 offset0:64 offset1:80
	ds_read2_b32 v[68:69], v68 offset0:96 offset1:112
	v_add_u32_e32 v21, 0x200, v21
	s_waitcnt lgkmcnt(3)
	v_mov_b32_e32 v78, v63
	v_mov_b32_e32 v70, v55
	v_mov_b32_e32 v72, v57
	s_waitcnt lgkmcnt(2)
	v_mov_b32_e32 v80, v65
	v_mov_b32_e32 v74, v59
	s_waitcnt lgkmcnt(1)
	v_mov_b32_e32 v82, v67
	v_mov_b32_e32 v76, v61
	s_waitcnt lgkmcnt(0)
	v_mov_b32_e32 v84, v69
	s_waitcnt vmcnt(7)
	v_pk_fma_f32 v[2:3], v[22:23], v[54:55], v[2:3] op_sel_hi:[1,0,1]
	v_pk_fma_f32 v[4:5], v[24:25], v[54:55], v[4:5] op_sel_hi:[1,0,1]
	v_pk_fma_f32 v[6:7], v[22:23], v[62:63], v[6:7] op_sel_hi:[1,0,1]
	v_pk_fma_f32 v[8:9], v[24:25], v[62:63], v[8:9] op_sel_hi:[1,0,1]
	s_waitcnt vmcnt(6)
	v_pk_fma_f32 v[2:3], v[26:27], v[70:71], v[2:3] op_sel_hi:[1,0,1]
	v_pk_fma_f32 v[4:5], v[28:29], v[70:71], v[4:5] op_sel_hi:[1,0,1]
	v_pk_fma_f32 v[6:7], v[26:27], v[78:79], v[6:7] op_sel_hi:[1,0,1]
	v_pk_fma_f32 v[8:9], v[28:29], v[78:79], v[8:9] op_sel_hi:[1,0,1]
	s_waitcnt vmcnt(5)
	v_pk_fma_f32 v[4:5], v[32:33], v[56:57], v[4:5] op_sel_hi:[1,0,1]
	v_pk_fma_f32 v[2:3], v[30:31], v[56:57], v[2:3] op_sel_hi:[1,0,1]
	v_pk_fma_f32 v[8:9], v[32:33], v[64:65], v[8:9] op_sel_hi:[1,0,1]
	v_pk_fma_f32 v[6:7], v[30:31], v[64:65], v[6:7] op_sel_hi:[1,0,1]
	s_waitcnt vmcnt(4)
	v_pk_fma_f32 v[4:5], v[36:37], v[72:73], v[4:5] op_sel_hi:[1,0,1]
	v_pk_fma_f32 v[2:3], v[34:35], v[72:73], v[2:3] op_sel_hi:[1,0,1]
	v_pk_fma_f32 v[8:9], v[36:37], v[80:81], v[8:9] op_sel_hi:[1,0,1]
	v_pk_fma_f32 v[6:7], v[34:35], v[80:81], v[6:7] op_sel_hi:[1,0,1]
	s_waitcnt vmcnt(3)
	v_pk_fma_f32 v[4:5], v[40:41], v[58:59], v[4:5] op_sel_hi:[1,0,1]
	v_pk_fma_f32 v[2:3], v[38:39], v[58:59], v[2:3] op_sel_hi:[1,0,1]
	v_pk_fma_f32 v[8:9], v[40:41], v[66:67], v[8:9] op_sel_hi:[1,0,1]
	v_pk_fma_f32 v[6:7], v[38:39], v[66:67], v[6:7] op_sel_hi:[1,0,1]
	s_waitcnt vmcnt(2)
	v_pk_fma_f32 v[4:5], v[44:45], v[74:75], v[4:5] op_sel_hi:[1,0,1]
	v_pk_fma_f32 v[2:3], v[42:43], v[74:75], v[2:3] op_sel_hi:[1,0,1]
	v_pk_fma_f32 v[8:9], v[44:45], v[82:83], v[8:9] op_sel_hi:[1,0,1]
	v_pk_fma_f32 v[6:7], v[42:43], v[82:83], v[6:7] op_sel_hi:[1,0,1]
	s_waitcnt vmcnt(1)
	v_pk_fma_f32 v[4:5], v[48:49], v[60:61], v[4:5] op_sel_hi:[1,0,1]
	v_pk_fma_f32 v[2:3], v[46:47], v[60:61], v[2:3] op_sel_hi:[1,0,1]
	v_pk_fma_f32 v[8:9], v[48:49], v[68:69], v[8:9] op_sel_hi:[1,0,1]
	v_pk_fma_f32 v[6:7], v[46:47], v[68:69], v[6:7] op_sel_hi:[1,0,1]
	s_waitcnt vmcnt(0)
	v_pk_fma_f32 v[4:5], v[52:53], v[76:77], v[4:5] op_sel_hi:[1,0,1]
	v_pk_fma_f32 v[2:3], v[50:51], v[76:77], v[2:3] op_sel_hi:[1,0,1]
	v_pk_fma_f32 v[8:9], v[52:53], v[84:85], v[8:9] op_sel_hi:[1,0,1]
	v_pk_fma_f32 v[6:7], v[50:51], v[84:85], v[6:7] op_sel_hi:[1,0,1]
	s_cbranch_scc0 .LBB0_14
	ds_write_b128 v1, v[2:5] offset:16384
	ds_write_b128 v1, v[6:9] offset:22528

.LBB0_34:
	s_add_i32 s48, s37, 0x2d0
	s_cmpk_gt_i32 s48, 0x10f
	s_mov_b64 s[28:29], -1
	s_cbranch_scc0 .LBB0_48
	s_cmpk_gt_u32 s48, 0x1cf
	s_cbranch_scc0 .LBB0_43
	s_cmpk_gt_u32 s48, 0x2cf
	s_mov_b64 s[26:27], -1
	s_cbranch_scc0 .LBB0_38
	s_lshr_b32 s10, s37, 4
	s_lshl_b32 s24, s10, 11
	s_sub_i32 s24, s35, s24
	s_ashr_i32 s25, s24, 31
	s_lshl_b32 s10, s10, 6
	s_lshl_b64 s[26:27], s[24:25], 13
	s_add_u32 s28, s22, s26
	v_mov_b32_e32 v1, v0
	s_addc_u32 s29, s23, s27
	s_lshl_b64 s[26:27], s[10:11], 2
	s_add_u32 s26, s28, s26
	v_lshlrev_b32_e32 v2, 2, v1
	v_ashrrev_i32_e32 v16, 4, v1
	v_and_b32_e32 v24, 60, v2
	s_addc_u32 s27, s29, s27
	v_lshlrev_b32_e32 v18, 2, v24
	v_ashrrev_i32_e32 v17, 31, v16
	v_lshl_add_u64 v[2:3], s[26:27], 0, v[18:19]
	v_lshlrev_b64 v[4:5], 13, v[16:17]
	v_lshl_add_u64 v[10:11], v[2:3], 0, v[4:5]
	v_add_co_u32_e32 v6, vcc, s42, v10
	v_mul_u32_u24_e32 v17, 0x204, v24
	s_nop 0
	v_addc_co_u32_e32 v7, vcc, 0, v11, vcc
	v_add_co_u32_e32 v12, vcc, s43, v10
	global_load_dwordx4 v[2:5], v[10:11], off nt
	s_nop 0
	global_load_dwordx4 v[6:9], v[6:7], off nt
	v_addc_co_u32_e32 v13, vcc, 0, v11, vcc
	v_add_co_u32_e32 v10, vcc, s44, v10
	s_lshl_b64 s[26:27], s[10:11], 12
	s_nop 0
	v_addc_co_u32_e32 v11, vcc, 0, v11, vcc
	global_load_dwordx4 v[12:15], v[12:13], off nt
	s_nop 0
	global_load_dwordx4 v[20:23], v[10:11], off nt
	v_ashrrev_i32_e32 v10, 3, v1
	v_lshlrev_b32_e32 v1, 4, v1
	v_lshlrev_b32_e32 v11, 2, v16
	v_and_b32_e32 v18, 0x70, v1
	v_mul_lo_u32 v16, v10, s45
	v_add3_u32 v11, 0, v11, v17
	v_lshlrev_b32_e32 v1, 2, v18
	v_add_u32_e32 v17, 0x400, v11
	v_add3_u32 v1, 0, v16, v1
	s_barrier
	s_add_u32 s10, s3, s26
	s_addc_u32 s26, s4, s27
	s_lshl_b64 s[24:25], s[24:25], 1
	s_add_u32 s24, s10, s24
	s_addc_u32 s25, s26, s25
	s_mov_b64 s[26:27], 0
	s_waitcnt vmcnt(2)
	ds_write2_b32 v11, v2, v6 offset1:32
	ds_write2_b32 v11, v3, v7 offset0:129 offset1:161
	ds_write2_b32 v17, v4, v8 offset0:2 offset1:34
	ds_write2_b32 v17, v5, v9 offset0:131 offset1:163
	s_waitcnt vmcnt(0)
	ds_write2_b32 v11, v12, v20 offset0:64 offset1:96
	ds_write2_b32 v11, v13, v21 offset0:193 offset1:225
	ds_write2_b32 v17, v14, v22 offset0:66 offset1:98
	ds_write2_b32 v17, v15, v23 offset0:195 offset1:227
	s_waitcnt lgkmcnt(0)
	s_barrier
	ds_read2_b32 v[2:3], v1 offset1:1
	ds_read2_b32 v[4:5], v1 offset0:2 offset1:3
	ds_read2_b32 v[6:7], v1 offset0:4 offset1:5
	ds_read2_b32 v[8:9], v1 offset0:6 offset1:7
	ds_read2_b32 v[12:13], v1 offset0:8 offset1:9
	ds_read2_b32 v[14:15], v1 offset0:10 offset1:11
	ds_read2_b32 v[16:17], v1 offset0:12 offset1:13
	ds_read2_b32 v[20:21], v1 offset0:14 offset1:15
	s_waitcnt lgkmcnt(7)
	v_cvt_pk_bf16_f32 v2, v2, v3
	s_waitcnt lgkmcnt(6)
	v_cvt_pk_bf16_f32 v3, v4, v5
	s_waitcnt lgkmcnt(5)
	v_cvt_pk_bf16_f32 v4, v6, v7
	s_waitcnt lgkmcnt(4)
	v_cvt_pk_bf16_f32 v5, v8, v9
	s_waitcnt lgkmcnt(3)
	v_cvt_pk_bf16_f32 v6, v12, v13
	s_waitcnt lgkmcnt(2)
	v_cvt_pk_bf16_f32 v7, v14, v15
	s_waitcnt lgkmcnt(1)
	v_cvt_pk_bf16_f32 v8, v16, v17
	s_waitcnt lgkmcnt(0)
	v_cvt_pk_bf16_f32 v9, v20, v21
.LBB0_38:
	s_andn2_b64 vcc, exec, s[26:27]
	s_mov_b64 s[26:27], 12
	s_cbranch_vccnz .LBB0_42
	s_lshl_b32 s10, s39, 7
	s_and_b32 s10, s10, 0xfffffe00
	s_sub_i32 s24, s38, s10
	s_lshl_b32 s10, s37, 4
	s_ashr_i32 s25, s24, 31
	s_addk_i32 s10, 0x1000
	s_andn2_b32 s10, s10, 63
	s_lshl_b64 s[26:27], s[24:25], 14
	s_add_u32 s28, s20, s26
	v_mov_b32_e32 v1, v0
	s_addc_u32 s29, s21, s27
	s_lshl_b64 s[26:27], s[10:11], 2
	s_add_u32 s26, s28, s26
	v_lshlrev_b32_e32 v2, 2, v1
	v_ashrrev_i32_e32 v20, 4, v1
	v_and_b32_e32 v22, 60, v2
	s_addc_u32 s27, s29, s27
	v_lshlrev_b32_e32 v18, 2, v22
	v_ashrrev_i32_e32 v21, 31, v20
	v_lshl_add_u64 v[2:3], s[26:27], 0, v[18:19]
	v_lshlrev_b64 v[4:5], 14, v[20:21]
	v_lshl_add_u64 v[10:11], v[2:3], 0, v[4:5]
	v_add_co_u32_e32 v6, vcc, s43, v10
	s_nop 1
	v_addc_co_u32_e32 v7, vcc, 0, v11, vcc
	v_add_co_u32_e32 v12, vcc, 0x100000, v10
	global_load_dwordx4 v[2:5], v[10:11], off nt
	s_nop 0
	global_load_dwordx4 v[6:9], v[6:7], off nt
	v_addc_co_u32_e32 v13, vcc, 0, v11, vcc
	v_add_co_u32_e32 v14, vcc, 0x180000, v10
	s_nop 1
	v_addc_co_u32_e32 v15, vcc, 0, v11, vcc
	global_load_dwordx4 v[10:13], v[12:13], off nt
	s_nop 0
	global_load_dwordx4 v[14:17], v[14:15], off nt
	s_andn2_b64 vcc, exec, s[6:7]
	s_cbranch_vccnz .LBB0_41
	s_lshl_b64 s[26:27], s[24:25], 2
	s_add_u32 s26, s16, s26
	s_addc_u32 s27, s17, s27
	v_lshl_add_u64 v[24:25], v[20:21], 2, s[26:27]
	global_load_dword v18, v[24:25], off
	global_load_dword v26, v[24:25], off offset:128
	global_load_dword v28, v[24:25], off offset:256
	s_nop 0
	global_load_dword v24, v[24:25], off offset:384
	s_waitcnt vmcnt(3)
	v_pk_mul_f32 v[4:5], v[4:5], v[18:19] op_sel_hi:[1,0]
	v_pk_mul_f32 v[2:3], v[2:3], v[18:19] op_sel_hi:[1,0]
	s_waitcnt vmcnt(2)
	v_pk_mul_f32 v[8:9], v[8:9], v[26:27] op_sel_hi:[1,0]
	v_pk_mul_f32 v[6:7], v[6:7], v[26:27] op_sel_hi:[1,0]
	s_waitcnt vmcnt(1)
	v_pk_mul_f32 v[12:13], v[12:13], v[28:29] op_sel_hi:[1,0]
	v_pk_mul_f32 v[10:11], v[10:11], v[28:29] op_sel_hi:[1,0]
	s_waitcnt vmcnt(0)
	v_pk_mul_f32 v[16:17], v[16:17], v[24:25] op_sel_hi:[1,0]
	v_pk_mul_f32 v[14:15], v[14:15], v[24:25] op_sel_hi:[1,0]

.LBB0_43:
	s_andn2_b64 vcc, exec, s[28:29]
	s_cbranch_vccnz .LBB0_47
	s_lshl_b32 s10, s41, 7
	s_and_b32 s10, s10, 0xfffffe00
	s_sub_i32 s24, s40, s10
	s_lshl_b32 s10, s37, 4
	s_addk_i32 s10, 0x1c00
	s_ashr_i32 s25, s24, 31
	s_andn2_b32 s10, s10, 63
	s_mul_i32 s27, s24, 0x3000
	s_mul_hi_i32 s26, s24, 0x3000
	s_add_u32 s28, s18, s27
	v_mov_b32_e32 v1, v0
	s_addc_u32 s29, s19, s26
	s_lshl_b64 s[26:27], s[10:11], 2
	s_add_u32 s26, s28, s26
	v_lshlrev_b32_e32 v2, 2, v1
	v_and_b32_e32 v22, 60, v2
	s_addc_u32 s27, s29, s27
	v_ashrrev_i32_e32 v20, 4, v1
	v_lshlrev_b32_e32 v18, 2, v22
	v_lshl_add_u64 v[10:11], s[26:27], 0, v[18:19]
	v_add_u32_e32 v4, 32, v20
	v_add_u32_e32 v12, 64, v20
	v_add_u32_e32 v14, 0x60, v20
	v_mad_i64_i32 v[2:3], s[26:27], v20, s46, v[10:11]
	v_mad_i64_i32 v[6:7], s[26:27], v4, s46, v[10:11]
	v_mad_i64_i32 v[12:13], s[26:27], v12, s46, v[10:11]
	v_mad_i64_i32 v[14:15], s[26:27], v14, s46, v[10:11]
	global_load_dwordx4 v[2:5], v[2:3], off nt
	s_nop 0
	global_load_dwordx4 v[6:9], v[6:7], off nt
	s_nop 0
	global_load_dwordx4 v[10:13], v[12:13], off nt
	s_nop 0
	global_load_dwordx4 v[14:17], v[14:15], off nt
	s_andn2_b64 vcc, exec, s[8:9]
	v_ashrrev_i32_e32 v21, 31, v20
	s_cbranch_vccnz .LBB0_46
	s_lshl_b64 s[26:27], s[24:25], 2
	s_add_u32 s26, s14, s26
	s_addc_u32 s27, s15, s27
	v_lshl_add_u64 v[24:25], v[20:21], 2, s[26:27]
	global_load_dword v18, v[24:25], off
	global_load_dword v26, v[24:25], off offset:128
	global_load_dword v28, v[24:25], off offset:256
	s_nop 0
	global_load_dword v24, v[24:25], off offset:384
	s_waitcnt vmcnt(3)
	v_pk_mul_f32 v[4:5], v[4:5], v[18:19] op_sel_hi:[1,0]
	v_pk_mul_f32 v[2:3], v[2:3], v[18:19] op_sel_hi:[1,0]
	s_waitcnt vmcnt(2)
	v_pk_mul_f32 v[8:9], v[8:9], v[26:27] op_sel_hi:[1,0]
	v_pk_mul_f32 v[6:7], v[6:7], v[26:27] op_sel_hi:[1,0]
	s_waitcnt vmcnt(1)
	v_pk_mul_f32 v[12:13], v[12:13], v[28:29] op_sel_hi:[1,0]
	v_pk_mul_f32 v[10:11], v[10:11], v[28:29] op_sel_hi:[1,0]
	s_waitcnt vmcnt(0)
	v_pk_mul_f32 v[16:17], v[16:17], v[24:25] op_sel_hi:[1,0]
	v_pk_mul_f32 v[14:15], v[14:15], v[24:25] op_sel_hi:[1,0]

.LBB0_48:
	s_andn2_b64 vcc, exec, s[28:29]
	s_cbranch_vccnz .LBB0_33
	s_ashr_i32 s10, s48, 31
	s_lshr_b32 s10, s10, 28
	s_add_i32 s48, s48, s10
	s_ashr_i32 s10, s48, 4
	s_lshl_b32 s24, s10, 11
	s_sub_i32 s24, s34, s24
	s_lshl_b32 s26, s10, 6
	s_ashr_i32 s25, s24, 31
	s_ashr_i32 s27, s26, 31
	s_mul_i32 s28, s24, 0x1100
	s_mul_hi_i32 s10, s24, 0x1100
	s_add_u32 s48, s12, s28
	v_mov_b32_e32 v1, v0
	s_addc_u32 s10, s13, s10
	s_lshl_b64 s[28:29], s[26:27], 2
	s_add_u32 s28, s48, s28
	v_lshlrev_b32_e32 v2, 2, v1
	v_and_b32_e32 v17, 60, v2
	s_addc_u32 s29, s10, s29
	v_ashrrev_i32_e32 v16, 4, v1
	v_lshlrev_b32_e32 v18, 2, v17
	v_lshl_add_u64 v[10:11], s[28:29], 0, v[18:19]
	v_add_u32_e32 v4, 32, v16
	v_add_u32_e32 v12, 64, v16
	v_mad_i64_i32 v[2:3], s[28:29], v16, s47, v[10:11]
	v_mad_i64_i32 v[6:7], s[28:29], v4, s47, v[10:11]
	v_mad_i64_i32 v[12:13], s[28:29], v12, s47, v[10:11]
	v_add_u32_e32 v14, 0x60, v16
	global_load_dwordx4 v[2:5], v[2:3], off nt
	s_nop 0
	global_load_dwordx4 v[6:9], v[6:7], off nt
	v_mad_i64_i32 v[10:11], s[28:29], v14, s47, v[10:11]
	global_load_dwordx4 v[12:15], v[12:13], off nt
	s_nop 0
	global_load_dwordx4 v[20:23], v[10:11], off nt
	v_ashrrev_i32_e32 v10, 3, v1
	v_lshlrev_b32_e32 v1, 4, v1
	v_lshlrev_b32_e32 v11, 2, v16
	v_mul_u32_u24_e32 v17, 0x204, v17
	v_and_b32_e32 v18, 0x70, v1
	v_mul_lo_u32 v16, v10, s45
	v_add3_u32 v11, 0, v11, v17
	v_lshlrev_b32_e32 v1, 2, v18
	v_add_u32_e32 v17, 0x400, v11
	v_add3_u32 v1, 0, v16, v1
	s_lshl_b64 s[26:27], s[26:27], 12
	s_barrier
	s_add_u32 s10, s0, s26
	s_addc_u32 s26, s1, s27
	s_lshl_b64 s[24:25], s[24:25], 1
	s_add_u32 s24, s10, s24
	s_addc_u32 s25, s26, s25
	s_mov_b64 s[26:27], 12
	s_waitcnt vmcnt(2)
	ds_write2_b32 v11, v2, v6 offset1:32
	ds_write2_b32 v11, v3, v7 offset0:129 offset1:161
	ds_write2_b32 v17, v4, v8 offset0:2 offset1:34
	ds_write2_b32 v17, v5, v9 offset0:131 offset1:163
	s_waitcnt vmcnt(0)
	ds_write2_b32 v11, v12, v20 offset0:64 offset1:96
	ds_write2_b32 v11, v13, v21 offset0:193 offset1:225
	ds_write2_b32 v17, v14, v22 offset0:66 offset1:98
	ds_write2_b32 v17, v15, v23 offset0:195 offset1:227
	s_waitcnt lgkmcnt(0)
	s_barrier
	ds_read2_b32 v[2:3], v1 offset1:1
	ds_read2_b32 v[4:5], v1 offset0:2 offset1:3
	ds_read2_b32 v[6:7], v1 offset0:4 offset1:5
	ds_read2_b32 v[8:9], v1 offset0:6 offset1:7
	ds_read2_b32 v[12:13], v1 offset0:8 offset1:9
	ds_read2_b32 v[14:15], v1 offset0:10 offset1:11
	ds_read2_b32 v[16:17], v1 offset0:12 offset1:13
	ds_read2_b32 v[20:21], v1 offset0:14 offset1:15
	s_waitcnt lgkmcnt(7)
	v_cvt_pk_bf16_f32 v2, v2, v3
	s_waitcnt lgkmcnt(6)
	v_cvt_pk_bf16_f32 v3, v4, v5
	s_waitcnt lgkmcnt(5)
	v_cvt_pk_bf16_f32 v4, v6, v7
	s_waitcnt lgkmcnt(4)
	v_cvt_pk_bf16_f32 v5, v8, v9
	s_waitcnt lgkmcnt(3)
	v_cvt_pk_bf16_f32 v6, v12, v13
	s_waitcnt lgkmcnt(2)
	v_cvt_pk_bf16_f32 v7, v14, v15
	s_waitcnt lgkmcnt(1)
	v_cvt_pk_bf16_f32 v8, v16, v17
	s_waitcnt lgkmcnt(0)
	v_cvt_pk_bf16_f32 v9, v20, v21
	s_branch .LBB0_33

.LBB0_108:
	v_readlane_b32 s0, v253, 11
	v_readlane_b32 s1, v253, 12
	s_mov_b32 s3, s1
	s_cmp_lt_i32 s0, 3
	s_cselect_b64 s[0:1], -1, 0
	s_cmp_gt_i32 s3, 2
	s_cselect_b64 s[4:5], -1, 0
	s_and_b64 s[0:1], s[0:1], s[4:5]
	s_andn2_b64 vcc, exec, s[0:1]
	s_cbranch_vccnz .LBB0_115
	v_readlane_b32 s14, v253, 0
	v_readlane_b32 s15, v253, 1
	s_load_dwordx2 s[0:1], s[14:15], 0x30
	s_load_dwordx2 s[6:7], s[14:15], 0xd0
	v_mov_b32_e32 v1, v0
	v_mov_b32_e32 v18, v0
	v_mov_b32_e32 v19, v0
	s_mov_b32 s3, 0x702000
	v_lshlrev_b32_e32 v2, 2, v19
	v_ashrrev_i32_e32 v3, 31, v2
	v_lshlrev_b64 v[2:3], 2, v[2:3]
	s_waitcnt lgkmcnt(0)
	v_lshl_add_u64 v[6:7], s[6:7], 0, v[2:3]
	v_lshl_add_u64 v[14:15], s[0:1], 0, v[2:3]
	v_add_co_u32_e32 v2, vcc, s3, v6
	s_mov_b32 s3, 0x700000
	s_nop 0
	v_addc_co_u32_e32 v3, vcc, 0, v7, vcc
	v_add_co_u32_e32 v16, vcc, s3, v6
	global_load_dwordx4 v[2:5], v[2:3], off nt
	s_nop 0
	v_addc_co_u32_e32 v17, vcc, 0, v7, vcc
	global_load_dwordx4 v[6:9], v[16:17], off nt
	global_load_dwordx4 v[10:13], v[14:15], off nt
	v_mov_b32_e32 v14, v0
	v_lshl_add_u32 v15, v19, 4, 0
	s_mov_b32 s3, 0x70e000
	s_waitcnt vmcnt(2)
	v_pk_add_f32 v[4:5], v[4:5], 1.0 op_sel_hi:[1,0]
	v_pk_add_f32 v[2:3], v[2:3], 1.0 op_sel_hi:[1,0]
	s_waitcnt vmcnt(1)
	ds_write_b128 v15, v[6:9] offset:8192
	s_waitcnt vmcnt(0)
	v_pk_mul_f32 v[4:5], v[12:13], v[4:5]
	v_pk_mul_f32 v[2:3], v[10:11], v[2:3]
	ds_write_b128 v15, v[2:5]
	v_ashrrev_i32_e32 v15, 6, v18
	v_lshlrev_b32_e32 v2, 2, v14
	v_ashrrev_i32_e32 v3, 31, v2
	v_lshlrev_b64 v[2:3], 2, v[2:3]
	v_lshl_add_u64 v[10:11], s[6:7], 0, v[2:3]
	v_add_co_u32_e32 v6, vcc, s3, v10
	v_lshl_add_u64 v[4:5], s[0:1], 0, v[2:3]
	s_nop 0
	v_addc_co_u32_e32 v7, vcc, 0, v11, vcc
	v_add_co_u32_e32 v10, vcc, 0x70c000, v10
	global_load_dwordx4 v[6:9], v[6:7], off nt
	s_nop 0
	v_addc_co_u32_e32 v11, vcc, 0, v11, vcc
	global_load_dwordx4 v[2:5], v[4:5], off nt
	s_movk_i32 s0, 0x4100
	global_load_dwordx4 v[10:13], v[10:11], off nt
	v_lshl_add_u32 v78, s2, 3, v15
	v_lshl_add_u32 v14, v14, 4, 0
	v_cmp_gt_i32_e32 vcc, s0, v78
	s_waitcnt vmcnt(2)
	v_pk_add_f32 v[8:9], v[8:9], 1.0 op_sel_hi:[1,0]
	v_pk_add_f32 v[6:7], v[6:7], 1.0 op_sel_hi:[1,0]
	s_waitcnt vmcnt(1)
	v_pk_mul_f32 v[4:5], v[4:5], v[8:9]
	v_pk_mul_f32 v[2:3], v[2:3], v[6:7]
	s_waitcnt vmcnt(0)
	ds_write_b128 v14, v[10:13] offset:24576
	ds_write_b128 v14, v[2:5] offset:16384
	s_waitcnt lgkmcnt(0)
	s_barrier
	s_and_saveexec_b64 s[8:9], vcc
	s_cbranch_execz .LBB0_114
	s_load_dwordx2 s[10:11], s[14:15], 0x0
	s_load_dwordx2 s[12:13], s[14:15], 0x10
	s_movk_i32 s1, 0x3fff
	v_ashrrev_i32_e32 v79, 31, v78
	v_add_u32_e32 v2, 0xffffc000, v78
	v_cmp_lt_i32_e32 vcc, s1, v78
	s_waitcnt lgkmcnt(0)
	v_mov_b32_e32 v4, s11
	v_mov_b32_e32 v5, s13
	v_cndmask_b32_e64 v3, v79, 0, vcc
	v_cndmask_b32_e32 v2, v78, v2, vcc
	v_cndmask_b32_e32 v5, v4, v5, vcc
	v_mov_b32_e32 v4, s10
	v_mov_b32_e32 v6, s12
	v_cndmask_b32_e32 v4, v4, v6, vcc
	v_lshlrev_b64 v[2:3], 13, v[2:3]
	v_lshl_add_u64 v[2:3], v[4:5], 0, v[2:3]
	v_lshlrev_b32_e32 v4, 2, v1
	v_and_b32_e32 v42, 0xfc, v4
	v_mov_b32_e32 v67, 0
	v_lshlrev_b32_e32 v66, 2, v42
	v_lshl_add_u64 v[10:11], v[2:3], 0, v[66:67]
	global_load_dwordx4 v[38:41], v[10:11], off nt
	global_load_dwordx4 v[30:33], v[10:11], off offset:1024 nt
	s_movk_i32 s3, 0x1000
	v_add_co_u32_e32 v12, vcc, s3, v10
	v_mbcnt_lo_u32_b32 v43, -1, 0
	s_nop 0
	v_addc_co_u32_e32 v13, vcc, 0, v11, vcc
	global_load_dwordx4 v[6:9], v[12:13], off offset:2048 nt
	global_load_dwordx4 v[2:5], v[12:13], off offset:3072 nt
	global_load_dwordx4 v[34:37], v[10:11], off offset:2048 nt
	global_load_dwordx4 v[26:29], v[10:11], off offset:3072 nt
	global_load_dwordx4 v[22:25], v[12:13], off nt
	global_load_dwordx4 v[18:21], v[12:13], off offset:1024 nt
	v_mbcnt_hi_u32_b32 v43, -1, v43
	v_and_b32_e32 v47, 63, v1
	v_lshlrev_b64 v[44:45], 12, v[78:79]
	v_and_b32_e32 v49, 64, v43
	v_xor_b32_e32 v51, 1, v43
	v_lshl_or_b32 v44, v47, 3, v44
	v_add_u32_e32 v47, 64, v49
	v_xor_b32_e32 v53, 2, v43
	v_or_b32_e32 v46, 0x400, v42
	v_cmp_lt_i32_e32 vcc, v51, v47
	v_xor_b32_e32 v54, 4, v43
	v_or_b32_e32 v48, 0x500, v42
	v_lshlrev_b32_e32 v68, 2, v46
	v_cndmask_b32_e32 v46, v43, v51, vcc
	v_cmp_lt_i32_e32 vcc, v53, v47
	v_xor_b32_e32 v55, 8, v43
	v_lshlrev_b32_e32 v70, 2, v48
	v_cndmask_b32_e32 v48, v43, v53, vcc
	v_cmp_lt_i32_e32 vcc, v54, v47
	v_xor_b32_e32 v56, 16, v43
	v_or_b32_e32 v50, 0x600, v42
	v_cndmask_b32_e32 v49, v43, v54, vcc
	v_cmp_lt_i32_e32 vcc, v55, v47
	v_xor_b32_e32 v57, 32, v43
	v_lshlrev_b32_e32 v72, 2, v50
	v_cndmask_b32_e32 v50, v43, v55, vcc
	v_cmp_lt_i32_e32 vcc, v56, v47
	s_lshl_b32 s14, s60, 3
	s_mov_b64 s[4:5], 0x25000000
	v_cndmask_b32_e32 v51, v43, v56, vcc
	v_cmp_lt_i32_e32 vcc, v57, v47
	s_ashr_i32 s15, s14, 31
	v_or_b32_e32 v52, 0x700, v42
	v_lshl_add_u64 v[44:45], s[6:7], 0, v[44:45]
	v_cndmask_b32_e32 v43, v43, v57, vcc
	s_mov_b64 s[16:17], 0
	s_movk_i32 s3, 0x40ff
	v_mov_b32_e32 v1, 0x358637bd
	v_mov_b32_e32 v80, 0x4000
	s_lshl_b64 s[18:19], s[14:15], 12
	v_add_u32_e32 v79, 0, v66
	v_lshlrev_b32_e32 v74, 2, v52
	v_lshl_add_u64 v[76:77], v[44:45], 0, s[4:5]
	v_lshlrev_b32_e32 v81, 2, v46
	v_lshlrev_b32_e32 v82, 2, v48
	v_lshlrev_b32_e32 v83, 2, v49
	v_lshlrev_b32_e32 v84, 2, v50
	v_lshlrev_b32_e32 v85, 2, v51
	v_lshlrev_b32_e32 v86, 2, v43
	v_lshlrev_b32_e32 v66, 2, v42
	s_waitcnt vmcnt(4)
	v_mov_b32_e32 v88, v2
	v_mov_b32_e32 v89, v3
	v_mov_b32_e32 v90, v4
	v_mov_b32_e32 v91, v5
	s_branch .LBB0_112

.LBB0_112:
	v_add_u32_e32 v87, s14, v78
	v_cmp_gt_i32_e64 s[6:7], s0, v87
	v_cmp_lt_i32_e32 vcc, s3, v87
	s_and_saveexec_b64 s[20:21], s[6:7]
	s_cbranch_execz .LBB0_111
	v_ashrrev_i32_e32 v10, 31, v87
	v_add_u32_e32 v12, 0xffffc000, v87
	v_cmp_lt_i32_e64 s[6:7], s1, v87
	v_mov_b32_e32 v13, s13
	v_mov_b32_e32 v14, s12
	v_cndmask_b32_e64 v11, v10, 0, s[6:7]
	v_cndmask_b32_e64 v10, v87, v12, s[6:7]
	v_mov_b32_e32 v12, s11
	v_cndmask_b32_e64 v13, v12, v13, s[6:7]
	v_mov_b32_e32 v12, s10
	v_cndmask_b32_e64 v12, v12, v14, s[6:7]
	v_lshlrev_b64 v[10:11], 13, v[10:11]
	v_lshl_add_u64 v[10:11], v[12:13], 0, v[10:11]
	v_lshl_add_u64 v[12:13], v[10:11], 0, v[66:67]
	global_load_dwordx4 v[54:57], v[12:13], off nt
	global_load_dwordx4 v[50:53], v[12:13], off offset:1024 nt
	global_load_dwordx4 v[46:49], v[12:13], off offset:2048 nt
	global_load_dwordx4 v[42:45], v[12:13], off offset:3072 nt
	v_mov_b32_e32 v69, v67
	v_mov_b32_e32 v71, v67
	v_mov_b32_e32 v73, v67
	v_lshl_add_u64 v[12:13], v[10:11], 0, v[68:69]
	v_lshl_add_u64 v[14:15], v[10:11], 0, v[70:71]
	v_lshl_add_u64 v[92:93], v[10:11], 0, v[72:73]
	v_mov_b32_e32 v75, v67
	global_load_dwordx4 v[62:65], v[12:13], off nt
	global_load_dwordx4 v[58:61], v[14:15], off nt
	v_lshl_add_u64 v[94:95], v[10:11], 0, v[74:75]
	global_load_dwordx4 v[14:17], v[92:93], off nt
	global_load_dwordx4 v[10:13], v[94:95], off nt
	s_branch .LBB0_111

.LBB0_243:
	s_or_b64 exec, exec, s[10:11]
	s_waitcnt lgkmcnt(0)
	s_barrier
	ds_read_b32 v1, v11 offset:40960
	s_mov_b64 s[10:11], -1
	s_waitcnt lgkmcnt(0)
	v_cmp_lt_u32_e32 vcc, s31, v1
	v_readfirstlane_b32 s26, v1
	s_cbranch_vccnz .LBB0_236
	s_cmpk_lt_u32 s26, 0x4a00
	s_cbranch_scc0 .LBB0_252
	s_cmpk_gt_u32 s26, 0x41ff
	s_cbranch_scc0 .LBB0_251
	s_cmpk_gt_u32 s26, 0x47ff
	s_cbranch_scc0 .LBB0_248
	s_add_i32 s8, s26, 0xffffb800
	s_lshr_b32 s12, s8, 4
	s_lshl_b32 s10, s12, 11
	s_lshl_b32 s8, s8, 7
	s_sub_i32 s10, s8, s10
	s_ashr_i32 s11, s10, 31
	s_lshl_b32 s8, s12, 6
	s_lshl_b64 s[12:13], s[10:11], 13
	s_add_u32 s27, s24, s12
	v_mov_b32_e32 v1, v0
	s_addc_u32 s40, s25, s13
	s_lshl_b64 s[12:13], s[8:9], 2
	s_add_u32 s12, s27, s12
	v_lshlrev_b32_e32 v2, 2, v1
	v_ashrrev_i32_e32 v12, 4, v1
	v_and_b32_e32 v24, 60, v2
	s_addc_u32 s13, s40, s13
	v_lshlrev_b32_e32 v10, 2, v24
	v_ashrrev_i32_e32 v13, 31, v12
	v_lshl_add_u64 v[2:3], s[12:13], 0, v[10:11]
	v_lshlrev_b64 v[4:5], 13, v[12:13]
	v_lshl_add_u64 v[14:15], v[2:3], 0, v[4:5]
	v_add_co_u32_e32 v6, vcc, s33, v14
	v_ashrrev_i32_e32 v22, 3, v1
	s_nop 0
	v_addc_co_u32_e32 v7, vcc, 0, v15, vcc
	v_add_co_u32_e32 v16, vcc, s34, v14
	global_load_dwordx4 v[2:5], v[14:15], off nt
	s_nop 0
	global_load_dwordx4 v[6:9], v[6:7], off nt
	v_addc_co_u32_e32 v17, vcc, 0, v15, vcc
	v_add_co_u32_e32 v18, vcc, s35, v14
	v_lshlrev_b32_e32 v1, 4, v1
	s_nop 0
	v_addc_co_u32_e32 v19, vcc, 0, v15, vcc
	global_load_dwordx4 v[14:17], v[16:17], off nt
	s_nop 0
	global_load_dwordx4 v[18:21], v[18:19], off nt
	v_lshlrev_b32_e32 v10, 2, v12
	v_ashrrev_i32_e32 v23, 31, v22
	v_mul_u32_u24_e32 v24, 0x204, v24
	v_mul_lo_u32 v25, v22, s36
	v_lshlrev_b64 v[12:13], 12, v[22:23]
	v_add3_u32 v22, 0, v10, v24
	v_and_b32_e32 v10, 0x70, v1
	v_lshlrev_b32_e32 v1, 2, v10
	v_add3_u32 v1, 0, v25, v1
	v_add_u32_e32 v23, 0x400, v22
	s_lshl_b64 s[12:13], s[8:9], 12
	s_barrier
	s_add_u32 s8, s0, s12
	s_addc_u32 s12, s1, s13
	s_lshl_b64 s[10:11], s[10:11], 1
	s_add_u32 s10, s8, s10
	s_addc_u32 s11, s12, s11
	v_lshl_add_u64 v[12:13], s[10:11], 0, v[12:13]
	s_mov_b64 s[10:11], 0
	s_waitcnt vmcnt(2)
	ds_write2_b32 v22, v2, v6 offset1:32
	ds_write2_b32 v22, v3, v7 offset0:129 offset1:161
	ds_write2_b32 v23, v4, v8 offset0:2 offset1:34
	ds_write2_b32 v23, v5, v9 offset0:131 offset1:163
	s_waitcnt vmcnt(0)
	ds_write2_b32 v22, v14, v18 offset0:64 offset1:96
	ds_write2_b32 v22, v15, v19 offset0:193 offset1:225
	ds_write2_b32 v23, v16, v20 offset0:66 offset1:98
	ds_write2_b32 v23, v17, v21 offset0:195 offset1:227
	s_waitcnt lgkmcnt(0)
	s_barrier
	ds_read2_b32 v[2:3], v1 offset1:1
	ds_read2_b32 v[4:5], v1 offset0:2 offset1:3
	ds_read2_b32 v[6:7], v1 offset0:4 offset1:5
	ds_read2_b32 v[8:9], v1 offset0:6 offset1:7
	ds_read2_b32 v[14:15], v1 offset0:8 offset1:9
	ds_read2_b32 v[16:17], v1 offset0:10 offset1:11
	ds_read2_b32 v[18:19], v1 offset0:12 offset1:13
	ds_read2_b32 v[20:21], v1 offset0:14 offset1:15
	s_waitcnt lgkmcnt(7)
	v_cvt_pk_bf16_f32 v2, v2, v3
	s_waitcnt lgkmcnt(6)
	v_cvt_pk_bf16_f32 v3, v4, v5
	s_waitcnt lgkmcnt(5)
	v_cvt_pk_bf16_f32 v4, v6, v7
	s_waitcnt lgkmcnt(4)
	v_cvt_pk_bf16_f32 v5, v8, v9
	s_waitcnt lgkmcnt(3)
	v_cvt_pk_bf16_f32 v6, v14, v15
	s_waitcnt lgkmcnt(2)
	v_cvt_pk_bf16_f32 v7, v16, v17
	s_waitcnt lgkmcnt(1)
	v_cvt_pk_bf16_f32 v8, v18, v19
	s_waitcnt lgkmcnt(0)
	v_cvt_pk_bf16_f32 v9, v20, v21
.LBB0_248:
	s_andn2_b64 vcc, exec, s[10:11]
	s_cbranch_vccnz .LBB0_250
	s_add_i32 s8, s26, 0xffffbe00
	s_lshr_b32 s12, s8, 4
	s_lshl_b32 s10, s12, 11
	s_lshl_b32 s8, s8, 7
	s_sub_i32 s10, s8, s10
	s_ashr_i32 s11, s10, 31
	s_lshl_b32 s8, s12, 6
	s_mul_i32 s13, s10, 0x6000
	s_mul_hi_i32 s12, s10, 0x6000
	s_add_u32 s27, s22, s13
	v_mov_b32_e32 v1, v0
	s_addc_u32 s40, s23, s12
	s_lshl_b64 s[12:13], s[8:9], 2
	s_add_u32 s12, s27, s12
	v_lshlrev_b32_e32 v2, 2, v1
	v_and_b32_e32 v22, 60, v2
	s_addc_u32 s13, s40, s13
	v_ashrrev_i32_e32 v21, 4, v1
	v_lshlrev_b32_e32 v10, 2, v22
	v_lshl_add_u64 v[12:13], s[12:13], 0, v[10:11]
	v_add_u32_e32 v10, 64, v21
	v_add_u32_e32 v4, 32, v21
	v_mad_i64_i32 v[14:15], s[12:13], v10, s37, v[12:13]
	v_add_u32_e32 v10, 0x60, v21
	v_mad_i64_i32 v[2:3], s[12:13], v21, s37, v[12:13]
	v_mad_i64_i32 v[6:7], s[12:13], v4, s37, v[12:13]
	v_mad_i64_i32 v[16:17], s[12:13], v10, s37, v[12:13]
	global_load_dwordx4 v[2:5], v[2:3], off nt
	s_nop 0
	global_load_dwordx4 v[6:9], v[6:7], off nt
	s_nop 0
	global_load_dwordx4 v[12:15], v[14:15], off nt
	s_nop 0
	global_load_dwordx4 v[16:19], v[16:17], off nt
	v_ashrrev_i32_e32 v20, 3, v1
	v_lshlrev_b32_e32 v1, 4, v1
	v_lshlrev_b32_e32 v10, 2, v21
	v_mul_u32_u24_e32 v22, 0x204, v22
	v_add3_u32 v22, 0, v10, v22
	v_and_b32_e32 v10, 0x70, v1
	v_mul_lo_u32 v23, v20, s36
	v_lshlrev_b32_e32 v1, 2, v10
	s_lshl_b64 s[12:13], s[8:9], 12
	v_add3_u32 v1, 0, v23, v1
	v_add_u32_e32 v24, 0x400, v22
	s_add_u32 s8, s3, s12
	s_barrier
	s_addc_u32 s12, s4, s13
	s_lshl_b64 s[10:11], s[10:11], 1
	v_ashrrev_i32_e32 v21, 31, v20
	s_add_u32 s10, s8, s10
	v_lshlrev_b64 v[20:21], 12, v[20:21]
	s_addc_u32 s11, s12, s11
	s_waitcnt vmcnt(2)
	ds_write2_b32 v22, v2, v6 offset1:32
	ds_write2_b32 v22, v3, v7 offset0:129 offset1:161
	ds_write2_b32 v24, v4, v8 offset0:2 offset1:34
	ds_write2_b32 v24, v5, v9 offset0:131 offset1:163
	s_waitcnt vmcnt(0)
	ds_write2_b32 v22, v12, v16 offset0:64 offset1:96
	ds_write2_b32 v22, v13, v17 offset0:193 offset1:225
	ds_write2_b32 v24, v14, v18 offset0:66 offset1:98
	ds_write2_b32 v24, v15, v19 offset0:195 offset1:227
	s_waitcnt lgkmcnt(0)
	s_barrier
	ds_read2_b32 v[2:3], v1 offset1:1
	ds_read2_b32 v[4:5], v1 offset0:2 offset1:3
	ds_read2_b32 v[6:7], v1 offset0:4 offset1:5
	ds_read2_b32 v[8:9], v1 offset0:6 offset1:7
	ds_read2_b32 v[12:13], v1 offset0:8 offset1:9
	ds_read2_b32 v[14:15], v1 offset0:10 offset1:11
	ds_read2_b32 v[16:17], v1 offset0:12 offset1:13
	ds_read2_b32 v[18:19], v1 offset0:14 offset1:15
	s_waitcnt lgkmcnt(7)
	v_cvt_pk_bf16_f32 v2, v2, v3
	s_waitcnt lgkmcnt(6)
	v_cvt_pk_bf16_f32 v3, v4, v5
	s_waitcnt lgkmcnt(5)
	v_cvt_pk_bf16_f32 v4, v6, v7
	s_waitcnt lgkmcnt(3)
	v_cvt_pk_bf16_f32 v6, v12, v13
	v_lshl_add_u64 v[12:13], s[10:11], 0, v[20:21]
	v_cvt_pk_bf16_f32 v5, v8, v9
	s_waitcnt lgkmcnt(2)
	v_cvt_pk_bf16_f32 v7, v14, v15
	s_waitcnt lgkmcnt(1)
	v_cvt_pk_bf16_f32 v8, v16, v17
	s_waitcnt lgkmcnt(0)
	v_cvt_pk_bf16_f32 v9, v18, v19

.LBB0_254:
	s_andn2_b64 vcc, exec, s[10:11]
	s_cbranch_vccnz .LBB0_235
	s_cmpk_gt_u32 s26, 0x2bff
	s_mov_b64 s[10:11], -1
	s_cbranch_scc0 .LBB0_257
	s_add_i32 s10, s26, 0xffffd400
	s_mul_i32 s11, s10, 0xba2f
	s_lshr_b32 s11, s11, 24
	s_mul_i32 s12, s11, 0xfffffea0
	s_add_i32 s11, s8, s11
	s_add_i32 s10, s12, s10
	s_mul_i32 s13, s11, 0xb00000
	s_mul_hi_u32 s12, s11, 0xb00000
	s_add_u32 s27, s14, s13
	s_addc_u32 s42, s15, s12
	s_mul_i32 s11, s11, 0x580000
	s_add_u32 s43, s5, s11
	s_mul_i32 s11, s10, 0x1746
	s_addc_u32 s44, s28, 0
	s_lshr_b32 s12, s11, 31
	s_lshr_b32 s11, s11, 16
	s_add_i32 s11, s11, s12
	s_sext_i32_i16 s45, s11
	s_mul_i32 s11, s45, -11
	s_add_i32 s11, s11, s10
	s_lshl_b32 s10, s11, 7
	s_ashr_i32 s11, s10, 31
	s_lshl_b32 s12, s45, 6
	s_ashr_i32 s13, s12, 31
	s_lshl_b64 s[40:41], s[10:11], 13
	s_add_u32 s27, s27, s40
	v_mov_b32_e32 v1, v0
	s_addc_u32 s42, s42, s41
	s_lshl_b64 s[40:41], s[12:13], 2
	s_add_u32 s40, s27, s40
	v_lshlrev_b32_e32 v2, 2, v1
	v_ashrrev_i32_e32 v12, 4, v1
	v_and_b32_e32 v22, 60, v2
	s_addc_u32 s41, s42, s41
	v_lshlrev_b32_e32 v10, 2, v22
	v_ashrrev_i32_e32 v13, 31, v12
	v_lshl_add_u64 v[2:3], s[40:41], 0, v[10:11]
	v_lshlrev_b64 v[4:5], 13, v[12:13]
	v_lshl_add_u64 v[14:15], v[2:3], 0, v[4:5]
	v_add_co_u32_e32 v6, vcc, s33, v14
	v_ashrrev_i32_e32 v23, 3, v1
	s_nop 0
	v_addc_co_u32_e32 v7, vcc, 0, v15, vcc
	v_add_co_u32_e32 v16, vcc, s34, v14
	global_load_dwordx4 v[2:5], v[14:15], off nt
	s_nop 0
	global_load_dwordx4 v[6:9], v[6:7], off nt
	v_addc_co_u32_e32 v17, vcc, 0, v15, vcc
	v_add_co_u32_e32 v18, vcc, s35, v14
	v_lshlrev_b32_e32 v1, 4, v1
	s_nop 0
	v_addc_co_u32_e32 v19, vcc, 0, v15, vcc
	global_load_dwordx4 v[14:17], v[16:17], off nt
	s_nop 0
	global_load_dwordx4 v[18:21], v[18:19], off nt
	v_lshlrev_b32_e32 v10, 2, v12
	v_mul_u32_u24_e32 v13, 0x204, v22
	v_add3_u32 v22, 0, v10, v13
	v_and_b32_e32 v10, 0x70, v1
	v_mul_lo_u32 v12, v23, s36
	s_mul_i32 s45, s45, 0x2c000
	v_lshlrev_b32_e32 v1, 2, v10
	s_mul_hi_i32 s12, s12, 0xb00
	s_add_u32 s13, s43, s45
	v_add3_u32 v1, 0, v12, v1
	v_add_u32_e32 v24, 0x400, v22
	s_addc_u32 s12, s44, s12
	s_lshl_b64 s[10:11], s[10:11], 1
	s_barrier
	s_add_u32 s10, s13, s10
	s_addc_u32 s11, s12, s11
	v_mov_b64_e32 v[12:13], s[10:11]
	v_mad_i64_i32 v[12:13], s[10:11], v23, s38, v[12:13]
	s_mov_b64 s[10:11], 0
	s_waitcnt vmcnt(2)
	ds_write2_b32 v22, v2, v6 offset1:32
	ds_write2_b32 v22, v3, v7 offset0:129 offset1:161
	ds_write2_b32 v24, v4, v8 offset0:2 offset1:34
	ds_write2_b32 v24, v5, v9 offset0:131 offset1:163
	s_waitcnt vmcnt(0)
	ds_write2_b32 v22, v14, v18 offset0:64 offset1:96
	ds_write2_b32 v22, v15, v19 offset0:193 offset1:225
	ds_write2_b32 v24, v16, v20 offset0:66 offset1:98
	ds_write2_b32 v24, v17, v21 offset0:195 offset1:227
	s_waitcnt lgkmcnt(0)
	s_barrier
	ds_read2_b32 v[2:3], v1 offset1:1
	ds_read2_b32 v[4:5], v1 offset0:2 offset1:3
	ds_read2_b32 v[6:7], v1 offset0:4 offset1:5
	ds_read2_b32 v[8:9], v1 offset0:6 offset1:7
	ds_read2_b32 v[14:15], v1 offset0:8 offset1:9
	ds_read2_b32 v[16:17], v1 offset0:10 offset1:11
	ds_read2_b32 v[18:19], v1 offset0:12 offset1:13
	ds_read2_b32 v[20:21], v1 offset0:14 offset1:15
	s_waitcnt lgkmcnt(7)
	v_cvt_pk_bf16_f32 v2, v2, v3
	s_waitcnt lgkmcnt(6)
	v_cvt_pk_bf16_f32 v3, v4, v5
	s_waitcnt lgkmcnt(5)
	v_cvt_pk_bf16_f32 v4, v6, v7
	s_waitcnt lgkmcnt(4)
	v_cvt_pk_bf16_f32 v5, v8, v9
	s_waitcnt lgkmcnt(3)
	v_cvt_pk_bf16_f32 v6, v14, v15
	s_waitcnt lgkmcnt(2)
	v_cvt_pk_bf16_f32 v7, v16, v17
	s_waitcnt lgkmcnt(1)
	v_cvt_pk_bf16_f32 v8, v18, v19
	s_waitcnt lgkmcnt(0)
	v_cvt_pk_bf16_f32 v9, v20, v21
.LBB0_257:
	s_andn2_b64 vcc, exec, s[10:11]
	s_cbranch_vccnz .LBB0_235
	s_mul_i32 s10, s26, 0xba2f
	s_lshr_b32 s10, s10, 25
	s_mul_i32 s11, s10, 0xfffffd40
	s_add_i32 s11, s11, s26
	s_mul_i32 s12, s11, 0xba3
	s_lshr_b32 s13, s12, 31
	s_ashr_i32 s12, s12, 20
	s_add_i32 s12, s12, s13
	s_sext_i32_i16 s13, s12
	s_mul_i32 s12, s13, 0xfffffea0
	s_add_i32 s27, s12, s11
	s_add_i32 s8, s8, s10
	s_addk_i32 s11, 0x15f
	s_cmpk_lt_u32 s11, 0x2bf
	s_cselect_b32 s11, s16, s18
	s_mul_i32 s8, s8, 0xb00000
	s_cselect_b32 s10, s17, s19
	s_add_u32 s11, s11, s8
	s_addc_u32 s40, s10, 0
	s_lshl_b32 s10, s27, 2
	s_lshl_b32 s27, s27, 3
	s_and_b32 s27, s27, 0xffffff00
	s_lshl_b32 s13, s13, 7
	s_and_b32 s12, s10, 0xffffffc0
	s_add_i32 s27, s27, s13
	s_and_b32 s10, s10, 64
	s_or_b32 s10, s27, s10
	s_add_u32 s8, s29, s8
	s_addc_u32 s27, s30, 0
	s_lshl_b32 s13, s26, 7
	s_and_b32 s26, s13, 0x780
	s_mul_i32 s13, s26, 0x1600
	s_add_u32 s11, s11, s13
	s_addc_u32 s40, s40, 0
	s_ashr_i32 s13, s12, 31
	v_mov_b32_e32 v1, v0
	s_lshl_b64 s[12:13], s[12:13], 2
	s_add_u32 s12, s11, s12
	v_lshlrev_b32_e32 v2, 2, v1
	v_and_b32_e32 v22, 60, v2
	s_addc_u32 s13, s40, s13
	v_ashrrev_i32_e32 v21, 4, v1
	v_lshlrev_b32_e32 v10, 2, v22
	v_lshl_add_u64 v[12:13], s[12:13], 0, v[10:11]
	v_add_u32_e32 v10, 64, v21
	v_add_u32_e32 v4, 32, v21
	v_mad_i64_i32 v[14:15], s[12:13], v10, s39, v[12:13]
	v_add_u32_e32 v10, 0x60, v21
	v_mad_i64_i32 v[2:3], s[12:13], v21, s39, v[12:13]
	v_mad_i64_i32 v[6:7], s[12:13], v4, s39, v[12:13]
	v_mad_i64_i32 v[16:17], s[12:13], v10, s39, v[12:13]
	global_load_dwordx4 v[2:5], v[2:3], off nt
	s_nop 0
	global_load_dwordx4 v[6:9], v[6:7], off nt
	s_nop 0
	global_load_dwordx4 v[12:15], v[14:15], off nt
	s_nop 0
	global_load_dwordx4 v[16:19], v[16:17], off nt
	v_ashrrev_i32_e32 v20, 3, v1
	v_lshlrev_b32_e32 v1, 4, v1
	v_lshlrev_b32_e32 v10, 2, v21
	v_mul_u32_u24_e32 v22, 0x204, v22
	v_add3_u32 v22, 0, v10, v22
	v_and_b32_e32 v10, 0x70, v1
	v_mul_lo_u32 v23, v20, s36
	s_ashr_i32 s11, s10, 31
	v_lshlrev_b32_e32 v1, 2, v10
	s_lshl_b64 s[10:11], s[10:11], 12
	v_add3_u32 v1, 0, v23, v1
	v_add_u32_e32 v24, 0x400, v22
	s_add_u32 s8, s8, s10
	s_barrier
	s_addc_u32 s11, s27, s11
	s_lshl_b32 s10, s26, 1
	v_ashrrev_i32_e32 v21, 31, v20
	s_add_u32 s10, s8, s10
	v_lshlrev_b64 v[20:21], 12, v[20:21]
	s_addc_u32 s11, s11, 0
	s_waitcnt vmcnt(2)
	ds_write2_b32 v22, v2, v6 offset1:32
	ds_write2_b32 v22, v3, v7 offset0:129 offset1:161
	ds_write2_b32 v24, v4, v8 offset0:2 offset1:34
	ds_write2_b32 v24, v5, v9 offset0:131 offset1:163
	s_waitcnt vmcnt(0)
	ds_write2_b32 v22, v12, v16 offset0:64 offset1:96
	ds_write2_b32 v22, v13, v17 offset0:193 offset1:225
	ds_write2_b32 v24, v14, v18 offset0:66 offset1:98
	ds_write2_b32 v24, v15, v19 offset0:195 offset1:227
	s_waitcnt lgkmcnt(0)
	s_barrier
	ds_read2_b32 v[2:3], v1 offset1:1
	ds_read2_b32 v[4:5], v1 offset0:2 offset1:3
	ds_read2_b32 v[6:7], v1 offset0:4 offset1:5
	ds_read2_b32 v[8:9], v1 offset0:6 offset1:7
	ds_read2_b32 v[12:13], v1 offset0:8 offset1:9
	ds_read2_b32 v[14:15], v1 offset0:10 offset1:11
	ds_read2_b32 v[16:17], v1 offset0:12 offset1:13
	ds_read2_b32 v[18:19], v1 offset0:14 offset1:15
	s_waitcnt lgkmcnt(7)
	v_cvt_pk_bf16_f32 v2, v2, v3
	s_waitcnt lgkmcnt(6)
	v_cvt_pk_bf16_f32 v3, v4, v5
	s_waitcnt lgkmcnt(5)
	v_cvt_pk_bf16_f32 v4, v6, v7
	s_waitcnt lgkmcnt(3)
	v_cvt_pk_bf16_f32 v6, v12, v13
	v_lshl_add_u64 v[12:13], s[10:11], 0, v[20:21]
	v_cvt_pk_bf16_f32 v5, v8, v9
	s_waitcnt lgkmcnt(2)
	v_cvt_pk_bf16_f32 v7, v14, v15
	s_waitcnt lgkmcnt(1)
	v_cvt_pk_bf16_f32 v8, v16, v17
	s_waitcnt lgkmcnt(0)
	v_cvt_pk_bf16_f32 v9, v18, v19
	s_branch .LBB0_235

.LBB0_390:
	s_or_b64 exec, exec, s[10:11]
	s_waitcnt lgkmcnt(0)
	s_barrier
	ds_read_b32 v1, v11 offset:40960
	s_mov_b64 s[10:11], -1
	s_waitcnt lgkmcnt(0)
	v_cmp_lt_u32_e32 vcc, s31, v1
	v_readfirstlane_b32 s26, v1
	s_cbranch_vccnz .LBB0_383
	s_cmpk_lt_u32 s26, 0x4a00
	s_cbranch_scc0 .LBB0_399
	s_cmpk_gt_u32 s26, 0x41ff
	s_cbranch_scc0 .LBB0_398
	s_cmpk_gt_u32 s26, 0x47ff
	s_cbranch_scc0 .LBB0_395
	s_add_i32 s8, s26, 0xffffb800
	s_lshr_b32 s24, s8, 4
	s_lshl_b32 s10, s24, 11
	s_lshl_b32 s8, s8, 7
	s_sub_i32 s10, s8, s10
	s_ashr_i32 s11, s10, 31
	s_lshl_b32 s8, s24, 6
	s_lshl_b64 s[24:25], s[10:11], 13
	s_add_u32 s27, s18, s24
	v_mov_b32_e32 v1, v0
	s_addc_u32 s40, s19, s25
	s_lshl_b64 s[24:25], s[8:9], 2
	s_add_u32 s24, s27, s24
	v_lshlrev_b32_e32 v2, 2, v1
	v_ashrrev_i32_e32 v12, 4, v1
	v_and_b32_e32 v24, 60, v2
	s_addc_u32 s25, s40, s25
	v_lshlrev_b32_e32 v10, 2, v24
	v_ashrrev_i32_e32 v13, 31, v12
	v_lshl_add_u64 v[2:3], s[24:25], 0, v[10:11]
	v_lshlrev_b64 v[4:5], 13, v[12:13]
	v_lshl_add_u64 v[14:15], v[2:3], 0, v[4:5]
	v_add_co_u32_e32 v6, vcc, s33, v14
	v_ashrrev_i32_e32 v22, 3, v1
	s_nop 0
	v_addc_co_u32_e32 v7, vcc, 0, v15, vcc
	v_add_co_u32_e32 v16, vcc, s34, v14
	global_load_dwordx4 v[2:5], v[14:15], off nt
	s_nop 0
	global_load_dwordx4 v[6:9], v[6:7], off nt
	v_addc_co_u32_e32 v17, vcc, 0, v15, vcc
	v_add_co_u32_e32 v18, vcc, s35, v14
	v_lshlrev_b32_e32 v1, 4, v1
	s_nop 0
	v_addc_co_u32_e32 v19, vcc, 0, v15, vcc
	global_load_dwordx4 v[14:17], v[16:17], off nt
	s_nop 0
	global_load_dwordx4 v[18:21], v[18:19], off nt
	v_lshlrev_b32_e32 v10, 2, v12
	v_ashrrev_i32_e32 v23, 31, v22
	v_mul_u32_u24_e32 v24, 0x204, v24
	v_mul_lo_u32 v25, v22, s36
	v_lshlrev_b64 v[12:13], 12, v[22:23]
	v_add3_u32 v22, 0, v10, v24
	v_and_b32_e32 v10, 0x70, v1
	v_lshlrev_b32_e32 v1, 2, v10
	v_add3_u32 v1, 0, v25, v1
	v_add_u32_e32 v23, 0x400, v22
	s_lshl_b64 s[24:25], s[8:9], 12
	s_barrier
	s_add_u32 s8, s0, s24
	s_addc_u32 s24, s1, s25
	s_lshl_b64 s[10:11], s[10:11], 1
	s_add_u32 s10, s8, s10
	s_addc_u32 s11, s24, s11
	v_lshl_add_u64 v[12:13], s[10:11], 0, v[12:13]
	s_mov_b64 s[10:11], 0
	s_waitcnt vmcnt(2)
	ds_write2_b32 v22, v2, v6 offset1:32
	ds_write2_b32 v22, v3, v7 offset0:129 offset1:161
	ds_write2_b32 v23, v4, v8 offset0:2 offset1:34
	ds_write2_b32 v23, v5, v9 offset0:131 offset1:163
	s_waitcnt vmcnt(0)
	ds_write2_b32 v22, v14, v18 offset0:64 offset1:96
	ds_write2_b32 v22, v15, v19 offset0:193 offset1:225
	ds_write2_b32 v23, v16, v20 offset0:66 offset1:98
	ds_write2_b32 v23, v17, v21 offset0:195 offset1:227
	s_waitcnt lgkmcnt(0)
	s_barrier
	ds_read2_b32 v[2:3], v1 offset1:1
	ds_read2_b32 v[4:5], v1 offset0:2 offset1:3
	ds_read2_b32 v[6:7], v1 offset0:4 offset1:5
	ds_read2_b32 v[8:9], v1 offset0:6 offset1:7
	ds_read2_b32 v[14:15], v1 offset0:8 offset1:9
	ds_read2_b32 v[16:17], v1 offset0:10 offset1:11
	ds_read2_b32 v[18:19], v1 offset0:12 offset1:13
	ds_read2_b32 v[20:21], v1 offset0:14 offset1:15
	s_waitcnt lgkmcnt(7)
	v_cvt_pk_bf16_f32 v2, v2, v3
	s_waitcnt lgkmcnt(6)
	v_cvt_pk_bf16_f32 v3, v4, v5
	s_waitcnt lgkmcnt(5)
	v_cvt_pk_bf16_f32 v4, v6, v7
	s_waitcnt lgkmcnt(4)
	v_cvt_pk_bf16_f32 v5, v8, v9
	s_waitcnt lgkmcnt(3)
	v_cvt_pk_bf16_f32 v6, v14, v15
	s_waitcnt lgkmcnt(2)
	v_cvt_pk_bf16_f32 v7, v16, v17
	s_waitcnt lgkmcnt(1)
	v_cvt_pk_bf16_f32 v8, v18, v19
	s_waitcnt lgkmcnt(0)
	v_cvt_pk_bf16_f32 v9, v20, v21
.LBB0_395:
	s_andn2_b64 vcc, exec, s[10:11]
	s_cbranch_vccnz .LBB0_397
	s_add_i32 s8, s26, 0xffffbe00
	s_lshr_b32 s24, s8, 4
	s_lshl_b32 s10, s24, 11
	s_lshl_b32 s8, s8, 7
	s_sub_i32 s10, s8, s10
	s_ashr_i32 s11, s10, 31
	s_lshl_b32 s8, s24, 6
	s_mul_i32 s25, s10, 0x6000
	s_mul_hi_i32 s24, s10, 0x6000
	s_add_u32 s27, s16, s25
	v_mov_b32_e32 v1, v0
	s_addc_u32 s40, s17, s24
	s_lshl_b64 s[24:25], s[8:9], 2
	s_add_u32 s24, s27, s24
	v_lshlrev_b32_e32 v2, 2, v1
	v_and_b32_e32 v22, 60, v2
	s_addc_u32 s25, s40, s25
	v_ashrrev_i32_e32 v21, 4, v1
	v_lshlrev_b32_e32 v10, 2, v22
	v_lshl_add_u64 v[12:13], s[24:25], 0, v[10:11]
	v_add_u32_e32 v10, 64, v21
	v_add_u32_e32 v4, 32, v21
	v_mad_i64_i32 v[14:15], s[24:25], v10, s37, v[12:13]
	v_add_u32_e32 v10, 0x60, v21
	v_mad_i64_i32 v[2:3], s[24:25], v21, s37, v[12:13]
	v_mad_i64_i32 v[6:7], s[24:25], v4, s37, v[12:13]
	v_mad_i64_i32 v[16:17], s[24:25], v10, s37, v[12:13]
	global_load_dwordx4 v[2:5], v[2:3], off nt
	s_nop 0
	global_load_dwordx4 v[6:9], v[6:7], off nt
	s_nop 0
	global_load_dwordx4 v[12:15], v[14:15], off nt
	s_nop 0
	global_load_dwordx4 v[16:19], v[16:17], off nt
	v_ashrrev_i32_e32 v20, 3, v1
	v_lshlrev_b32_e32 v1, 4, v1
	v_lshlrev_b32_e32 v10, 2, v21
	v_mul_u32_u24_e32 v22, 0x204, v22
	v_add3_u32 v22, 0, v10, v22
	v_and_b32_e32 v10, 0x70, v1
	v_mul_lo_u32 v23, v20, s36
	v_lshlrev_b32_e32 v1, 2, v10
	s_lshl_b64 s[24:25], s[8:9], 12
	v_add3_u32 v1, 0, v23, v1
	v_add_u32_e32 v24, 0x400, v22
	s_add_u32 s8, s3, s24
	s_barrier
	s_addc_u32 s24, s4, s25
	s_lshl_b64 s[10:11], s[10:11], 1
	v_ashrrev_i32_e32 v21, 31, v20
	s_add_u32 s10, s8, s10
	v_lshlrev_b64 v[20:21], 12, v[20:21]
	s_addc_u32 s11, s24, s11
	s_waitcnt vmcnt(2)
	ds_write2_b32 v22, v2, v6 offset1:32
	ds_write2_b32 v22, v3, v7 offset0:129 offset1:161
	ds_write2_b32 v24, v4, v8 offset0:2 offset1:34
	ds_write2_b32 v24, v5, v9 offset0:131 offset1:163
	s_waitcnt vmcnt(0)
	ds_write2_b32 v22, v12, v16 offset0:64 offset1:96
	ds_write2_b32 v22, v13, v17 offset0:193 offset1:225
	ds_write2_b32 v24, v14, v18 offset0:66 offset1:98
	ds_write2_b32 v24, v15, v19 offset0:195 offset1:227
	s_waitcnt lgkmcnt(0)
	s_barrier
	ds_read2_b32 v[2:3], v1 offset1:1
	ds_read2_b32 v[4:5], v1 offset0:2 offset1:3
	ds_read2_b32 v[6:7], v1 offset0:4 offset1:5
	ds_read2_b32 v[8:9], v1 offset0:6 offset1:7
	ds_read2_b32 v[12:13], v1 offset0:8 offset1:9
	ds_read2_b32 v[14:15], v1 offset0:10 offset1:11
	ds_read2_b32 v[16:17], v1 offset0:12 offset1:13
	ds_read2_b32 v[18:19], v1 offset0:14 offset1:15
	s_waitcnt lgkmcnt(7)
	v_cvt_pk_bf16_f32 v2, v2, v3
	s_waitcnt lgkmcnt(6)
	v_cvt_pk_bf16_f32 v3, v4, v5
	s_waitcnt lgkmcnt(5)
	v_cvt_pk_bf16_f32 v4, v6, v7
	s_waitcnt lgkmcnt(3)
	v_cvt_pk_bf16_f32 v6, v12, v13
	v_lshl_add_u64 v[12:13], s[10:11], 0, v[20:21]
	v_cvt_pk_bf16_f32 v5, v8, v9
	s_waitcnt lgkmcnt(2)
	v_cvt_pk_bf16_f32 v7, v14, v15
	s_waitcnt lgkmcnt(1)
	v_cvt_pk_bf16_f32 v8, v16, v17
	s_waitcnt lgkmcnt(0)
	v_cvt_pk_bf16_f32 v9, v18, v19

.LBB0_401:
	s_andn2_b64 vcc, exec, s[10:11]
	s_cbranch_vccnz .LBB0_382
	s_cmpk_gt_u32 s26, 0x2bff
	s_mov_b64 s[10:11], -1
	s_cbranch_scc0 .LBB0_404
	s_add_i32 s10, s26, 0xffffd400
	s_mul_i32 s11, s10, 0xba2f
	s_lshr_b32 s11, s11, 24
	s_mul_i32 s24, s11, 0xfffffea0
	s_add_i32 s11, s8, s11
	s_add_i32 s10, s24, s10
	s_mul_i32 s25, s11, 0xb00000
	s_mul_hi_u32 s24, s11, 0xb00000
	s_add_u32 s27, s20, s25
	s_addc_u32 s42, s21, s24
	s_mul_i32 s11, s11, 0x580000
	s_add_u32 s43, s5, s11
	s_mul_i32 s11, s10, 0x1746
	s_addc_u32 s44, s28, 0
	s_lshr_b32 s24, s11, 31
	s_lshr_b32 s11, s11, 16
	s_add_i32 s11, s11, s24
	s_sext_i32_i16 s45, s11
	s_mul_i32 s11, s45, -11
	s_add_i32 s11, s11, s10
	s_lshl_b32 s10, s11, 7
	s_ashr_i32 s11, s10, 31
	s_lshl_b32 s24, s45, 6
	s_ashr_i32 s25, s24, 31
	s_lshl_b64 s[40:41], s[10:11], 13
	s_add_u32 s27, s27, s40
	v_mov_b32_e32 v1, v0
	s_addc_u32 s42, s42, s41
	s_lshl_b64 s[40:41], s[24:25], 2
	s_add_u32 s40, s27, s40
	v_lshlrev_b32_e32 v2, 2, v1
	v_ashrrev_i32_e32 v12, 4, v1
	v_and_b32_e32 v22, 60, v2
	s_addc_u32 s41, s42, s41
	v_lshlrev_b32_e32 v10, 2, v22
	v_ashrrev_i32_e32 v13, 31, v12
	v_lshl_add_u64 v[2:3], s[40:41], 0, v[10:11]
	v_lshlrev_b64 v[4:5], 13, v[12:13]
	v_lshl_add_u64 v[14:15], v[2:3], 0, v[4:5]
	v_add_co_u32_e32 v6, vcc, s33, v14
	v_ashrrev_i32_e32 v23, 3, v1
	s_nop 0
	v_addc_co_u32_e32 v7, vcc, 0, v15, vcc
	v_add_co_u32_e32 v16, vcc, s34, v14
	global_load_dwordx4 v[2:5], v[14:15], off nt
	s_nop 0
	global_load_dwordx4 v[6:9], v[6:7], off nt
	v_addc_co_u32_e32 v17, vcc, 0, v15, vcc
	v_add_co_u32_e32 v18, vcc, s35, v14
	v_lshlrev_b32_e32 v1, 4, v1
	s_nop 0
	v_addc_co_u32_e32 v19, vcc, 0, v15, vcc
	global_load_dwordx4 v[14:17], v[16:17], off nt
	s_nop 0
	global_load_dwordx4 v[18:21], v[18:19], off nt
	v_lshlrev_b32_e32 v10, 2, v12
	v_mul_u32_u24_e32 v13, 0x204, v22
	v_add3_u32 v22, 0, v10, v13
	v_and_b32_e32 v10, 0x70, v1
	v_mul_lo_u32 v12, v23, s36
	s_mul_i32 s45, s45, 0x2c000
	v_lshlrev_b32_e32 v1, 2, v10
	s_mul_hi_i32 s24, s24, 0xb00
	s_add_u32 s25, s43, s45
	v_add3_u32 v1, 0, v12, v1
	v_add_u32_e32 v24, 0x400, v22
	s_addc_u32 s24, s44, s24
	s_lshl_b64 s[10:11], s[10:11], 1
	s_barrier
	s_add_u32 s10, s25, s10
	s_addc_u32 s11, s24, s11
	v_mov_b64_e32 v[12:13], s[10:11]
	v_mad_i64_i32 v[12:13], s[10:11], v23, s38, v[12:13]
	s_mov_b64 s[10:11], 0
	s_waitcnt vmcnt(2)
	ds_write2_b32 v22, v2, v6 offset1:32
	ds_write2_b32 v22, v3, v7 offset0:129 offset1:161
	ds_write2_b32 v24, v4, v8 offset0:2 offset1:34
	ds_write2_b32 v24, v5, v9 offset0:131 offset1:163
	s_waitcnt vmcnt(0)
	ds_write2_b32 v22, v14, v18 offset0:64 offset1:96
	ds_write2_b32 v22, v15, v19 offset0:193 offset1:225
	ds_write2_b32 v24, v16, v20 offset0:66 offset1:98
	ds_write2_b32 v24, v17, v21 offset0:195 offset1:227
	s_waitcnt lgkmcnt(0)
	s_barrier
	ds_read2_b32 v[2:3], v1 offset1:1
	ds_read2_b32 v[4:5], v1 offset0:2 offset1:3
	ds_read2_b32 v[6:7], v1 offset0:4 offset1:5
	ds_read2_b32 v[8:9], v1 offset0:6 offset1:7
	ds_read2_b32 v[14:15], v1 offset0:8 offset1:9
	ds_read2_b32 v[16:17], v1 offset0:10 offset1:11
	ds_read2_b32 v[18:19], v1 offset0:12 offset1:13
	ds_read2_b32 v[20:21], v1 offset0:14 offset1:15
	s_waitcnt lgkmcnt(7)
	v_cvt_pk_bf16_f32 v2, v2, v3
	s_waitcnt lgkmcnt(6)
	v_cvt_pk_bf16_f32 v3, v4, v5
	s_waitcnt lgkmcnt(5)
	v_cvt_pk_bf16_f32 v4, v6, v7
	s_waitcnt lgkmcnt(4)
	v_cvt_pk_bf16_f32 v5, v8, v9
	s_waitcnt lgkmcnt(3)
	v_cvt_pk_bf16_f32 v6, v14, v15
	s_waitcnt lgkmcnt(2)
	v_cvt_pk_bf16_f32 v7, v16, v17
	s_waitcnt lgkmcnt(1)
	v_cvt_pk_bf16_f32 v8, v18, v19
	s_waitcnt lgkmcnt(0)
	v_cvt_pk_bf16_f32 v9, v20, v21
.LBB0_404:
	s_andn2_b64 vcc, exec, s[10:11]
	s_cbranch_vccnz .LBB0_382
	s_mul_i32 s10, s26, 0xba2f
	s_lshr_b32 s10, s10, 25
	s_mul_i32 s11, s10, 0xfffffd40
	s_add_i32 s11, s11, s26
	s_mul_i32 s24, s11, 0xba3
	s_lshr_b32 s25, s24, 31
	s_ashr_i32 s24, s24, 20
	s_add_i32 s24, s24, s25
	s_sext_i32_i16 s25, s24
	s_mul_i32 s24, s25, 0xfffffea0
	s_add_i32 s27, s24, s11
	s_add_i32 s8, s8, s10
	s_addk_i32 s11, 0x15f
	s_cmpk_lt_u32 s11, 0x2bf
	s_cselect_b32 s11, s12, s14
	s_mul_i32 s8, s8, 0xb00000
	s_cselect_b32 s10, s13, s15
	s_add_u32 s11, s11, s8
	s_addc_u32 s40, s10, 0
	s_lshl_b32 s10, s27, 2
	s_lshl_b32 s27, s27, 3
	s_and_b32 s27, s27, 0xffffff00
	s_lshl_b32 s25, s25, 7
	s_and_b32 s24, s10, 0xffffffc0
	s_add_i32 s27, s27, s25
	s_and_b32 s10, s10, 64
	s_or_b32 s10, s27, s10
	s_add_u32 s8, s29, s8
	s_addc_u32 s27, s30, 0
	s_lshl_b32 s25, s26, 7
	s_and_b32 s26, s25, 0x780
	s_mul_i32 s25, s26, 0x1600
	s_add_u32 s11, s11, s25
	s_addc_u32 s40, s40, 0
	s_ashr_i32 s25, s24, 31
	v_mov_b32_e32 v1, v0
	s_lshl_b64 s[24:25], s[24:25], 2
	s_add_u32 s24, s11, s24
	v_lshlrev_b32_e32 v2, 2, v1
	v_and_b32_e32 v22, 60, v2
	s_addc_u32 s25, s40, s25
	v_ashrrev_i32_e32 v21, 4, v1
	v_lshlrev_b32_e32 v10, 2, v22
	v_lshl_add_u64 v[12:13], s[24:25], 0, v[10:11]
	v_add_u32_e32 v10, 64, v21
	v_add_u32_e32 v4, 32, v21
	v_mad_i64_i32 v[14:15], s[24:25], v10, s39, v[12:13]
	v_add_u32_e32 v10, 0x60, v21
	v_mad_i64_i32 v[2:3], s[24:25], v21, s39, v[12:13]
	v_mad_i64_i32 v[6:7], s[24:25], v4, s39, v[12:13]
	v_mad_i64_i32 v[16:17], s[24:25], v10, s39, v[12:13]
	global_load_dwordx4 v[2:5], v[2:3], off nt
	s_nop 0
	global_load_dwordx4 v[6:9], v[6:7], off nt
	s_nop 0
	global_load_dwordx4 v[12:15], v[14:15], off nt
	s_nop 0
	global_load_dwordx4 v[16:19], v[16:17], off nt
	v_ashrrev_i32_e32 v20, 3, v1
	v_lshlrev_b32_e32 v1, 4, v1
	v_lshlrev_b32_e32 v10, 2, v21
	v_mul_u32_u24_e32 v22, 0x204, v22
	v_add3_u32 v22, 0, v10, v22
	v_and_b32_e32 v10, 0x70, v1
	v_mul_lo_u32 v23, v20, s36
	s_ashr_i32 s11, s10, 31
	v_lshlrev_b32_e32 v1, 2, v10
	s_lshl_b64 s[10:11], s[10:11], 12
	v_add3_u32 v1, 0, v23, v1
	v_add_u32_e32 v24, 0x400, v22
	s_add_u32 s8, s8, s10
	s_barrier
	s_addc_u32 s11, s27, s11
	s_lshl_b32 s10, s26, 1
	v_ashrrev_i32_e32 v21, 31, v20
	s_add_u32 s10, s8, s10
	v_lshlrev_b64 v[20:21], 12, v[20:21]
	s_addc_u32 s11, s11, 0
	s_waitcnt vmcnt(2)
	ds_write2_b32 v22, v2, v6 offset1:32
	ds_write2_b32 v22, v3, v7 offset0:129 offset1:161
	ds_write2_b32 v24, v4, v8 offset0:2 offset1:34
	ds_write2_b32 v24, v5, v9 offset0:131 offset1:163
	s_waitcnt vmcnt(0)
	ds_write2_b32 v22, v12, v16 offset0:64 offset1:96
	ds_write2_b32 v22, v13, v17 offset0:193 offset1:225
	ds_write2_b32 v24, v14, v18 offset0:66 offset1:98
	ds_write2_b32 v24, v15, v19 offset0:195 offset1:227
	s_waitcnt lgkmcnt(0)
	s_barrier
	ds_read2_b32 v[2:3], v1 offset1:1
	ds_read2_b32 v[4:5], v1 offset0:2 offset1:3
	ds_read2_b32 v[6:7], v1 offset0:4 offset1:5
	ds_read2_b32 v[8:9], v1 offset0:6 offset1:7
	ds_read2_b32 v[12:13], v1 offset0:8 offset1:9
	ds_read2_b32 v[14:15], v1 offset0:10 offset1:11
	ds_read2_b32 v[16:17], v1 offset0:12 offset1:13
	ds_read2_b32 v[18:19], v1 offset0:14 offset1:15
	s_waitcnt lgkmcnt(7)
	v_cvt_pk_bf16_f32 v2, v2, v3
	s_waitcnt lgkmcnt(6)
	v_cvt_pk_bf16_f32 v3, v4, v5
	s_waitcnt lgkmcnt(5)
	v_cvt_pk_bf16_f32 v4, v6, v7
	s_waitcnt lgkmcnt(3)
	v_cvt_pk_bf16_f32 v6, v12, v13
	v_lshl_add_u64 v[12:13], s[10:11], 0, v[20:21]
	v_cvt_pk_bf16_f32 v5, v8, v9
	s_waitcnt lgkmcnt(2)
	v_cvt_pk_bf16_f32 v7, v14, v15
	s_waitcnt lgkmcnt(1)
	v_cvt_pk_bf16_f32 v8, v16, v17
	s_waitcnt lgkmcnt(0)
	v_cvt_pk_bf16_f32 v9, v18, v19
	s_branch .LBB0_382

.LBB0_617:
	s_or_b64 exec, exec, s[10:11]
	s_waitcnt lgkmcnt(0)
	s_barrier
	ds_read_b32 v1, v11 offset:40960
	s_mov_b64 s[10:11], -1
	s_waitcnt lgkmcnt(0)
	v_cmp_lt_u32_e32 vcc, s19, v1
	v_readfirstlane_b32 s14, v1
	s_cbranch_vccnz .LBB0_610
	s_cmpk_lt_u32 s14, 0x4a00
	s_cbranch_scc0 .LBB0_626
	s_cmpk_gt_u32 s14, 0x41ff
	s_cbranch_scc0 .LBB0_625
	s_cmpk_gt_u32 s14, 0x47ff
	s_cbranch_scc0 .LBB0_622
	s_add_i32 s8, s14, 0xffffb800
	s_lshr_b32 s12, s8, 4
	s_lshl_b32 s10, s12, 11
	s_lshl_b32 s8, s8, 7
	s_sub_i32 s10, s8, s10
	s_ashr_i32 s11, s10, 31
	s_lshl_b32 s8, s12, 6
	s_lshl_b64 s[12:13], s[10:11], 13
	s_add_u32 s15, s42, s12
	v_mov_b32_e32 v1, v0
	s_addc_u32 s34, s43, s13
	s_lshl_b64 s[12:13], s[8:9], 2
	s_add_u32 s12, s15, s12
	v_lshlrev_b32_e32 v2, 2, v1
	v_ashrrev_i32_e32 v12, 4, v1
	v_and_b32_e32 v24, 60, v2
	s_addc_u32 s13, s34, s13
	v_lshlrev_b32_e32 v10, 2, v24
	v_ashrrev_i32_e32 v13, 31, v12
	v_lshl_add_u64 v[2:3], s[12:13], 0, v[10:11]
	v_lshlrev_b64 v[4:5], 13, v[12:13]
	v_lshl_add_u64 v[14:15], v[2:3], 0, v[4:5]
	v_add_co_u32_e32 v6, vcc, s20, v14
	v_ashrrev_i32_e32 v22, 3, v1
	s_nop 0
	v_addc_co_u32_e32 v7, vcc, 0, v15, vcc
	v_add_co_u32_e32 v16, vcc, s21, v14
	global_load_dwordx4 v[2:5], v[14:15], off nt
	s_nop 0
	global_load_dwordx4 v[6:9], v[6:7], off nt
	v_addc_co_u32_e32 v17, vcc, 0, v15, vcc
	v_add_co_u32_e32 v18, vcc, s22, v14
	v_lshlrev_b32_e32 v1, 4, v1
	s_nop 0
	v_addc_co_u32_e32 v19, vcc, 0, v15, vcc
	global_load_dwordx4 v[14:17], v[16:17], off nt
	s_nop 0
	global_load_dwordx4 v[18:21], v[18:19], off nt
	v_lshlrev_b32_e32 v10, 2, v12
	v_ashrrev_i32_e32 v23, 31, v22
	v_mul_u32_u24_e32 v24, 0x204, v24
	v_mul_lo_u32 v25, v22, s23
	v_lshlrev_b64 v[12:13], 12, v[22:23]
	v_add3_u32 v22, 0, v10, v24
	v_and_b32_e32 v10, 0x70, v1
	v_lshlrev_b32_e32 v1, 2, v10
	v_add3_u32 v1, 0, v25, v1
	v_add_u32_e32 v23, 0x400, v22
	s_lshl_b64 s[12:13], s[8:9], 12
	s_waitcnt vmcnt(63) expcnt(7) lgkmcnt(15)
	s_barrier
	s_add_u32 s8, s0, s12
	s_addc_u32 s12, s1, s13
	s_lshl_b64 s[10:11], s[10:11], 1
	s_add_u32 s10, s8, s10
	s_addc_u32 s11, s12, s11
	v_lshl_add_u64 v[12:13], s[10:11], 0, v[12:13]
	s_mov_b64 s[10:11], 0
	s_waitcnt vmcnt(2)
	ds_write2_b32 v22, v2, v6 offset1:32
	ds_write2_b32 v22, v3, v7 offset0:129 offset1:161
	ds_write2_b32 v23, v4, v8 offset0:2 offset1:34
	ds_write2_b32 v23, v5, v9 offset0:131 offset1:163
	s_waitcnt vmcnt(0)
	ds_write2_b32 v22, v14, v18 offset0:64 offset1:96
	ds_write2_b32 v22, v15, v19 offset0:193 offset1:225
	ds_write2_b32 v23, v16, v20 offset0:66 offset1:98
	ds_write2_b32 v23, v17, v21 offset0:195 offset1:227
	s_waitcnt lgkmcnt(0)
	s_barrier
	ds_read2_b32 v[2:3], v1 offset1:1
	ds_read2_b32 v[4:5], v1 offset0:2 offset1:3
	ds_read2_b32 v[6:7], v1 offset0:4 offset1:5
	ds_read2_b32 v[8:9], v1 offset0:6 offset1:7
	ds_read2_b32 v[14:15], v1 offset0:8 offset1:9
	ds_read2_b32 v[16:17], v1 offset0:10 offset1:11
	ds_read2_b32 v[18:19], v1 offset0:12 offset1:13
	ds_read2_b32 v[20:21], v1 offset0:14 offset1:15
	s_waitcnt lgkmcnt(7)
	v_cvt_pk_bf16_f32 v2, v2, v3
	s_waitcnt lgkmcnt(6)
	v_cvt_pk_bf16_f32 v3, v4, v5
	s_waitcnt lgkmcnt(5)
	v_cvt_pk_bf16_f32 v4, v6, v7
	s_waitcnt lgkmcnt(4)
	v_cvt_pk_bf16_f32 v5, v8, v9
	s_waitcnt lgkmcnt(3)
	v_cvt_pk_bf16_f32 v6, v14, v15
	s_waitcnt lgkmcnt(2)
	v_cvt_pk_bf16_f32 v7, v16, v17
	s_waitcnt lgkmcnt(1)
	v_cvt_pk_bf16_f32 v8, v18, v19
	s_waitcnt lgkmcnt(0)
	v_cvt_pk_bf16_f32 v9, v20, v21
.LBB0_622:
	s_andn2_b64 vcc, exec, s[10:11]
	s_cbranch_vccnz .LBB0_624
	s_add_i32 s8, s14, 0xffffbe00
	s_lshr_b32 s12, s8, 4
	s_lshl_b32 s10, s12, 11
	s_lshl_b32 s8, s8, 7
	s_sub_i32 s10, s8, s10
	s_ashr_i32 s11, s10, 31
	s_lshl_b32 s8, s12, 6
	s_mul_i32 s13, s10, 0x6000
	s_mul_hi_i32 s12, s10, 0x6000
	s_add_u32 s15, s62, s13
	v_mov_b32_e32 v1, v0
	s_addc_u32 s34, s63, s12
	s_lshl_b64 s[12:13], s[8:9], 2
	s_add_u32 s12, s15, s12
	v_lshlrev_b32_e32 v2, 2, v1
	v_and_b32_e32 v22, 60, v2
	s_addc_u32 s13, s34, s13
	v_ashrrev_i32_e32 v21, 4, v1
	v_lshlrev_b32_e32 v10, 2, v22
	v_lshl_add_u64 v[12:13], s[12:13], 0, v[10:11]
	v_add_u32_e32 v10, 64, v21
	v_add_u32_e32 v4, 32, v21
	v_mad_i64_i32 v[14:15], s[12:13], v10, s30, v[12:13]
	v_add_u32_e32 v10, 0x60, v21
	v_mad_i64_i32 v[2:3], s[12:13], v21, s30, v[12:13]
	v_mad_i64_i32 v[6:7], s[12:13], v4, s30, v[12:13]
	v_mad_i64_i32 v[16:17], s[12:13], v10, s30, v[12:13]
	global_load_dwordx4 v[2:5], v[2:3], off nt
	s_nop 0
	global_load_dwordx4 v[6:9], v[6:7], off nt
	s_nop 0
	global_load_dwordx4 v[12:15], v[14:15], off nt
	s_nop 0
	global_load_dwordx4 v[16:19], v[16:17], off nt
	v_ashrrev_i32_e32 v20, 3, v1
	v_lshlrev_b32_e32 v1, 4, v1
	v_lshlrev_b32_e32 v10, 2, v21
	v_mul_u32_u24_e32 v22, 0x204, v22
	v_add3_u32 v22, 0, v10, v22
	v_and_b32_e32 v10, 0x70, v1
	v_mul_lo_u32 v23, v20, s23
	v_lshlrev_b32_e32 v1, 2, v10
	s_lshl_b64 s[12:13], s[8:9], 12
	v_add3_u32 v1, 0, v23, v1
	v_add_u32_e32 v24, 0x400, v22
	s_add_u32 s8, s3, s12
	s_waitcnt vmcnt(63) expcnt(7) lgkmcnt(15)
	s_barrier
	s_addc_u32 s12, s4, s13
	s_lshl_b64 s[10:11], s[10:11], 1
	v_ashrrev_i32_e32 v21, 31, v20
	s_add_u32 s10, s8, s10
	v_lshlrev_b64 v[20:21], 12, v[20:21]
	s_addc_u32 s11, s12, s11
	s_waitcnt vmcnt(2)
	ds_write2_b32 v22, v2, v6 offset1:32
	ds_write2_b32 v22, v3, v7 offset0:129 offset1:161
	ds_write2_b32 v24, v4, v8 offset0:2 offset1:34
	ds_write2_b32 v24, v5, v9 offset0:131 offset1:163
	s_waitcnt vmcnt(0)
	ds_write2_b32 v22, v12, v16 offset0:64 offset1:96
	ds_write2_b32 v22, v13, v17 offset0:193 offset1:225
	ds_write2_b32 v24, v14, v18 offset0:66 offset1:98
	ds_write2_b32 v24, v15, v19 offset0:195 offset1:227
	s_waitcnt lgkmcnt(0)
	s_barrier
	ds_read2_b32 v[2:3], v1 offset1:1
	ds_read2_b32 v[4:5], v1 offset0:2 offset1:3
	ds_read2_b32 v[6:7], v1 offset0:4 offset1:5
	ds_read2_b32 v[8:9], v1 offset0:6 offset1:7
	ds_read2_b32 v[12:13], v1 offset0:8 offset1:9
	ds_read2_b32 v[14:15], v1 offset0:10 offset1:11
	ds_read2_b32 v[16:17], v1 offset0:12 offset1:13
	ds_read2_b32 v[18:19], v1 offset0:14 offset1:15
	s_waitcnt lgkmcnt(7)
	v_cvt_pk_bf16_f32 v2, v2, v3
	s_waitcnt lgkmcnt(6)
	v_cvt_pk_bf16_f32 v3, v4, v5
	s_waitcnt lgkmcnt(5)
	v_cvt_pk_bf16_f32 v4, v6, v7
	s_waitcnt lgkmcnt(3)
	v_cvt_pk_bf16_f32 v6, v12, v13
	v_lshl_add_u64 v[12:13], s[10:11], 0, v[20:21]
	v_cvt_pk_bf16_f32 v5, v8, v9
	s_waitcnt lgkmcnt(2)
	v_cvt_pk_bf16_f32 v7, v14, v15
	s_waitcnt lgkmcnt(1)
	v_cvt_pk_bf16_f32 v8, v16, v17
	s_waitcnt lgkmcnt(0)
	v_cvt_pk_bf16_f32 v9, v18, v19

.LBB0_628:
	s_andn2_b64 vcc, exec, s[10:11]
	s_cbranch_vccnz .LBB0_609
	s_cmpk_gt_u32 s14, 0x2bff
	s_mov_b64 s[10:11], -1
	s_cbranch_scc0 .LBB0_631
	s_add_i32 s10, s14, 0xffffd400
	s_mul_i32 s11, s10, 0xba2f
	s_lshr_b32 s11, s11, 24
	s_mul_i32 s12, s11, 0xfffffea0
	s_add_i32 s11, s8, s11
	s_add_i32 s10, s12, s10
	s_mul_i32 s13, s11, 0xb00000
	s_mul_hi_u32 s12, s11, 0xb00000
	s_add_u32 s15, s36, s13
	s_addc_u32 s38, s37, s12
	s_mul_i32 s11, s11, 0x580000
	s_add_u32 s39, s5, s11
	s_mul_i32 s11, s10, 0x1746
	s_addc_u32 s40, s16, 0
	s_lshr_b32 s12, s11, 31
	s_lshr_b32 s11, s11, 16
	s_add_i32 s11, s11, s12
	s_sext_i32_i16 s41, s11
	s_mul_i32 s11, s41, -11
	s_add_i32 s11, s11, s10
	s_lshl_b32 s10, s11, 7
	s_ashr_i32 s11, s10, 31
	s_lshl_b32 s12, s41, 6
	s_ashr_i32 s13, s12, 31
	s_lshl_b64 s[34:35], s[10:11], 13
	s_add_u32 s15, s15, s34
	v_mov_b32_e32 v1, v0
	s_addc_u32 s38, s38, s35
	s_lshl_b64 s[34:35], s[12:13], 2
	s_add_u32 s34, s15, s34
	v_lshlrev_b32_e32 v2, 2, v1
	v_ashrrev_i32_e32 v12, 4, v1
	v_and_b32_e32 v22, 60, v2
	s_addc_u32 s35, s38, s35
	v_lshlrev_b32_e32 v10, 2, v22
	v_ashrrev_i32_e32 v13, 31, v12
	v_lshl_add_u64 v[2:3], s[34:35], 0, v[10:11]
	v_lshlrev_b64 v[4:5], 13, v[12:13]
	v_lshl_add_u64 v[14:15], v[2:3], 0, v[4:5]
	v_add_co_u32_e32 v6, vcc, s20, v14
	v_ashrrev_i32_e32 v23, 3, v1
	s_nop 0
	v_addc_co_u32_e32 v7, vcc, 0, v15, vcc
	v_add_co_u32_e32 v16, vcc, s21, v14
	global_load_dwordx4 v[2:5], v[14:15], off nt
	s_nop 0
	global_load_dwordx4 v[6:9], v[6:7], off nt
	v_addc_co_u32_e32 v17, vcc, 0, v15, vcc
	v_add_co_u32_e32 v18, vcc, s22, v14
	v_lshlrev_b32_e32 v1, 4, v1
	s_nop 0
	v_addc_co_u32_e32 v19, vcc, 0, v15, vcc
	global_load_dwordx4 v[14:17], v[16:17], off nt
	s_nop 0
	global_load_dwordx4 v[18:21], v[18:19], off nt
	v_lshlrev_b32_e32 v10, 2, v12
	v_mul_u32_u24_e32 v13, 0x204, v22
	v_add3_u32 v22, 0, v10, v13
	v_and_b32_e32 v10, 0x70, v1
	v_mul_lo_u32 v12, v23, s23
	s_mul_i32 s41, s41, 0x2c000
	v_lshlrev_b32_e32 v1, 2, v10
	s_mul_hi_i32 s12, s12, 0xb00
	s_add_u32 s13, s39, s41
	v_add3_u32 v1, 0, v12, v1
	v_add_u32_e32 v24, 0x400, v22
	s_addc_u32 s12, s40, s12
	s_lshl_b64 s[10:11], s[10:11], 1
	s_waitcnt vmcnt(63) expcnt(7) lgkmcnt(15)
	s_barrier
	s_add_u32 s10, s13, s10
	s_addc_u32 s11, s12, s11
	v_mov_b64_e32 v[12:13], s[10:11]
	v_mad_i64_i32 v[12:13], s[10:11], v23, s31, v[12:13]
	s_mov_b64 s[10:11], 0
	s_waitcnt vmcnt(2)
	ds_write2_b32 v22, v2, v6 offset1:32
	ds_write2_b32 v22, v3, v7 offset0:129 offset1:161
	ds_write2_b32 v24, v4, v8 offset0:2 offset1:34
	ds_write2_b32 v24, v5, v9 offset0:131 offset1:163
	s_waitcnt vmcnt(0)
	ds_write2_b32 v22, v14, v18 offset0:64 offset1:96
	ds_write2_b32 v22, v15, v19 offset0:193 offset1:225
	ds_write2_b32 v24, v16, v20 offset0:66 offset1:98
	ds_write2_b32 v24, v17, v21 offset0:195 offset1:227
	s_waitcnt lgkmcnt(0)
	s_barrier
	ds_read2_b32 v[2:3], v1 offset1:1
	ds_read2_b32 v[4:5], v1 offset0:2 offset1:3
	ds_read2_b32 v[6:7], v1 offset0:4 offset1:5
	ds_read2_b32 v[8:9], v1 offset0:6 offset1:7
	ds_read2_b32 v[14:15], v1 offset0:8 offset1:9
	ds_read2_b32 v[16:17], v1 offset0:10 offset1:11
	ds_read2_b32 v[18:19], v1 offset0:12 offset1:13
	ds_read2_b32 v[20:21], v1 offset0:14 offset1:15
	s_waitcnt lgkmcnt(7)
	v_cvt_pk_bf16_f32 v2, v2, v3
	s_waitcnt lgkmcnt(6)
	v_cvt_pk_bf16_f32 v3, v4, v5
	s_waitcnt lgkmcnt(5)
	v_cvt_pk_bf16_f32 v4, v6, v7
	s_waitcnt lgkmcnt(4)
	v_cvt_pk_bf16_f32 v5, v8, v9
	s_waitcnt lgkmcnt(3)
	v_cvt_pk_bf16_f32 v6, v14, v15
	s_waitcnt lgkmcnt(2)
	v_cvt_pk_bf16_f32 v7, v16, v17
	s_waitcnt lgkmcnt(1)
	v_cvt_pk_bf16_f32 v8, v18, v19
	s_waitcnt lgkmcnt(0)
	v_cvt_pk_bf16_f32 v9, v20, v21
.LBB0_631:
	s_andn2_b64 vcc, exec, s[10:11]
	s_cbranch_vccnz .LBB0_609
	s_mul_i32 s10, s14, 0xba2f
	s_lshr_b32 s10, s10, 25
	s_mul_i32 s11, s10, 0xfffffd40
	s_add_i32 s11, s11, s14
	s_mul_i32 s12, s11, 0xba3
	s_lshr_b32 s13, s12, 31
	s_ashr_i32 s12, s12, 20
	s_add_i32 s12, s12, s13
	s_sext_i32_i16 s13, s12
	s_mul_i32 s12, s13, 0xfffffea0
	s_add_i32 s15, s12, s11
	s_add_i32 s8, s8, s10
	s_addk_i32 s11, 0x15f
	s_cmpk_lt_u32 s11, 0x2bf
	s_cselect_b32 s11, s24, s26
	s_mul_i32 s8, s8, 0xb00000
	s_cselect_b32 s10, s25, s27
	s_add_u32 s11, s11, s8
	s_addc_u32 s34, s10, 0
	s_lshl_b32 s10, s15, 2
	s_lshl_b32 s15, s15, 3
	s_and_b32 s15, s15, 0xffffff00
	s_lshl_b32 s13, s13, 7
	s_and_b32 s12, s10, 0xffffffc0
	s_add_i32 s15, s15, s13
	s_and_b32 s10, s10, 64
	s_or_b32 s10, s15, s10
	s_add_u32 s8, s17, s8
	s_addc_u32 s15, s18, 0
	s_lshl_b32 s13, s14, 7
	s_and_b32 s14, s13, 0x780
	s_mul_i32 s13, s14, 0x1600
	s_add_u32 s11, s11, s13
	s_addc_u32 s34, s34, 0
	s_ashr_i32 s13, s12, 31
	v_mov_b32_e32 v1, v0
	s_lshl_b64 s[12:13], s[12:13], 2
	s_add_u32 s12, s11, s12
	v_lshlrev_b32_e32 v2, 2, v1
	v_and_b32_e32 v22, 60, v2
	s_addc_u32 s13, s34, s13
	v_ashrrev_i32_e32 v21, 4, v1
	v_lshlrev_b32_e32 v10, 2, v22
	v_lshl_add_u64 v[12:13], s[12:13], 0, v[10:11]
	v_add_u32_e32 v10, 64, v21
	v_add_u32_e32 v4, 32, v21
	v_mad_i64_i32 v[14:15], s[12:13], v10, s33, v[12:13]
	v_add_u32_e32 v10, 0x60, v21
	v_mad_i64_i32 v[2:3], s[12:13], v21, s33, v[12:13]
	v_mad_i64_i32 v[6:7], s[12:13], v4, s33, v[12:13]
	v_mad_i64_i32 v[16:17], s[12:13], v10, s33, v[12:13]
	global_load_dwordx4 v[2:5], v[2:3], off nt
	s_nop 0
	global_load_dwordx4 v[6:9], v[6:7], off nt
	s_nop 0
	global_load_dwordx4 v[12:15], v[14:15], off nt
	s_nop 0
	global_load_dwordx4 v[16:19], v[16:17], off nt
	v_ashrrev_i32_e32 v20, 3, v1
	v_lshlrev_b32_e32 v1, 4, v1
	v_lshlrev_b32_e32 v10, 2, v21
	v_mul_u32_u24_e32 v22, 0x204, v22
	v_add3_u32 v22, 0, v10, v22
	v_and_b32_e32 v10, 0x70, v1
	v_mul_lo_u32 v23, v20, s23
	s_ashr_i32 s11, s10, 31
	v_lshlrev_b32_e32 v1, 2, v10
	s_lshl_b64 s[10:11], s[10:11], 12
	v_add3_u32 v1, 0, v23, v1
	v_add_u32_e32 v24, 0x400, v22
	s_add_u32 s8, s8, s10
	s_waitcnt vmcnt(63) expcnt(7) lgkmcnt(15)
	s_barrier
	s_addc_u32 s11, s15, s11
	s_lshl_b32 s10, s14, 1
	v_ashrrev_i32_e32 v21, 31, v20
	s_add_u32 s10, s8, s10
	v_lshlrev_b64 v[20:21], 12, v[20:21]
	s_addc_u32 s11, s11, 0
	s_waitcnt vmcnt(2)
	ds_write2_b32 v22, v2, v6 offset1:32
	ds_write2_b32 v22, v3, v7 offset0:129 offset1:161
	ds_write2_b32 v24, v4, v8 offset0:2 offset1:34
	ds_write2_b32 v24, v5, v9 offset0:131 offset1:163
	s_waitcnt vmcnt(0)
	ds_write2_b32 v22, v12, v16 offset0:64 offset1:96
	ds_write2_b32 v22, v13, v17 offset0:193 offset1:225
	ds_write2_b32 v24, v14, v18 offset0:66 offset1:98
	ds_write2_b32 v24, v15, v19 offset0:195 offset1:227
	s_waitcnt lgkmcnt(0)
	s_barrier
	ds_read2_b32 v[2:3], v1 offset1:1
	ds_read2_b32 v[4:5], v1 offset0:2 offset1:3
	ds_read2_b32 v[6:7], v1 offset0:4 offset1:5
	ds_read2_b32 v[8:9], v1 offset0:6 offset1:7
	ds_read2_b32 v[12:13], v1 offset0:8 offset1:9
	ds_read2_b32 v[14:15], v1 offset0:10 offset1:11
	ds_read2_b32 v[16:17], v1 offset0:12 offset1:13
	ds_read2_b32 v[18:19], v1 offset0:14 offset1:15
	s_waitcnt lgkmcnt(7)
	v_cvt_pk_bf16_f32 v2, v2, v3
	s_waitcnt lgkmcnt(6)
	v_cvt_pk_bf16_f32 v3, v4, v5
	s_waitcnt lgkmcnt(5)
	v_cvt_pk_bf16_f32 v4, v6, v7
	s_waitcnt lgkmcnt(3)
	v_cvt_pk_bf16_f32 v6, v12, v13
	v_lshl_add_u64 v[12:13], s[10:11], 0, v[20:21]
	v_cvt_pk_bf16_f32 v5, v8, v9
	s_waitcnt lgkmcnt(2)
	v_cvt_pk_bf16_f32 v7, v14, v15
	s_waitcnt lgkmcnt(1)
	v_cvt_pk_bf16_f32 v8, v16, v17
	s_waitcnt lgkmcnt(0)
	v_cvt_pk_bf16_f32 v9, v18, v19
	s_branch .LBB0_609

.LBB0_722:
	s_or_b64 exec, exec, s[22:23]
	s_waitcnt lgkmcnt(0)
	s_barrier
	ds_read_b32 v1, v11 offset:40960
	s_mov_b64 s[22:23], -1
	s_waitcnt lgkmcnt(0)
	v_cmp_lt_u32_e32 vcc, s31, v1
	v_readfirstlane_b32 s26, v1
	s_cbranch_vccnz .LBB0_715
	s_cmpk_lt_u32 s26, 0x4a00
	s_cbranch_scc0 .LBB0_731
	s_cmpk_gt_u32 s26, 0x41ff
	s_cbranch_scc0 .LBB0_730
	s_cmpk_gt_u32 s26, 0x47ff
	s_cbranch_scc0 .LBB0_727
	s_add_i32 s20, s26, 0xffffb800
	s_lshr_b32 s24, s20, 4
	s_lshl_b32 s22, s24, 11
	s_lshl_b32 s20, s20, 7
	s_sub_i32 s22, s20, s22
	s_ashr_i32 s23, s22, 31
	s_lshl_b32 s20, s24, 6
	s_lshl_b64 s[24:25], s[22:23], 13
	s_add_u32 s27, s14, s24
	v_mov_b32_e32 v1, v0
	s_addc_u32 s40, s15, s25
	s_lshl_b64 s[24:25], s[20:21], 2
	s_add_u32 s24, s27, s24
	v_lshlrev_b32_e32 v2, 2, v1
	v_ashrrev_i32_e32 v12, 4, v1
	v_and_b32_e32 v24, 60, v2
	s_addc_u32 s25, s40, s25
	v_lshlrev_b32_e32 v10, 2, v24
	v_ashrrev_i32_e32 v13, 31, v12
	v_lshl_add_u64 v[2:3], s[24:25], 0, v[10:11]
	v_lshlrev_b64 v[4:5], 13, v[12:13]
	v_lshl_add_u64 v[14:15], v[2:3], 0, v[4:5]
	v_add_co_u32_e32 v6, vcc, s33, v14
	v_ashrrev_i32_e32 v22, 3, v1
	s_nop 0
	v_addc_co_u32_e32 v7, vcc, 0, v15, vcc
	v_add_co_u32_e32 v16, vcc, s34, v14
	global_load_dwordx4 v[2:5], v[14:15], off nt
	s_nop 0
	global_load_dwordx4 v[6:9], v[6:7], off nt
	v_addc_co_u32_e32 v17, vcc, 0, v15, vcc
	v_add_co_u32_e32 v18, vcc, s35, v14
	v_lshlrev_b32_e32 v1, 4, v1
	s_nop 0
	v_addc_co_u32_e32 v19, vcc, 0, v15, vcc
	global_load_dwordx4 v[14:17], v[16:17], off nt
	s_nop 0
	global_load_dwordx4 v[18:21], v[18:19], off nt
	v_lshlrev_b32_e32 v10, 2, v12
	v_ashrrev_i32_e32 v23, 31, v22
	v_mul_u32_u24_e32 v24, 0x204, v24
	v_mul_lo_u32 v25, v22, s36
	v_lshlrev_b64 v[12:13], 12, v[22:23]
	v_add3_u32 v22, 0, v10, v24
	v_and_b32_e32 v10, 0x70, v1
	v_lshlrev_b32_e32 v1, 2, v10
	v_add3_u32 v1, 0, v25, v1
	v_add_u32_e32 v23, 0x400, v22
	s_lshl_b64 s[24:25], s[20:21], 12
	s_waitcnt vmcnt(63) expcnt(7) lgkmcnt(15)
	s_barrier
	s_add_u32 s20, s0, s24
	s_addc_u32 s24, s1, s25
	s_lshl_b64 s[22:23], s[22:23], 1
	s_add_u32 s22, s20, s22
	s_addc_u32 s23, s24, s23
	v_lshl_add_u64 v[12:13], s[22:23], 0, v[12:13]
	s_mov_b64 s[22:23], 0
	s_waitcnt vmcnt(2)
	ds_write2_b32 v22, v2, v6 offset1:32
	ds_write2_b32 v22, v3, v7 offset0:129 offset1:161
	ds_write2_b32 v23, v4, v8 offset0:2 offset1:34
	ds_write2_b32 v23, v5, v9 offset0:131 offset1:163
	s_waitcnt vmcnt(0)
	ds_write2_b32 v22, v14, v18 offset0:64 offset1:96
	ds_write2_b32 v22, v15, v19 offset0:193 offset1:225
	ds_write2_b32 v23, v16, v20 offset0:66 offset1:98
	ds_write2_b32 v23, v17, v21 offset0:195 offset1:227
	s_waitcnt lgkmcnt(0)
	s_barrier
	ds_read2_b32 v[2:3], v1 offset1:1
	ds_read2_b32 v[4:5], v1 offset0:2 offset1:3
	ds_read2_b32 v[6:7], v1 offset0:4 offset1:5
	ds_read2_b32 v[8:9], v1 offset0:6 offset1:7
	ds_read2_b32 v[14:15], v1 offset0:8 offset1:9
	ds_read2_b32 v[16:17], v1 offset0:10 offset1:11
	ds_read2_b32 v[18:19], v1 offset0:12 offset1:13
	ds_read2_b32 v[20:21], v1 offset0:14 offset1:15
	s_waitcnt lgkmcnt(7)
	v_cvt_pk_bf16_f32 v2, v2, v3
	s_waitcnt lgkmcnt(6)
	v_cvt_pk_bf16_f32 v3, v4, v5
	s_waitcnt lgkmcnt(5)
	v_cvt_pk_bf16_f32 v4, v6, v7
	s_waitcnt lgkmcnt(4)
	v_cvt_pk_bf16_f32 v5, v8, v9
	s_waitcnt lgkmcnt(3)
	v_cvt_pk_bf16_f32 v6, v14, v15
	s_waitcnt lgkmcnt(2)
	v_cvt_pk_bf16_f32 v7, v16, v17
	s_waitcnt lgkmcnt(1)
	v_cvt_pk_bf16_f32 v8, v18, v19
	s_waitcnt lgkmcnt(0)
	v_cvt_pk_bf16_f32 v9, v20, v21
.LBB0_727:
	s_andn2_b64 vcc, exec, s[22:23]
	s_cbranch_vccnz .LBB0_729
	s_add_i32 s20, s26, 0xffffbe00
	s_lshr_b32 s24, s20, 4
	s_lshl_b32 s22, s24, 11
	s_lshl_b32 s20, s20, 7
	s_sub_i32 s22, s20, s22
	s_ashr_i32 s23, s22, 31
	s_lshl_b32 s20, s24, 6
	s_mul_i32 s25, s22, 0x6000
	s_mul_hi_i32 s24, s22, 0x6000
	s_add_u32 s27, s12, s25
	v_mov_b32_e32 v1, v0
	s_addc_u32 s40, s13, s24
	s_lshl_b64 s[24:25], s[20:21], 2
	s_add_u32 s24, s27, s24
	v_lshlrev_b32_e32 v2, 2, v1
	v_and_b32_e32 v22, 60, v2
	s_addc_u32 s25, s40, s25
	v_ashrrev_i32_e32 v21, 4, v1
	v_lshlrev_b32_e32 v10, 2, v22
	v_lshl_add_u64 v[12:13], s[24:25], 0, v[10:11]
	v_add_u32_e32 v10, 64, v21
	v_add_u32_e32 v4, 32, v21
	v_mad_i64_i32 v[14:15], s[24:25], v10, s37, v[12:13]
	v_add_u32_e32 v10, 0x60, v21
	v_mad_i64_i32 v[2:3], s[24:25], v21, s37, v[12:13]
	v_mad_i64_i32 v[6:7], s[24:25], v4, s37, v[12:13]
	v_mad_i64_i32 v[16:17], s[24:25], v10, s37, v[12:13]
	global_load_dwordx4 v[2:5], v[2:3], off nt
	s_nop 0
	global_load_dwordx4 v[6:9], v[6:7], off nt
	s_nop 0
	global_load_dwordx4 v[12:15], v[14:15], off nt
	s_nop 0
	global_load_dwordx4 v[16:19], v[16:17], off nt
	v_ashrrev_i32_e32 v20, 3, v1
	v_lshlrev_b32_e32 v1, 4, v1
	v_lshlrev_b32_e32 v10, 2, v21
	v_mul_u32_u24_e32 v22, 0x204, v22
	v_add3_u32 v22, 0, v10, v22
	v_and_b32_e32 v10, 0x70, v1
	v_mul_lo_u32 v23, v20, s36
	v_lshlrev_b32_e32 v1, 2, v10
	s_lshl_b64 s[24:25], s[20:21], 12
	v_add3_u32 v1, 0, v23, v1
	v_add_u32_e32 v24, 0x400, v22
	s_add_u32 s20, s3, s24
	s_waitcnt vmcnt(63) expcnt(7) lgkmcnt(15)
	s_barrier
	s_addc_u32 s24, s4, s25
	s_lshl_b64 s[22:23], s[22:23], 1
	v_ashrrev_i32_e32 v21, 31, v20
	s_add_u32 s22, s20, s22
	v_lshlrev_b64 v[20:21], 12, v[20:21]
	s_addc_u32 s23, s24, s23
	s_waitcnt vmcnt(2)
	ds_write2_b32 v22, v2, v6 offset1:32
	ds_write2_b32 v22, v3, v7 offset0:129 offset1:161
	ds_write2_b32 v24, v4, v8 offset0:2 offset1:34
	ds_write2_b32 v24, v5, v9 offset0:131 offset1:163
	s_waitcnt vmcnt(0)
	ds_write2_b32 v22, v12, v16 offset0:64 offset1:96
	ds_write2_b32 v22, v13, v17 offset0:193 offset1:225
	ds_write2_b32 v24, v14, v18 offset0:66 offset1:98
	ds_write2_b32 v24, v15, v19 offset0:195 offset1:227
	s_waitcnt lgkmcnt(0)
	s_barrier
	ds_read2_b32 v[2:3], v1 offset1:1
	ds_read2_b32 v[4:5], v1 offset0:2 offset1:3
	ds_read2_b32 v[6:7], v1 offset0:4 offset1:5
	ds_read2_b32 v[8:9], v1 offset0:6 offset1:7
	ds_read2_b32 v[12:13], v1 offset0:8 offset1:9
	ds_read2_b32 v[14:15], v1 offset0:10 offset1:11
	ds_read2_b32 v[16:17], v1 offset0:12 offset1:13
	ds_read2_b32 v[18:19], v1 offset0:14 offset1:15
	s_waitcnt lgkmcnt(7)
	v_cvt_pk_bf16_f32 v2, v2, v3
	s_waitcnt lgkmcnt(6)
	v_cvt_pk_bf16_f32 v3, v4, v5
	s_waitcnt lgkmcnt(5)
	v_cvt_pk_bf16_f32 v4, v6, v7
	s_waitcnt lgkmcnt(3)
	v_cvt_pk_bf16_f32 v6, v12, v13
	v_lshl_add_u64 v[12:13], s[22:23], 0, v[20:21]
	v_cvt_pk_bf16_f32 v5, v8, v9
	s_waitcnt lgkmcnt(2)
	v_cvt_pk_bf16_f32 v7, v14, v15
	s_waitcnt lgkmcnt(1)
	v_cvt_pk_bf16_f32 v8, v16, v17
	s_waitcnt lgkmcnt(0)
	v_cvt_pk_bf16_f32 v9, v18, v19

.LBB0_733:
	s_andn2_b64 vcc, exec, s[22:23]
	s_cbranch_vccnz .LBB0_714
	s_cmpk_gt_u32 s26, 0x2bff
	s_mov_b64 s[22:23], -1
	s_cbranch_scc0 .LBB0_736
	s_add_i32 s22, s26, 0xffffd400
	s_mul_i32 s23, s22, 0xba2f
	s_lshr_b32 s23, s23, 24
	s_mul_i32 s24, s23, 0xfffffea0
	s_add_i32 s23, s20, s23
	s_add_i32 s22, s24, s22
	s_mul_i32 s25, s23, 0xb00000
	s_mul_hi_u32 s24, s23, 0xb00000
	s_add_u32 s27, s16, s25
	s_addc_u32 s42, s17, s24
	s_mul_i32 s23, s23, 0x580000
	s_add_u32 s43, s5, s23
	s_mul_i32 s23, s22, 0x1746
	s_addc_u32 s44, s28, 0
	s_lshr_b32 s24, s23, 31
	s_lshr_b32 s23, s23, 16
	s_add_i32 s23, s23, s24
	s_sext_i32_i16 s45, s23
	s_mul_i32 s23, s45, -11
	s_add_i32 s23, s23, s22
	s_lshl_b32 s22, s23, 7
	s_ashr_i32 s23, s22, 31
	s_lshl_b32 s24, s45, 6
	s_ashr_i32 s25, s24, 31
	s_lshl_b64 s[40:41], s[22:23], 13
	s_add_u32 s27, s27, s40
	v_mov_b32_e32 v1, v0
	s_addc_u32 s42, s42, s41
	s_lshl_b64 s[40:41], s[24:25], 2
	s_add_u32 s40, s27, s40
	v_lshlrev_b32_e32 v2, 2, v1
	v_ashrrev_i32_e32 v12, 4, v1
	v_and_b32_e32 v22, 60, v2
	s_addc_u32 s41, s42, s41
	v_lshlrev_b32_e32 v10, 2, v22
	v_ashrrev_i32_e32 v13, 31, v12
	v_lshl_add_u64 v[2:3], s[40:41], 0, v[10:11]
	v_lshlrev_b64 v[4:5], 13, v[12:13]
	v_lshl_add_u64 v[14:15], v[2:3], 0, v[4:5]
	v_add_co_u32_e32 v6, vcc, s33, v14
	v_ashrrev_i32_e32 v23, 3, v1
	s_nop 0
	v_addc_co_u32_e32 v7, vcc, 0, v15, vcc
	v_add_co_u32_e32 v16, vcc, s34, v14
	global_load_dwordx4 v[2:5], v[14:15], off nt
	s_nop 0
	global_load_dwordx4 v[6:9], v[6:7], off nt
	v_addc_co_u32_e32 v17, vcc, 0, v15, vcc
	v_add_co_u32_e32 v18, vcc, s35, v14
	v_lshlrev_b32_e32 v1, 4, v1
	s_nop 0
	v_addc_co_u32_e32 v19, vcc, 0, v15, vcc
	global_load_dwordx4 v[14:17], v[16:17], off nt
	s_nop 0
	global_load_dwordx4 v[18:21], v[18:19], off nt
	v_lshlrev_b32_e32 v10, 2, v12
	v_mul_u32_u24_e32 v13, 0x204, v22
	v_add3_u32 v22, 0, v10, v13
	v_and_b32_e32 v10, 0x70, v1
	v_mul_lo_u32 v12, v23, s36
	s_mul_i32 s45, s45, 0x2c000
	v_lshlrev_b32_e32 v1, 2, v10
	s_mul_hi_i32 s24, s24, 0xb00
	s_add_u32 s25, s43, s45
	v_add3_u32 v1, 0, v12, v1
	v_add_u32_e32 v24, 0x400, v22
	s_addc_u32 s24, s44, s24
	s_lshl_b64 s[22:23], s[22:23], 1
	s_waitcnt vmcnt(63) expcnt(7) lgkmcnt(15)
	s_barrier
	s_add_u32 s22, s25, s22
	s_addc_u32 s23, s24, s23
	v_mov_b64_e32 v[12:13], s[22:23]
	v_mad_i64_i32 v[12:13], s[22:23], v23, s38, v[12:13]
	s_mov_b64 s[22:23], 0
	s_waitcnt vmcnt(2)
	ds_write2_b32 v22, v2, v6 offset1:32
	ds_write2_b32 v22, v3, v7 offset0:129 offset1:161
	ds_write2_b32 v24, v4, v8 offset0:2 offset1:34
	ds_write2_b32 v24, v5, v9 offset0:131 offset1:163
	s_waitcnt vmcnt(0)
	ds_write2_b32 v22, v14, v18 offset0:64 offset1:96
	ds_write2_b32 v22, v15, v19 offset0:193 offset1:225
	ds_write2_b32 v24, v16, v20 offset0:66 offset1:98
	ds_write2_b32 v24, v17, v21 offset0:195 offset1:227
	s_waitcnt lgkmcnt(0)
	s_barrier
	ds_read2_b32 v[2:3], v1 offset1:1
	ds_read2_b32 v[4:5], v1 offset0:2 offset1:3
	ds_read2_b32 v[6:7], v1 offset0:4 offset1:5
	ds_read2_b32 v[8:9], v1 offset0:6 offset1:7
	ds_read2_b32 v[14:15], v1 offset0:8 offset1:9
	ds_read2_b32 v[16:17], v1 offset0:10 offset1:11
	ds_read2_b32 v[18:19], v1 offset0:12 offset1:13
	ds_read2_b32 v[20:21], v1 offset0:14 offset1:15
	s_waitcnt lgkmcnt(7)
	v_cvt_pk_bf16_f32 v2, v2, v3
	s_waitcnt lgkmcnt(6)
	v_cvt_pk_bf16_f32 v3, v4, v5
	s_waitcnt lgkmcnt(5)
	v_cvt_pk_bf16_f32 v4, v6, v7
	s_waitcnt lgkmcnt(4)
	v_cvt_pk_bf16_f32 v5, v8, v9
	s_waitcnt lgkmcnt(3)
	v_cvt_pk_bf16_f32 v6, v14, v15
	s_waitcnt lgkmcnt(2)
	v_cvt_pk_bf16_f32 v7, v16, v17
	s_waitcnt lgkmcnt(1)
	v_cvt_pk_bf16_f32 v8, v18, v19
	s_waitcnt lgkmcnt(0)
	v_cvt_pk_bf16_f32 v9, v20, v21
.LBB0_736:
	s_andn2_b64 vcc, exec, s[22:23]
	s_cbranch_vccnz .LBB0_714
	s_mul_i32 s22, s26, 0xba2f
	s_lshr_b32 s22, s22, 25
	s_mul_i32 s23, s22, 0xfffffd40
	s_add_i32 s23, s23, s26
	s_mul_i32 s24, s23, 0xba3
	s_lshr_b32 s25, s24, 31
	s_ashr_i32 s24, s24, 20
	s_add_i32 s24, s24, s25
	s_sext_i32_i16 s25, s24
	s_mul_i32 s24, s25, 0xfffffea0
	s_add_i32 s27, s24, s23
	s_add_i32 s20, s20, s22
	s_addk_i32 s23, 0x15f
	s_cmpk_lt_u32 s23, 0x2bf
	s_cselect_b32 s23, s8, s10
	s_mul_i32 s20, s20, 0xb00000
	s_cselect_b32 s22, s9, s11
	s_add_u32 s23, s23, s20
	s_addc_u32 s40, s22, 0
	s_lshl_b32 s22, s27, 2
	s_lshl_b32 s27, s27, 3
	s_and_b32 s27, s27, 0xffffff00
	s_lshl_b32 s25, s25, 7
	s_and_b32 s24, s22, 0xffffffc0
	s_add_i32 s27, s27, s25
	s_and_b32 s22, s22, 64
	s_or_b32 s22, s27, s22
	s_add_u32 s20, s29, s20
	s_addc_u32 s27, s30, 0
	s_lshl_b32 s25, s26, 7
	s_and_b32 s26, s25, 0x780
	s_mul_i32 s25, s26, 0x1600
	s_add_u32 s23, s23, s25
	s_addc_u32 s40, s40, 0
	s_ashr_i32 s25, s24, 31
	v_mov_b32_e32 v1, v0
	s_lshl_b64 s[24:25], s[24:25], 2
	s_add_u32 s24, s23, s24
	v_lshlrev_b32_e32 v2, 2, v1
	v_and_b32_e32 v22, 60, v2
	s_addc_u32 s25, s40, s25
	v_ashrrev_i32_e32 v21, 4, v1
	v_lshlrev_b32_e32 v10, 2, v22
	v_lshl_add_u64 v[12:13], s[24:25], 0, v[10:11]
	v_add_u32_e32 v10, 64, v21
	v_add_u32_e32 v4, 32, v21
	v_mad_i64_i32 v[14:15], s[24:25], v10, s39, v[12:13]
	v_add_u32_e32 v10, 0x60, v21
	v_mad_i64_i32 v[2:3], s[24:25], v21, s39, v[12:13]
	v_mad_i64_i32 v[6:7], s[24:25], v4, s39, v[12:13]
	v_mad_i64_i32 v[16:17], s[24:25], v10, s39, v[12:13]
	global_load_dwordx4 v[2:5], v[2:3], off nt
	s_nop 0
	global_load_dwordx4 v[6:9], v[6:7], off nt
	s_nop 0
	global_load_dwordx4 v[12:15], v[14:15], off nt
	s_nop 0
	global_load_dwordx4 v[16:19], v[16:17], off nt
	v_ashrrev_i32_e32 v20, 3, v1
	v_lshlrev_b32_e32 v1, 4, v1
	v_lshlrev_b32_e32 v10, 2, v21
	v_mul_u32_u24_e32 v22, 0x204, v22
	v_add3_u32 v22, 0, v10, v22
	v_and_b32_e32 v10, 0x70, v1
	v_mul_lo_u32 v23, v20, s36
	s_ashr_i32 s23, s22, 31
	v_lshlrev_b32_e32 v1, 2, v10
	s_lshl_b64 s[22:23], s[22:23], 12
	v_add3_u32 v1, 0, v23, v1
	v_add_u32_e32 v24, 0x400, v22
	s_add_u32 s20, s20, s22
	s_waitcnt vmcnt(63) expcnt(7) lgkmcnt(15)
	s_barrier
	s_addc_u32 s23, s27, s23
	s_lshl_b32 s22, s26, 1
	v_ashrrev_i32_e32 v21, 31, v20
	s_add_u32 s22, s20, s22
	v_lshlrev_b64 v[20:21], 12, v[20:21]
	s_addc_u32 s23, s23, 0
	s_waitcnt vmcnt(2)
	ds_write2_b32 v22, v2, v6 offset1:32
	ds_write2_b32 v22, v3, v7 offset0:129 offset1:161
	ds_write2_b32 v24, v4, v8 offset0:2 offset1:34
	ds_write2_b32 v24, v5, v9 offset0:131 offset1:163
	s_waitcnt vmcnt(0)
	ds_write2_b32 v22, v12, v16 offset0:64 offset1:96
	ds_write2_b32 v22, v13, v17 offset0:193 offset1:225
	ds_write2_b32 v24, v14, v18 offset0:66 offset1:98
	ds_write2_b32 v24, v15, v19 offset0:195 offset1:227
	s_waitcnt lgkmcnt(0)
	s_barrier
	ds_read2_b32 v[2:3], v1 offset1:1
	ds_read2_b32 v[4:5], v1 offset0:2 offset1:3
	ds_read2_b32 v[6:7], v1 offset0:4 offset1:5
	ds_read2_b32 v[8:9], v1 offset0:6 offset1:7
	ds_read2_b32 v[12:13], v1 offset0:8 offset1:9
	ds_read2_b32 v[14:15], v1 offset0:10 offset1:11
	ds_read2_b32 v[16:17], v1 offset0:12 offset1:13
	ds_read2_b32 v[18:19], v1 offset0:14 offset1:15
	s_waitcnt lgkmcnt(7)
	v_cvt_pk_bf16_f32 v2, v2, v3
	s_waitcnt lgkmcnt(6)
	v_cvt_pk_bf16_f32 v3, v4, v5
	s_waitcnt lgkmcnt(5)
	v_cvt_pk_bf16_f32 v4, v6, v7
	s_waitcnt lgkmcnt(3)
	v_cvt_pk_bf16_f32 v6, v12, v13
	v_lshl_add_u64 v[12:13], s[22:23], 0, v[20:21]
	v_cvt_pk_bf16_f32 v5, v8, v9
	s_waitcnt lgkmcnt(2)
	v_cvt_pk_bf16_f32 v7, v14, v15
	s_waitcnt lgkmcnt(1)
	v_cvt_pk_bf16_f32 v8, v16, v17
	s_waitcnt lgkmcnt(0)
	v_cvt_pk_bf16_f32 v9, v18, v19
	s_branch .LBB0_714

.LBB0_990:
	s_or_b64 exec, exec, s[10:11]
	s_waitcnt lgkmcnt(0)
	s_barrier
	ds_read_b32 v1, v11 offset:40960
	s_mov_b64 s[10:11], -1
	s_waitcnt lgkmcnt(0)
	v_cmp_lt_u32_e32 vcc, s19, v1
	v_readfirstlane_b32 s14, v1
	s_cbranch_vccnz .LBB0_983
	s_cmpk_lt_u32 s14, 0x4a00
	s_cbranch_scc0 .LBB0_999
	s_cmpk_gt_u32 s14, 0x41ff
	s_cbranch_scc0 .LBB0_998
	s_cmpk_gt_u32 s14, 0x47ff
	s_cbranch_scc0 .LBB0_995
	s_add_i32 s8, s14, 0xffffb800
	s_lshr_b32 s12, s8, 4
	s_lshl_b32 s10, s12, 11
	s_lshl_b32 s8, s8, 7
	s_sub_i32 s10, s8, s10
	s_ashr_i32 s11, s10, 31
	s_lshl_b32 s8, s12, 6
	s_lshl_b64 s[12:13], s[10:11], 13
	s_add_u32 s15, s72, s12
	v_mov_b32_e32 v1, v0
	s_addc_u32 s27, s73, s13
	s_lshl_b64 s[12:13], s[8:9], 2
	s_add_u32 s12, s15, s12
	v_lshlrev_b32_e32 v2, 2, v1
	v_ashrrev_i32_e32 v12, 4, v1
	v_and_b32_e32 v24, 60, v2
	s_addc_u32 s13, s27, s13
	v_lshlrev_b32_e32 v10, 2, v24
	v_ashrrev_i32_e32 v13, 31, v12
	v_lshl_add_u64 v[2:3], s[12:13], 0, v[10:11]
	v_lshlrev_b64 v[4:5], 13, v[12:13]
	v_lshl_add_u64 v[14:15], v[2:3], 0, v[4:5]
	v_add_co_u32_e32 v6, vcc, s20, v14
	v_ashrrev_i32_e32 v22, 3, v1
	s_nop 0
	v_addc_co_u32_e32 v7, vcc, 0, v15, vcc
	v_add_co_u32_e32 v16, vcc, s21, v14
	global_load_dwordx4 v[2:5], v[14:15], off nt
	s_nop 0
	global_load_dwordx4 v[6:9], v[6:7], off nt
	v_addc_co_u32_e32 v17, vcc, 0, v15, vcc
	v_add_co_u32_e32 v18, vcc, s22, v14
	v_lshlrev_b32_e32 v1, 4, v1
	s_nop 0
	v_addc_co_u32_e32 v19, vcc, 0, v15, vcc
	global_load_dwordx4 v[14:17], v[16:17], off nt
	s_nop 0
	global_load_dwordx4 v[18:21], v[18:19], off nt
	v_lshlrev_b32_e32 v10, 2, v12
	v_ashrrev_i32_e32 v23, 31, v22
	v_mul_u32_u24_e32 v24, 0x204, v24
	v_mul_lo_u32 v25, v22, s23
	v_lshlrev_b64 v[12:13], 12, v[22:23]
	v_add3_u32 v22, 0, v10, v24
	v_and_b32_e32 v10, 0x70, v1
	v_lshlrev_b32_e32 v1, 2, v10
	v_add3_u32 v1, 0, v25, v1
	v_add_u32_e32 v23, 0x400, v22
	s_lshl_b64 s[12:13], s[8:9], 12
	s_waitcnt vmcnt(63) expcnt(7) lgkmcnt(15)
	s_barrier
	s_add_u32 s8, s0, s12
	s_addc_u32 s12, s1, s13
	s_lshl_b64 s[10:11], s[10:11], 1
	s_add_u32 s10, s8, s10
	s_addc_u32 s11, s12, s11
	v_lshl_add_u64 v[12:13], s[10:11], 0, v[12:13]
	s_mov_b64 s[10:11], 0
	s_waitcnt vmcnt(2)
	ds_write2_b32 v22, v2, v6 offset1:32
	ds_write2_b32 v22, v3, v7 offset0:129 offset1:161
	ds_write2_b32 v23, v4, v8 offset0:2 offset1:34
	ds_write2_b32 v23, v5, v9 offset0:131 offset1:163
	s_waitcnt vmcnt(0)
	ds_write2_b32 v22, v14, v18 offset0:64 offset1:96
	ds_write2_b32 v22, v15, v19 offset0:193 offset1:225
	ds_write2_b32 v23, v16, v20 offset0:66 offset1:98
	ds_write2_b32 v23, v17, v21 offset0:195 offset1:227
	s_waitcnt lgkmcnt(0)
	s_barrier
	ds_read2_b32 v[2:3], v1 offset1:1
	ds_read2_b32 v[4:5], v1 offset0:2 offset1:3
	ds_read2_b32 v[6:7], v1 offset0:4 offset1:5
	ds_read2_b32 v[8:9], v1 offset0:6 offset1:7
	ds_read2_b32 v[14:15], v1 offset0:8 offset1:9
	ds_read2_b32 v[16:17], v1 offset0:10 offset1:11
	ds_read2_b32 v[18:19], v1 offset0:12 offset1:13
	ds_read2_b32 v[20:21], v1 offset0:14 offset1:15
	s_waitcnt lgkmcnt(7)
	v_cvt_pk_bf16_f32 v2, v2, v3
	s_waitcnt lgkmcnt(6)
	v_cvt_pk_bf16_f32 v3, v4, v5
	s_waitcnt lgkmcnt(5)
	v_cvt_pk_bf16_f32 v4, v6, v7
	s_waitcnt lgkmcnt(4)
	v_cvt_pk_bf16_f32 v5, v8, v9
	s_waitcnt lgkmcnt(3)
	v_cvt_pk_bf16_f32 v6, v14, v15
	s_waitcnt lgkmcnt(2)
	v_cvt_pk_bf16_f32 v7, v16, v17
	s_waitcnt lgkmcnt(1)
	v_cvt_pk_bf16_f32 v8, v18, v19
	s_waitcnt lgkmcnt(0)
	v_cvt_pk_bf16_f32 v9, v20, v21
.LBB0_995:
	s_andn2_b64 vcc, exec, s[10:11]
	s_cbranch_vccnz .LBB0_997
	s_add_i32 s8, s14, 0xffffbe00
	s_lshr_b32 s12, s8, 4
	s_lshl_b32 s10, s12, 11
	s_lshl_b32 s8, s8, 7
	s_sub_i32 s10, s8, s10
	s_ashr_i32 s11, s10, 31
	s_lshl_b32 s8, s12, 6
	s_mul_i32 s13, s10, 0x6000
	s_mul_hi_i32 s12, s10, 0x6000
	s_add_u32 s15, s70, s13
	v_mov_b32_e32 v1, v0
	s_addc_u32 s27, s71, s12
	s_lshl_b64 s[12:13], s[8:9], 2
	s_add_u32 s12, s15, s12
	v_lshlrev_b32_e32 v2, 2, v1
	v_and_b32_e32 v22, 60, v2
	s_addc_u32 s13, s27, s13
	v_ashrrev_i32_e32 v21, 4, v1
	v_lshlrev_b32_e32 v10, 2, v22
	v_lshl_add_u64 v[12:13], s[12:13], 0, v[10:11]
	v_add_u32_e32 v10, 64, v21
	v_add_u32_e32 v4, 32, v21
	v_mad_i64_i32 v[14:15], s[12:13], v10, s24, v[12:13]
	v_add_u32_e32 v10, 0x60, v21
	v_mad_i64_i32 v[2:3], s[12:13], v21, s24, v[12:13]
	v_mad_i64_i32 v[6:7], s[12:13], v4, s24, v[12:13]
	v_mad_i64_i32 v[16:17], s[12:13], v10, s24, v[12:13]
	global_load_dwordx4 v[2:5], v[2:3], off nt
	s_nop 0
	global_load_dwordx4 v[6:9], v[6:7], off nt
	s_nop 0
	global_load_dwordx4 v[12:15], v[14:15], off nt
	s_nop 0
	global_load_dwordx4 v[16:19], v[16:17], off nt
	v_ashrrev_i32_e32 v20, 3, v1
	v_lshlrev_b32_e32 v1, 4, v1
	v_lshlrev_b32_e32 v10, 2, v21
	v_mul_u32_u24_e32 v22, 0x204, v22
	v_add3_u32 v22, 0, v10, v22
	v_and_b32_e32 v10, 0x70, v1
	v_mul_lo_u32 v23, v20, s23
	v_lshlrev_b32_e32 v1, 2, v10
	s_lshl_b64 s[12:13], s[8:9], 12
	v_add3_u32 v1, 0, v23, v1
	v_add_u32_e32 v24, 0x400, v22
	s_add_u32 s8, s3, s12
	s_waitcnt vmcnt(63) expcnt(7) lgkmcnt(15)
	s_barrier
	s_addc_u32 s12, s4, s13
	s_lshl_b64 s[10:11], s[10:11], 1
	v_ashrrev_i32_e32 v21, 31, v20
	s_add_u32 s10, s8, s10
	v_lshlrev_b64 v[20:21], 12, v[20:21]
	s_addc_u32 s11, s12, s11
	s_waitcnt vmcnt(2)
	ds_write2_b32 v22, v2, v6 offset1:32
	ds_write2_b32 v22, v3, v7 offset0:129 offset1:161
	ds_write2_b32 v24, v4, v8 offset0:2 offset1:34
	ds_write2_b32 v24, v5, v9 offset0:131 offset1:163
	s_waitcnt vmcnt(0)
	ds_write2_b32 v22, v12, v16 offset0:64 offset1:96
	ds_write2_b32 v22, v13, v17 offset0:193 offset1:225
	ds_write2_b32 v24, v14, v18 offset0:66 offset1:98
	ds_write2_b32 v24, v15, v19 offset0:195 offset1:227
	s_waitcnt lgkmcnt(0)
	s_barrier
	ds_read2_b32 v[2:3], v1 offset1:1
	ds_read2_b32 v[4:5], v1 offset0:2 offset1:3
	ds_read2_b32 v[6:7], v1 offset0:4 offset1:5
	ds_read2_b32 v[8:9], v1 offset0:6 offset1:7
	ds_read2_b32 v[12:13], v1 offset0:8 offset1:9
	ds_read2_b32 v[14:15], v1 offset0:10 offset1:11
	ds_read2_b32 v[16:17], v1 offset0:12 offset1:13
	ds_read2_b32 v[18:19], v1 offset0:14 offset1:15
	s_waitcnt lgkmcnt(7)
	v_cvt_pk_bf16_f32 v2, v2, v3
	s_waitcnt lgkmcnt(6)
	v_cvt_pk_bf16_f32 v3, v4, v5
	s_waitcnt lgkmcnt(5)
	v_cvt_pk_bf16_f32 v4, v6, v7
	s_waitcnt lgkmcnt(3)
	v_cvt_pk_bf16_f32 v6, v12, v13
	v_lshl_add_u64 v[12:13], s[10:11], 0, v[20:21]
	v_cvt_pk_bf16_f32 v5, v8, v9
	s_waitcnt lgkmcnt(2)
	v_cvt_pk_bf16_f32 v7, v14, v15
	s_waitcnt lgkmcnt(1)
	v_cvt_pk_bf16_f32 v8, v16, v17
	s_waitcnt lgkmcnt(0)
	v_cvt_pk_bf16_f32 v9, v18, v19

.LBB0_1001:
	s_andn2_b64 vcc, exec, s[10:11]
	s_cbranch_vccnz .LBB0_982
	s_cmpk_gt_u32 s14, 0x2bff
	s_mov_b64 s[10:11], -1
	s_cbranch_scc0 .LBB0_1004
	s_add_i32 s10, s14, 0xffffd400
	s_mul_i32 s11, s10, 0xba2f
	s_lshr_b32 s11, s11, 24
	s_mul_i32 s12, s11, 0xfffffea0
	s_add_i32 s11, s8, s11
	s_add_i32 s10, s12, s10
	s_mul_i32 s13, s11, 0xb00000
	s_mul_hi_u32 s12, s11, 0xb00000
	s_add_u32 s15, s74, s13
	s_addc_u32 s27, s75, s12
	s_mul_i32 s11, s11, 0x580000
	s_add_u32 s30, s5, s11
	s_mul_i32 s11, s10, 0x1746
	s_addc_u32 s31, s16, 0
	s_lshr_b32 s12, s11, 31
	s_lshr_b32 s11, s11, 16
	s_add_i32 s11, s11, s12
	s_sext_i32_i16 s33, s11
	s_mul_i32 s11, s33, -11
	s_add_i32 s11, s11, s10
	s_lshl_b32 s10, s11, 7
	s_ashr_i32 s11, s10, 31
	s_lshl_b32 s12, s33, 6
	s_ashr_i32 s13, s12, 31
	s_lshl_b64 s[28:29], s[10:11], 13
	s_add_u32 s15, s15, s28
	v_mov_b32_e32 v1, v0
	s_addc_u32 s27, s27, s29
	s_lshl_b64 s[28:29], s[12:13], 2
	s_add_u32 s28, s15, s28
	v_lshlrev_b32_e32 v2, 2, v1
	v_ashrrev_i32_e32 v12, 4, v1
	v_and_b32_e32 v22, 60, v2
	s_addc_u32 s29, s27, s29
	v_lshlrev_b32_e32 v10, 2, v22
	v_ashrrev_i32_e32 v13, 31, v12
	v_lshl_add_u64 v[2:3], s[28:29], 0, v[10:11]
	v_lshlrev_b64 v[4:5], 13, v[12:13]
	v_lshl_add_u64 v[14:15], v[2:3], 0, v[4:5]
	v_add_co_u32_e32 v6, vcc, s20, v14
	v_ashrrev_i32_e32 v23, 3, v1
	s_nop 0
	v_addc_co_u32_e32 v7, vcc, 0, v15, vcc
	v_add_co_u32_e32 v16, vcc, s21, v14
	global_load_dwordx4 v[2:5], v[14:15], off nt
	s_nop 0
	global_load_dwordx4 v[6:9], v[6:7], off nt
	v_addc_co_u32_e32 v17, vcc, 0, v15, vcc
	v_add_co_u32_e32 v18, vcc, s22, v14
	v_lshlrev_b32_e32 v1, 4, v1
	s_nop 0
	v_addc_co_u32_e32 v19, vcc, 0, v15, vcc
	global_load_dwordx4 v[14:17], v[16:17], off nt
	s_nop 0
	global_load_dwordx4 v[18:21], v[18:19], off nt
	v_lshlrev_b32_e32 v10, 2, v12
	v_mul_u32_u24_e32 v13, 0x204, v22
	v_add3_u32 v22, 0, v10, v13
	v_and_b32_e32 v10, 0x70, v1
	v_mul_lo_u32 v12, v23, s23
	s_mul_i32 s33, s33, 0x2c000
	v_lshlrev_b32_e32 v1, 2, v10
	s_mul_hi_i32 s12, s12, 0xb00
	s_add_u32 s13, s30, s33
	v_add3_u32 v1, 0, v12, v1
	v_add_u32_e32 v24, 0x400, v22
	s_addc_u32 s12, s31, s12
	s_lshl_b64 s[10:11], s[10:11], 1
	s_waitcnt vmcnt(63) expcnt(7) lgkmcnt(15)
	s_barrier
	s_add_u32 s10, s13, s10
	s_addc_u32 s11, s12, s11
	v_mov_b64_e32 v[12:13], s[10:11]
	v_mad_i64_i32 v[12:13], s[10:11], v23, s25, v[12:13]
	s_mov_b64 s[10:11], 0
	s_waitcnt vmcnt(2)
	ds_write2_b32 v22, v2, v6 offset1:32
	ds_write2_b32 v22, v3, v7 offset0:129 offset1:161
	ds_write2_b32 v24, v4, v8 offset0:2 offset1:34
	ds_write2_b32 v24, v5, v9 offset0:131 offset1:163
	s_waitcnt vmcnt(0)
	ds_write2_b32 v22, v14, v18 offset0:64 offset1:96
	ds_write2_b32 v22, v15, v19 offset0:193 offset1:225
	ds_write2_b32 v24, v16, v20 offset0:66 offset1:98
	ds_write2_b32 v24, v17, v21 offset0:195 offset1:227
	s_waitcnt lgkmcnt(0)
	s_barrier
	ds_read2_b32 v[2:3], v1 offset1:1
	ds_read2_b32 v[4:5], v1 offset0:2 offset1:3
	ds_read2_b32 v[6:7], v1 offset0:4 offset1:5
	ds_read2_b32 v[8:9], v1 offset0:6 offset1:7
	ds_read2_b32 v[14:15], v1 offset0:8 offset1:9
	ds_read2_b32 v[16:17], v1 offset0:10 offset1:11
	ds_read2_b32 v[18:19], v1 offset0:12 offset1:13
	ds_read2_b32 v[20:21], v1 offset0:14 offset1:15
	s_waitcnt lgkmcnt(7)
	v_cvt_pk_bf16_f32 v2, v2, v3
	s_waitcnt lgkmcnt(6)
	v_cvt_pk_bf16_f32 v3, v4, v5
	s_waitcnt lgkmcnt(5)
	v_cvt_pk_bf16_f32 v4, v6, v7
	s_waitcnt lgkmcnt(4)
	v_cvt_pk_bf16_f32 v5, v8, v9
	s_waitcnt lgkmcnt(3)
	v_cvt_pk_bf16_f32 v6, v14, v15
	s_waitcnt lgkmcnt(2)
	v_cvt_pk_bf16_f32 v7, v16, v17
	s_waitcnt lgkmcnt(1)
	v_cvt_pk_bf16_f32 v8, v18, v19
	s_waitcnt lgkmcnt(0)
	v_cvt_pk_bf16_f32 v9, v20, v21
.LBB0_1004:
	s_andn2_b64 vcc, exec, s[10:11]
	s_cbranch_vccnz .LBB0_982
	s_mul_i32 s10, s14, 0xba2f
	s_lshr_b32 s10, s10, 25
	s_mul_i32 s11, s10, 0xfffffd40
	s_add_i32 s11, s11, s14
	s_mul_i32 s12, s11, 0xba3
	s_lshr_b32 s13, s12, 31
	s_ashr_i32 s12, s12, 20
	s_add_i32 s12, s12, s13
	s_sext_i32_i16 s13, s12
	s_mul_i32 s12, s13, 0xfffffea0
	s_add_i32 s15, s12, s11
	s_add_i32 s8, s8, s10
	s_addk_i32 s11, 0x15f
	s_cmpk_lt_u32 s11, 0x2bf
	s_cselect_b32 s11, s56, s58
	s_mul_i32 s8, s8, 0xb00000
	s_cselect_b32 s10, s57, s59
	s_add_u32 s11, s11, s8
	s_addc_u32 s27, s10, 0
	s_lshl_b32 s10, s15, 2
	s_lshl_b32 s15, s15, 3
	s_and_b32 s15, s15, 0xffffff00
	s_lshl_b32 s13, s13, 7
	s_and_b32 s12, s10, 0xffffffc0
	s_add_i32 s15, s15, s13
	s_and_b32 s10, s10, 64
	s_or_b32 s10, s15, s10
	s_add_u32 s8, s17, s8
	s_addc_u32 s15, s18, 0
	s_lshl_b32 s13, s14, 7
	s_and_b32 s14, s13, 0x780
	s_mul_i32 s13, s14, 0x1600
	s_add_u32 s11, s11, s13
	s_addc_u32 s27, s27, 0
	s_ashr_i32 s13, s12, 31
	v_mov_b32_e32 v1, v0
	s_lshl_b64 s[12:13], s[12:13], 2
	s_add_u32 s12, s11, s12
	v_lshlrev_b32_e32 v2, 2, v1
	v_and_b32_e32 v22, 60, v2
	s_addc_u32 s13, s27, s13
	v_ashrrev_i32_e32 v21, 4, v1
	v_lshlrev_b32_e32 v10, 2, v22
	v_lshl_add_u64 v[12:13], s[12:13], 0, v[10:11]
	v_add_u32_e32 v10, 64, v21
	v_add_u32_e32 v4, 32, v21
	v_mad_i64_i32 v[14:15], s[12:13], v10, s26, v[12:13]
	v_add_u32_e32 v10, 0x60, v21
	v_mad_i64_i32 v[2:3], s[12:13], v21, s26, v[12:13]
	v_mad_i64_i32 v[6:7], s[12:13], v4, s26, v[12:13]
	v_mad_i64_i32 v[16:17], s[12:13], v10, s26, v[12:13]
	global_load_dwordx4 v[2:5], v[2:3], off nt
	s_nop 0
	global_load_dwordx4 v[6:9], v[6:7], off nt
	s_nop 0
	global_load_dwordx4 v[12:15], v[14:15], off nt
	s_nop 0
	global_load_dwordx4 v[16:19], v[16:17], off nt
	v_ashrrev_i32_e32 v20, 3, v1
	v_lshlrev_b32_e32 v1, 4, v1
	v_lshlrev_b32_e32 v10, 2, v21
	v_mul_u32_u24_e32 v22, 0x204, v22
	v_add3_u32 v22, 0, v10, v22
	v_and_b32_e32 v10, 0x70, v1
	v_mul_lo_u32 v23, v20, s23
	s_ashr_i32 s11, s10, 31
	v_lshlrev_b32_e32 v1, 2, v10
	s_lshl_b64 s[10:11], s[10:11], 12
	v_add3_u32 v1, 0, v23, v1
	v_add_u32_e32 v24, 0x400, v22
	s_add_u32 s8, s8, s10
	s_waitcnt vmcnt(63) expcnt(7) lgkmcnt(15)
	s_barrier
	s_addc_u32 s11, s15, s11
	s_lshl_b32 s10, s14, 1
	v_ashrrev_i32_e32 v21, 31, v20
	s_add_u32 s10, s8, s10
	v_lshlrev_b64 v[20:21], 12, v[20:21]
	s_addc_u32 s11, s11, 0
	s_waitcnt vmcnt(2)
	ds_write2_b32 v22, v2, v6 offset1:32
	ds_write2_b32 v22, v3, v7 offset0:129 offset1:161
	ds_write2_b32 v24, v4, v8 offset0:2 offset1:34
	ds_write2_b32 v24, v5, v9 offset0:131 offset1:163
	s_waitcnt vmcnt(0)
	ds_write2_b32 v22, v12, v16 offset0:64 offset1:96
	ds_write2_b32 v22, v13, v17 offset0:193 offset1:225
	ds_write2_b32 v24, v14, v18 offset0:66 offset1:98
	ds_write2_b32 v24, v15, v19 offset0:195 offset1:227
	s_waitcnt lgkmcnt(0)
	s_barrier
	ds_read2_b32 v[2:3], v1 offset1:1
	ds_read2_b32 v[4:5], v1 offset0:2 offset1:3
	ds_read2_b32 v[6:7], v1 offset0:4 offset1:5
	ds_read2_b32 v[8:9], v1 offset0:6 offset1:7
	ds_read2_b32 v[12:13], v1 offset0:8 offset1:9
	ds_read2_b32 v[14:15], v1 offset0:10 offset1:11
	ds_read2_b32 v[16:17], v1 offset0:12 offset1:13
	ds_read2_b32 v[18:19], v1 offset0:14 offset1:15
	s_waitcnt lgkmcnt(7)
	v_cvt_pk_bf16_f32 v2, v2, v3
	s_waitcnt lgkmcnt(6)
	v_cvt_pk_bf16_f32 v3, v4, v5
	s_waitcnt lgkmcnt(5)
	v_cvt_pk_bf16_f32 v4, v6, v7
	s_waitcnt lgkmcnt(3)
	v_cvt_pk_bf16_f32 v6, v12, v13
	v_lshl_add_u64 v[12:13], s[10:11], 0, v[20:21]
	v_cvt_pk_bf16_f32 v5, v8, v9
	s_waitcnt lgkmcnt(2)
	v_cvt_pk_bf16_f32 v7, v14, v15
	s_waitcnt lgkmcnt(1)
	v_cvt_pk_bf16_f32 v8, v16, v17
	s_waitcnt lgkmcnt(0)
	v_cvt_pk_bf16_f32 v9, v18, v19
	s_branch .LBB0_982

.LBB0_1024:
	s_andn2_b64 vcc, exec, s[10:11]
	s_cbranch_vccnz .LBB0_1007
	s_cmpk_gt_u32 s8, 0x2bff
	s_mov_b64 s[10:11], -1
	s_cbranch_scc0 .LBB0_1027
	s_add_i32 s10, s8, 0xffffd400
	s_mul_i32 s11, s10, 0xba2f
	s_lshr_b32 s11, s11, 24
	s_mul_i32 s12, s11, 0xfffffea0
	s_add_i32 s11, s15, s11
	s_add_i32 s10, s12, s10
	s_mul_i32 s13, s11, 0xb00000
	s_mul_hi_u32 s12, s11, 0xb00000
	s_add_u32 s27, s74, s13
	s_addc_u32 s30, s75, s12
	s_mul_i32 s11, s11, 0x580000
	s_add_u32 s31, s5, s11
	s_mul_i32 s11, s10, 0x1746
	s_addc_u32 s33, s16, 0
	s_lshr_b32 s12, s11, 31
	s_lshr_b32 s11, s11, 16
	s_add_i32 s11, s11, s12
	s_sext_i32_i16 s34, s11
	s_mul_i32 s11, s34, -11
	s_add_i32 s11, s11, s10
	s_lshl_b32 s10, s11, 7
	s_ashr_i32 s11, s10, 31
	s_lshl_b32 s12, s34, 6
	s_ashr_i32 s13, s12, 31
	s_lshl_b64 s[28:29], s[10:11], 13
	s_add_u32 s27, s27, s28
	v_mov_b32_e32 v1, v0
	s_addc_u32 s30, s30, s29
	s_lshl_b64 s[28:29], s[12:13], 2
	s_add_u32 s28, s27, s28
	v_lshlrev_b32_e32 v2, 2, v1
	v_ashrrev_i32_e32 v12, 4, v1
	v_and_b32_e32 v22, 60, v2
	s_addc_u32 s29, s30, s29
	v_lshlrev_b32_e32 v10, 2, v22
	v_ashrrev_i32_e32 v13, 31, v12
	v_lshl_add_u64 v[2:3], s[28:29], 0, v[10:11]
	v_lshlrev_b64 v[4:5], 13, v[12:13]
	v_lshl_add_u64 v[14:15], v[2:3], 0, v[4:5]
	v_add_co_u32_e32 v6, vcc, s20, v14
	v_ashrrev_i32_e32 v23, 3, v1
	s_nop 0
	v_addc_co_u32_e32 v7, vcc, 0, v15, vcc
	v_add_co_u32_e32 v16, vcc, s21, v14
	global_load_dwordx4 v[2:5], v[14:15], off nt
	s_nop 0
	global_load_dwordx4 v[6:9], v[6:7], off nt
	v_addc_co_u32_e32 v17, vcc, 0, v15, vcc
	v_add_co_u32_e32 v18, vcc, s22, v14
	v_lshlrev_b32_e32 v1, 4, v1
	s_nop 0
	v_addc_co_u32_e32 v19, vcc, 0, v15, vcc
	global_load_dwordx4 v[14:17], v[16:17], off nt
	s_nop 0
	global_load_dwordx4 v[18:21], v[18:19], off nt
	v_lshlrev_b32_e32 v10, 2, v12
	v_mul_u32_u24_e32 v13, 0x204, v22
	v_add3_u32 v22, 0, v10, v13
	v_and_b32_e32 v10, 0x70, v1
	v_mul_lo_u32 v12, v23, s23
	s_mul_i32 s34, s34, 0x2c000
	v_lshlrev_b32_e32 v1, 2, v10
	s_mul_hi_i32 s12, s12, 0xb00
	s_add_u32 s13, s31, s34
	v_add3_u32 v1, 0, v12, v1
	v_add_u32_e32 v24, 0x400, v22
	s_addc_u32 s12, s33, s12
	s_lshl_b64 s[10:11], s[10:11], 1
	s_waitcnt vmcnt(63) expcnt(7) lgkmcnt(15)
	s_barrier
	s_add_u32 s10, s13, s10
	s_addc_u32 s11, s12, s11
	v_mov_b64_e32 v[12:13], s[10:11]
	v_mad_i64_i32 v[12:13], s[10:11], v23, s25, v[12:13]
	s_mov_b64 s[10:11], 0
	s_waitcnt vmcnt(2)
	ds_write2_b32 v22, v2, v6 offset1:32
	ds_write2_b32 v22, v3, v7 offset0:129 offset1:161
	ds_write2_b32 v24, v4, v8 offset0:2 offset1:34
	ds_write2_b32 v24, v5, v9 offset0:131 offset1:163
	s_waitcnt vmcnt(0)
	ds_write2_b32 v22, v14, v18 offset0:64 offset1:96
	ds_write2_b32 v22, v15, v19 offset0:193 offset1:225
	ds_write2_b32 v24, v16, v20 offset0:66 offset1:98
	ds_write2_b32 v24, v17, v21 offset0:195 offset1:227
	s_waitcnt lgkmcnt(0)
	s_barrier
	ds_read2_b32 v[2:3], v1 offset1:1
	ds_read2_b32 v[4:5], v1 offset0:2 offset1:3
	ds_read2_b32 v[6:7], v1 offset0:4 offset1:5
	ds_read2_b32 v[8:9], v1 offset0:6 offset1:7
	ds_read2_b32 v[14:15], v1 offset0:8 offset1:9
	ds_read2_b32 v[16:17], v1 offset0:10 offset1:11
	ds_read2_b32 v[18:19], v1 offset0:12 offset1:13
	ds_read2_b32 v[20:21], v1 offset0:14 offset1:15
	s_waitcnt lgkmcnt(7)
	v_cvt_pk_bf16_f32 v2, v2, v3
	s_waitcnt lgkmcnt(6)
	v_cvt_pk_bf16_f32 v3, v4, v5
	s_waitcnt lgkmcnt(5)
	v_cvt_pk_bf16_f32 v4, v6, v7
	s_waitcnt lgkmcnt(4)
	v_cvt_pk_bf16_f32 v5, v8, v9
	s_waitcnt lgkmcnt(3)
	v_cvt_pk_bf16_f32 v6, v14, v15
	s_waitcnt lgkmcnt(2)
	v_cvt_pk_bf16_f32 v7, v16, v17
	s_waitcnt lgkmcnt(1)
	v_cvt_pk_bf16_f32 v8, v18, v19
	s_waitcnt lgkmcnt(0)
	v_cvt_pk_bf16_f32 v9, v20, v21
.LBB0_1027:
	s_andn2_b64 vcc, exec, s[10:11]
	s_cbranch_vccnz .LBB0_1007
	s_mul_i32 s10, s8, 0xba2f
	s_lshr_b32 s10, s10, 25
	s_mul_i32 s11, s10, 0xfffffd40
	s_add_i32 s11, s11, s8
	s_mul_i32 s12, s11, 0xba3
	s_lshr_b32 s13, s12, 31
	s_ashr_i32 s12, s12, 20
	s_add_i32 s12, s12, s13
	s_sext_i32_i16 s13, s12
	s_mul_i32 s12, s13, 0xfffffea0
	s_add_i32 s27, s12, s11
	s_add_i32 s10, s15, s10
	s_addk_i32 s11, 0x15f
	s_cmpk_lt_u32 s11, 0x2bf
	s_cselect_b32 s12, s56, s58
	s_mul_i32 s15, s10, 0xb00000
	s_cselect_b32 s11, s57, s59
	s_add_u32 s28, s12, s15
	s_addc_u32 s11, s11, 0
	s_lshl_b32 s10, s27, 2
	s_lshl_b32 s27, s27, 3
	s_and_b32 s27, s27, 0xffffff00
	s_lshl_b32 s13, s13, 7
	s_and_b32 s12, s10, 0xffffffc0
	s_add_i32 s27, s27, s13
	s_and_b32 s10, s10, 64
	s_or_b32 s10, s27, s10
	s_add_u32 s15, s17, s15
	s_addc_u32 s27, s18, 0
	s_lshl_b32 s8, s8, 7
	s_and_b32 s8, s8, 0x780
	s_mul_i32 s13, s8, 0x1600
	s_add_u32 s28, s28, s13
	s_addc_u32 s11, s11, 0
	s_ashr_i32 s13, s12, 31
	v_mov_b32_e32 v1, v0
	s_lshl_b64 s[12:13], s[12:13], 2
	s_add_u32 s12, s28, s12
	v_lshlrev_b32_e32 v2, 2, v1
	v_and_b32_e32 v22, 60, v2
	s_addc_u32 s13, s11, s13
	v_ashrrev_i32_e32 v21, 4, v1
	v_lshlrev_b32_e32 v10, 2, v22
	v_lshl_add_u64 v[12:13], s[12:13], 0, v[10:11]
	v_add_u32_e32 v10, 64, v21
	v_add_u32_e32 v4, 32, v21
	v_mad_i64_i32 v[14:15], s[12:13], v10, s26, v[12:13]
	v_add_u32_e32 v10, 0x60, v21
	v_mad_i64_i32 v[2:3], s[12:13], v21, s26, v[12:13]
	v_mad_i64_i32 v[6:7], s[12:13], v4, s26, v[12:13]
	v_mad_i64_i32 v[16:17], s[12:13], v10, s26, v[12:13]
	global_load_dwordx4 v[2:5], v[2:3], off nt
	s_nop 0
	global_load_dwordx4 v[6:9], v[6:7], off nt
	s_nop 0
	global_load_dwordx4 v[12:15], v[14:15], off nt
	s_nop 0
	global_load_dwordx4 v[16:19], v[16:17], off nt
	v_ashrrev_i32_e32 v20, 3, v1
	v_lshlrev_b32_e32 v1, 4, v1
	v_lshlrev_b32_e32 v10, 2, v21
	v_mul_u32_u24_e32 v22, 0x204, v22
	v_add3_u32 v22, 0, v10, v22
	v_and_b32_e32 v10, 0x70, v1
	v_mul_lo_u32 v23, v20, s23
	s_ashr_i32 s11, s10, 31
	v_lshlrev_b32_e32 v1, 2, v10
	s_lshl_b64 s[10:11], s[10:11], 12
	v_add3_u32 v1, 0, v23, v1
	v_add_u32_e32 v24, 0x400, v22
	s_add_u32 s10, s15, s10
	s_waitcnt vmcnt(63) expcnt(7) lgkmcnt(15)
	s_barrier
	s_addc_u32 s11, s27, s11
	s_lshl_b32 s8, s8, 1
	v_ashrrev_i32_e32 v21, 31, v20
	s_add_u32 s10, s10, s8
	v_lshlrev_b64 v[20:21], 12, v[20:21]
	s_addc_u32 s11, s11, 0
	s_waitcnt vmcnt(2)
	ds_write2_b32 v22, v2, v6 offset1:32
	ds_write2_b32 v22, v3, v7 offset0:129 offset1:161
	ds_write2_b32 v24, v4, v8 offset0:2 offset1:34
	ds_write2_b32 v24, v5, v9 offset0:131 offset1:163
	s_waitcnt vmcnt(0)
	ds_write2_b32 v22, v12, v16 offset0:64 offset1:96
	ds_write2_b32 v22, v13, v17 offset0:193 offset1:225
	ds_write2_b32 v24, v14, v18 offset0:66 offset1:98
	ds_write2_b32 v24, v15, v19 offset0:195 offset1:227
	s_waitcnt lgkmcnt(0)
	s_barrier
	ds_read2_b32 v[2:3], v1 offset1:1
	ds_read2_b32 v[4:5], v1 offset0:2 offset1:3
	ds_read2_b32 v[6:7], v1 offset0:4 offset1:5
	ds_read2_b32 v[8:9], v1 offset0:6 offset1:7
	ds_read2_b32 v[12:13], v1 offset0:8 offset1:9
	ds_read2_b32 v[14:15], v1 offset0:10 offset1:11
	ds_read2_b32 v[16:17], v1 offset0:12 offset1:13
	ds_read2_b32 v[18:19], v1 offset0:14 offset1:15
	s_waitcnt lgkmcnt(7)
	v_cvt_pk_bf16_f32 v2, v2, v3
	s_waitcnt lgkmcnt(6)
	v_cvt_pk_bf16_f32 v3, v4, v5
	s_waitcnt lgkmcnt(5)
	v_cvt_pk_bf16_f32 v4, v6, v7
	s_waitcnt lgkmcnt(3)
	v_cvt_pk_bf16_f32 v6, v12, v13
	v_lshl_add_u64 v[12:13], s[10:11], 0, v[20:21]
	v_cvt_pk_bf16_f32 v5, v8, v9
	s_waitcnt lgkmcnt(2)
	v_cvt_pk_bf16_f32 v7, v14, v15
	s_waitcnt lgkmcnt(1)
	v_cvt_pk_bf16_f32 v8, v16, v17
	s_waitcnt lgkmcnt(0)
	v_cvt_pk_bf16_f32 v9, v18, v19
	s_branch .LBB0_1007

.LBB0_1120:
	s_or_b64 exec, exec, s[24:25]
	s_waitcnt lgkmcnt(0)
	s_barrier
	ds_read_b32 v1, v11 offset:40960
	s_mov_b64 s[24:25], -1
	s_waitcnt lgkmcnt(0)
	v_cmp_lt_u32_e32 vcc, s34, v1
	v_readfirstlane_b32 s28, v1
	s_cbranch_vccnz .LBB0_1113
	s_cmpk_lt_u32 s28, 0x4a00
	s_cbranch_scc0 .LBB0_1129
	s_cmpk_gt_u32 s28, 0x41ff
	s_cbranch_scc0 .LBB0_1128
	s_cmpk_gt_u32 s28, 0x47ff
	s_cbranch_scc0 .LBB0_1125
	s_add_i32 s22, s28, 0xffffb800
	s_lshr_b32 s26, s22, 4
	s_lshl_b32 s24, s26, 11
	s_lshl_b32 s22, s22, 7
	s_sub_i32 s24, s22, s24
	s_ashr_i32 s25, s24, 31
	s_lshl_b32 s22, s26, 6
	s_lshl_b64 s[26:27], s[24:25], 13
	s_add_u32 s29, s16, s26
	v_mov_b32_e32 v1, v0
	s_addc_u32 s42, s17, s27
	s_lshl_b64 s[26:27], s[22:23], 2
	s_add_u32 s26, s29, s26
	v_lshlrev_b32_e32 v2, 2, v1
	v_ashrrev_i32_e32 v12, 4, v1
	v_and_b32_e32 v24, 60, v2
	s_addc_u32 s27, s42, s27
	v_lshlrev_b32_e32 v10, 2, v24
	v_ashrrev_i32_e32 v13, 31, v12
	v_lshl_add_u64 v[2:3], s[26:27], 0, v[10:11]
	v_lshlrev_b64 v[4:5], 13, v[12:13]
	v_lshl_add_u64 v[14:15], v[2:3], 0, v[4:5]
	v_add_co_u32_e32 v6, vcc, s35, v14
	v_ashrrev_i32_e32 v22, 3, v1
	s_nop 0
	v_addc_co_u32_e32 v7, vcc, 0, v15, vcc
	v_add_co_u32_e32 v16, vcc, s36, v14
	global_load_dwordx4 v[2:5], v[14:15], off nt
	s_nop 0
	global_load_dwordx4 v[6:9], v[6:7], off nt
	v_addc_co_u32_e32 v17, vcc, 0, v15, vcc
	v_add_co_u32_e32 v18, vcc, s37, v14
	v_lshlrev_b32_e32 v1, 4, v1
	s_nop 0
	v_addc_co_u32_e32 v19, vcc, 0, v15, vcc
	global_load_dwordx4 v[14:17], v[16:17], off nt
	s_nop 0
	global_load_dwordx4 v[18:21], v[18:19], off nt
	v_lshlrev_b32_e32 v10, 2, v12
	v_ashrrev_i32_e32 v23, 31, v22
	v_mul_u32_u24_e32 v24, 0x204, v24
	v_mul_lo_u32 v25, v22, s38
	v_lshlrev_b64 v[12:13], 12, v[22:23]
	v_add3_u32 v22, 0, v10, v24
	v_and_b32_e32 v10, 0x70, v1
	v_lshlrev_b32_e32 v1, 2, v10
	v_add3_u32 v1, 0, v25, v1
	v_add_u32_e32 v23, 0x400, v22
	s_lshl_b64 s[26:27], s[22:23], 12
	s_barrier
	s_add_u32 s22, s3, s26
	s_addc_u32 s26, s4, s27
	s_lshl_b64 s[24:25], s[24:25], 1
	s_add_u32 s24, s22, s24
	s_addc_u32 s25, s26, s25
	v_lshl_add_u64 v[12:13], s[24:25], 0, v[12:13]
	s_mov_b64 s[24:25], 0
	s_waitcnt vmcnt(2)
	ds_write2_b32 v22, v2, v6 offset1:32
	ds_write2_b32 v22, v3, v7 offset0:129 offset1:161
	ds_write2_b32 v23, v4, v8 offset0:2 offset1:34
	ds_write2_b32 v23, v5, v9 offset0:131 offset1:163
	s_waitcnt vmcnt(0)
	ds_write2_b32 v22, v14, v18 offset0:64 offset1:96
	ds_write2_b32 v22, v15, v19 offset0:193 offset1:225
	ds_write2_b32 v23, v16, v20 offset0:66 offset1:98
	ds_write2_b32 v23, v17, v21 offset0:195 offset1:227
	s_waitcnt lgkmcnt(0)
	s_barrier
	ds_read2_b32 v[2:3], v1 offset1:1
	ds_read2_b32 v[4:5], v1 offset0:2 offset1:3
	ds_read2_b32 v[6:7], v1 offset0:4 offset1:5
	ds_read2_b32 v[8:9], v1 offset0:6 offset1:7
	ds_read2_b32 v[14:15], v1 offset0:8 offset1:9
	ds_read2_b32 v[16:17], v1 offset0:10 offset1:11
	ds_read2_b32 v[18:19], v1 offset0:12 offset1:13
	ds_read2_b32 v[20:21], v1 offset0:14 offset1:15
	s_waitcnt lgkmcnt(7)
	v_cvt_pk_bf16_f32 v2, v2, v3
	s_waitcnt lgkmcnt(6)
	v_cvt_pk_bf16_f32 v3, v4, v5
	s_waitcnt lgkmcnt(5)
	v_cvt_pk_bf16_f32 v4, v6, v7
	s_waitcnt lgkmcnt(4)
	v_cvt_pk_bf16_f32 v5, v8, v9
	s_waitcnt lgkmcnt(3)
	v_cvt_pk_bf16_f32 v6, v14, v15
	s_waitcnt lgkmcnt(2)
	v_cvt_pk_bf16_f32 v7, v16, v17
	s_waitcnt lgkmcnt(1)
	v_cvt_pk_bf16_f32 v8, v18, v19
	s_waitcnt lgkmcnt(0)
	v_cvt_pk_bf16_f32 v9, v20, v21
.LBB0_1125:
	s_andn2_b64 vcc, exec, s[24:25]
	s_cbranch_vccnz .LBB0_1127
	s_add_i32 s22, s28, 0xffffbe00
	s_lshr_b32 s26, s22, 4
	s_lshl_b32 s24, s26, 11
	s_lshl_b32 s22, s22, 7
	s_sub_i32 s24, s22, s24
	s_ashr_i32 s25, s24, 31
	s_lshl_b32 s22, s26, 6
	s_mul_i32 s27, s24, 0x6000
	s_mul_hi_i32 s26, s24, 0x6000
	s_add_u32 s29, s14, s27
	v_mov_b32_e32 v1, v0
	s_addc_u32 s42, s15, s26
	s_lshl_b64 s[26:27], s[22:23], 2
	s_add_u32 s26, s29, s26
	v_lshlrev_b32_e32 v2, 2, v1
	v_and_b32_e32 v22, 60, v2
	s_addc_u32 s27, s42, s27
	v_ashrrev_i32_e32 v21, 4, v1
	v_lshlrev_b32_e32 v10, 2, v22
	v_lshl_add_u64 v[12:13], s[26:27], 0, v[10:11]
	v_add_u32_e32 v10, 64, v21
	v_add_u32_e32 v4, 32, v21
	v_mad_i64_i32 v[14:15], s[26:27], v10, s39, v[12:13]
	v_add_u32_e32 v10, 0x60, v21
	v_mad_i64_i32 v[2:3], s[26:27], v21, s39, v[12:13]
	v_mad_i64_i32 v[6:7], s[26:27], v4, s39, v[12:13]
	v_mad_i64_i32 v[16:17], s[26:27], v10, s39, v[12:13]
	global_load_dwordx4 v[2:5], v[2:3], off nt
	s_nop 0
	global_load_dwordx4 v[6:9], v[6:7], off nt
	s_nop 0
	global_load_dwordx4 v[12:15], v[14:15], off nt
	s_nop 0
	global_load_dwordx4 v[16:19], v[16:17], off nt
	v_ashrrev_i32_e32 v20, 3, v1
	v_lshlrev_b32_e32 v1, 4, v1
	v_lshlrev_b32_e32 v10, 2, v21
	v_mul_u32_u24_e32 v22, 0x204, v22
	v_add3_u32 v22, 0, v10, v22
	v_and_b32_e32 v10, 0x70, v1
	v_mul_lo_u32 v23, v20, s38
	v_lshlrev_b32_e32 v1, 2, v10
	s_lshl_b64 s[26:27], s[22:23], 12
	v_add3_u32 v1, 0, v23, v1
	v_add_u32_e32 v24, 0x400, v22
	s_add_u32 s22, s5, s26
	s_barrier
	s_addc_u32 s26, s30, s27
	s_lshl_b64 s[24:25], s[24:25], 1
	v_ashrrev_i32_e32 v21, 31, v20
	s_add_u32 s24, s22, s24
	v_lshlrev_b64 v[20:21], 12, v[20:21]
	s_addc_u32 s25, s26, s25
	s_waitcnt vmcnt(2)
	ds_write2_b32 v22, v2, v6 offset1:32
	ds_write2_b32 v22, v3, v7 offset0:129 offset1:161
	ds_write2_b32 v24, v4, v8 offset0:2 offset1:34
	ds_write2_b32 v24, v5, v9 offset0:131 offset1:163
	s_waitcnt vmcnt(0)
	ds_write2_b32 v22, v12, v16 offset0:64 offset1:96
	ds_write2_b32 v22, v13, v17 offset0:193 offset1:225
	ds_write2_b32 v24, v14, v18 offset0:66 offset1:98
	ds_write2_b32 v24, v15, v19 offset0:195 offset1:227
	s_waitcnt lgkmcnt(0)
	s_barrier
	ds_read2_b32 v[2:3], v1 offset1:1
	ds_read2_b32 v[4:5], v1 offset0:2 offset1:3
	ds_read2_b32 v[6:7], v1 offset0:4 offset1:5
	ds_read2_b32 v[8:9], v1 offset0:6 offset1:7
	ds_read2_b32 v[12:13], v1 offset0:8 offset1:9
	ds_read2_b32 v[14:15], v1 offset0:10 offset1:11
	ds_read2_b32 v[16:17], v1 offset0:12 offset1:13
	ds_read2_b32 v[18:19], v1 offset0:14 offset1:15
	s_waitcnt lgkmcnt(7)
	v_cvt_pk_bf16_f32 v2, v2, v3
	s_waitcnt lgkmcnt(6)
	v_cvt_pk_bf16_f32 v3, v4, v5
	s_waitcnt lgkmcnt(5)
	v_cvt_pk_bf16_f32 v4, v6, v7
	s_waitcnt lgkmcnt(3)
	v_cvt_pk_bf16_f32 v6, v12, v13
	v_lshl_add_u64 v[12:13], s[24:25], 0, v[20:21]
	v_cvt_pk_bf16_f32 v5, v8, v9
	s_waitcnt lgkmcnt(2)
	v_cvt_pk_bf16_f32 v7, v14, v15
	s_waitcnt lgkmcnt(1)
	v_cvt_pk_bf16_f32 v8, v16, v17
	s_waitcnt lgkmcnt(0)
	v_cvt_pk_bf16_f32 v9, v18, v19

.LBB0_1131:
	s_andn2_b64 vcc, exec, s[24:25]
	s_cbranch_vccnz .LBB0_1112
	s_cmpk_gt_u32 s28, 0x2bff
	s_mov_b64 s[24:25], -1
	s_cbranch_scc0 .LBB0_1134
	s_add_i32 s24, s28, 0xffffd400
	s_mul_i32 s25, s24, 0xba2f
	s_lshr_b32 s25, s25, 24
	s_mul_i32 s26, s25, 0xfffffea0
	s_add_i32 s25, s22, s25
	s_add_i32 s24, s26, s24
	s_mul_i32 s27, s25, 0xb00000
	s_mul_hi_u32 s26, s25, 0xb00000
	s_add_u32 s29, s18, s27
	s_addc_u32 s44, s19, s26
	s_mul_i32 s25, s25, 0x580000
	s_add_u32 s45, s31, s25
	s_mul_i32 s25, s24, 0x1746
	s_addc_u32 s46, s33, 0
	s_lshr_b32 s26, s25, 31
	s_lshr_b32 s25, s25, 16
	s_add_i32 s25, s25, s26
	s_sext_i32_i16 s47, s25
	s_mul_i32 s25, s47, -11
	s_add_i32 s25, s25, s24
	s_lshl_b32 s24, s25, 7
	s_ashr_i32 s25, s24, 31
	s_lshl_b32 s26, s47, 6
	s_ashr_i32 s27, s26, 31
	s_lshl_b64 s[42:43], s[24:25], 13
	s_add_u32 s29, s29, s42
	v_mov_b32_e32 v1, v0
	s_addc_u32 s44, s44, s43
	s_lshl_b64 s[42:43], s[26:27], 2
	s_add_u32 s42, s29, s42
	v_lshlrev_b32_e32 v2, 2, v1
	v_ashrrev_i32_e32 v12, 4, v1
	v_and_b32_e32 v22, 60, v2
	s_addc_u32 s43, s44, s43
	v_lshlrev_b32_e32 v10, 2, v22
	v_ashrrev_i32_e32 v13, 31, v12
	v_lshl_add_u64 v[2:3], s[42:43], 0, v[10:11]
	v_lshlrev_b64 v[4:5], 13, v[12:13]
	v_lshl_add_u64 v[14:15], v[2:3], 0, v[4:5]
	v_add_co_u32_e32 v6, vcc, s35, v14
	v_ashrrev_i32_e32 v23, 3, v1
	s_nop 0
	v_addc_co_u32_e32 v7, vcc, 0, v15, vcc
	v_add_co_u32_e32 v16, vcc, s36, v14
	global_load_dwordx4 v[2:5], v[14:15], off nt
	s_nop 0
	global_load_dwordx4 v[6:9], v[6:7], off nt
	v_addc_co_u32_e32 v17, vcc, 0, v15, vcc
	v_add_co_u32_e32 v18, vcc, s37, v14
	v_lshlrev_b32_e32 v1, 4, v1
	s_nop 0
	v_addc_co_u32_e32 v19, vcc, 0, v15, vcc
	global_load_dwordx4 v[14:17], v[16:17], off nt
	s_nop 0
	global_load_dwordx4 v[18:21], v[18:19], off nt
	v_lshlrev_b32_e32 v10, 2, v12
	v_mul_u32_u24_e32 v13, 0x204, v22
	v_add3_u32 v22, 0, v10, v13
	v_and_b32_e32 v10, 0x70, v1
	v_mul_lo_u32 v12, v23, s38
	s_mul_i32 s47, s47, 0x2c000
	v_lshlrev_b32_e32 v1, 2, v10
	s_mul_hi_i32 s26, s26, 0xb00
	s_add_u32 s27, s45, s47
	v_add3_u32 v1, 0, v12, v1
	v_add_u32_e32 v24, 0x400, v22
	s_addc_u32 s26, s46, s26
	s_lshl_b64 s[24:25], s[24:25], 1
	s_barrier
	s_add_u32 s24, s27, s24
	s_addc_u32 s25, s26, s25
	v_mov_b64_e32 v[12:13], s[24:25]
	v_mad_i64_i32 v[12:13], s[24:25], v23, s40, v[12:13]
	s_mov_b64 s[24:25], 0
	s_waitcnt vmcnt(2)
	ds_write2_b32 v22, v2, v6 offset1:32
	ds_write2_b32 v22, v3, v7 offset0:129 offset1:161
	ds_write2_b32 v24, v4, v8 offset0:2 offset1:34
	ds_write2_b32 v24, v5, v9 offset0:131 offset1:163
	s_waitcnt vmcnt(0)
	ds_write2_b32 v22, v14, v18 offset0:64 offset1:96
	ds_write2_b32 v22, v15, v19 offset0:193 offset1:225
	ds_write2_b32 v24, v16, v20 offset0:66 offset1:98
	ds_write2_b32 v24, v17, v21 offset0:195 offset1:227
	s_waitcnt lgkmcnt(0)
	s_barrier
	ds_read2_b32 v[2:3], v1 offset1:1
	ds_read2_b32 v[4:5], v1 offset0:2 offset1:3
	ds_read2_b32 v[6:7], v1 offset0:4 offset1:5
	ds_read2_b32 v[8:9], v1 offset0:6 offset1:7
	ds_read2_b32 v[14:15], v1 offset0:8 offset1:9
	ds_read2_b32 v[16:17], v1 offset0:10 offset1:11
	ds_read2_b32 v[18:19], v1 offset0:12 offset1:13
	ds_read2_b32 v[20:21], v1 offset0:14 offset1:15
	s_waitcnt lgkmcnt(7)
	v_cvt_pk_bf16_f32 v2, v2, v3
	s_waitcnt lgkmcnt(6)
	v_cvt_pk_bf16_f32 v3, v4, v5
	s_waitcnt lgkmcnt(5)
	v_cvt_pk_bf16_f32 v4, v6, v7
	s_waitcnt lgkmcnt(4)
	v_cvt_pk_bf16_f32 v5, v8, v9
	s_waitcnt lgkmcnt(3)
	v_cvt_pk_bf16_f32 v6, v14, v15
	s_waitcnt lgkmcnt(2)
	v_cvt_pk_bf16_f32 v7, v16, v17
	s_waitcnt lgkmcnt(1)
	v_cvt_pk_bf16_f32 v8, v18, v19
	s_waitcnt lgkmcnt(0)
	v_cvt_pk_bf16_f32 v9, v20, v21
.LBB0_1134:
	s_andn2_b64 vcc, exec, s[24:25]
	s_cbranch_vccnz .LBB0_1112
	s_mul_i32 s24, s28, 0xba2f
	s_lshr_b32 s24, s24, 25
	s_mul_i32 s25, s24, 0xfffffd40
	s_add_i32 s25, s25, s28
	s_mul_i32 s26, s25, 0xba3
	s_lshr_b32 s27, s26, 31
	s_ashr_i32 s26, s26, 20
	s_add_i32 s26, s26, s27
	s_sext_i32_i16 s27, s26
	s_mul_i32 s26, s27, 0xfffffea0
	s_add_i32 s29, s26, s25
	s_add_i32 s22, s22, s24
	s_addk_i32 s25, 0x15f
	s_cmpk_lt_u32 s25, 0x2bf
	s_cselect_b32 s25, s8, s10
	s_mul_i32 s22, s22, 0xb00000
	s_cselect_b32 s24, s9, s11
	s_add_u32 s25, s25, s22
	s_addc_u32 s42, s24, 0
	s_lshl_b32 s24, s29, 2
	s_lshl_b32 s29, s29, 3
	s_and_b32 s29, s29, 0xffffff00
	s_lshl_b32 s27, s27, 7
	s_and_b32 s26, s24, 0xffffffc0
	s_add_i32 s29, s29, s27
	s_and_b32 s24, s24, 64
	s_or_b32 s24, s29, s24
	s_add_u32 s22, s0, s22
	s_addc_u32 s29, s1, 0
	s_lshl_b32 s27, s28, 7
	s_and_b32 s28, s27, 0x780
	s_mul_i32 s27, s28, 0x1600
	s_add_u32 s25, s25, s27
	s_addc_u32 s42, s42, 0
	s_ashr_i32 s27, s26, 31
	v_mov_b32_e32 v1, v0
	s_lshl_b64 s[26:27], s[26:27], 2
	s_add_u32 s26, s25, s26
	v_lshlrev_b32_e32 v2, 2, v1
	v_and_b32_e32 v22, 60, v2
	s_addc_u32 s27, s42, s27
	v_ashrrev_i32_e32 v21, 4, v1
	v_lshlrev_b32_e32 v10, 2, v22
	v_lshl_add_u64 v[12:13], s[26:27], 0, v[10:11]
	v_add_u32_e32 v10, 64, v21
	v_add_u32_e32 v4, 32, v21
	v_mad_i64_i32 v[14:15], s[26:27], v10, s41, v[12:13]
	v_add_u32_e32 v10, 0x60, v21
	v_mad_i64_i32 v[2:3], s[26:27], v21, s41, v[12:13]
	v_mad_i64_i32 v[6:7], s[26:27], v4, s41, v[12:13]
	v_mad_i64_i32 v[16:17], s[26:27], v10, s41, v[12:13]
	global_load_dwordx4 v[2:5], v[2:3], off nt
	s_nop 0
	global_load_dwordx4 v[6:9], v[6:7], off nt
	s_nop 0
	global_load_dwordx4 v[12:15], v[14:15], off nt
	s_nop 0
	global_load_dwordx4 v[16:19], v[16:17], off nt
	v_ashrrev_i32_e32 v20, 3, v1
	v_lshlrev_b32_e32 v1, 4, v1
	v_lshlrev_b32_e32 v10, 2, v21
	v_mul_u32_u24_e32 v22, 0x204, v22
	v_add3_u32 v22, 0, v10, v22
	v_and_b32_e32 v10, 0x70, v1
	v_mul_lo_u32 v23, v20, s38
	s_ashr_i32 s25, s24, 31
	v_lshlrev_b32_e32 v1, 2, v10
	s_lshl_b64 s[24:25], s[24:25], 12
	v_add3_u32 v1, 0, v23, v1
	v_add_u32_e32 v24, 0x400, v22
	s_add_u32 s22, s22, s24
	s_barrier
	s_addc_u32 s25, s29, s25
	s_lshl_b32 s24, s28, 1
	v_ashrrev_i32_e32 v21, 31, v20
	s_add_u32 s24, s22, s24
	v_lshlrev_b64 v[20:21], 12, v[20:21]
	s_addc_u32 s25, s25, 0
	s_waitcnt vmcnt(2)
	ds_write2_b32 v22, v2, v6 offset1:32
	ds_write2_b32 v22, v3, v7 offset0:129 offset1:161
	ds_write2_b32 v24, v4, v8 offset0:2 offset1:34
	ds_write2_b32 v24, v5, v9 offset0:131 offset1:163
	s_waitcnt vmcnt(0)
	ds_write2_b32 v22, v12, v16 offset0:64 offset1:96
	ds_write2_b32 v22, v13, v17 offset0:193 offset1:225
	ds_write2_b32 v24, v14, v18 offset0:66 offset1:98
	ds_write2_b32 v24, v15, v19 offset0:195 offset1:227
	s_waitcnt lgkmcnt(0)
	s_barrier
	ds_read2_b32 v[2:3], v1 offset1:1
	ds_read2_b32 v[4:5], v1 offset0:2 offset1:3
	ds_read2_b32 v[6:7], v1 offset0:4 offset1:5
	ds_read2_b32 v[8:9], v1 offset0:6 offset1:7
	ds_read2_b32 v[12:13], v1 offset0:8 offset1:9
	ds_read2_b32 v[14:15], v1 offset0:10 offset1:11
	ds_read2_b32 v[16:17], v1 offset0:12 offset1:13
	ds_read2_b32 v[18:19], v1 offset0:14 offset1:15
	s_waitcnt lgkmcnt(7)
	v_cvt_pk_bf16_f32 v2, v2, v3
	s_waitcnt lgkmcnt(6)
	v_cvt_pk_bf16_f32 v3, v4, v5
	s_waitcnt lgkmcnt(5)
	v_cvt_pk_bf16_f32 v4, v6, v7
	s_waitcnt lgkmcnt(3)
	v_cvt_pk_bf16_f32 v6, v12, v13
	v_lshl_add_u64 v[12:13], s[24:25], 0, v[20:21]
	v_cvt_pk_bf16_f32 v5, v8, v9
	s_waitcnt lgkmcnt(2)
	v_cvt_pk_bf16_f32 v7, v14, v15
	s_waitcnt lgkmcnt(1)
	v_cvt_pk_bf16_f32 v8, v16, v17
	s_waitcnt lgkmcnt(0)
	v_cvt_pk_bf16_f32 v9, v18, v19
	s_branch .LBB0_1112

.LBB0_1229:
	s_or_b64 exec, exec, s[24:25]
	s_waitcnt lgkmcnt(0)
	s_barrier
	ds_read_b32 v1, v11 offset:40960
	s_mov_b64 s[24:25], -1
	s_waitcnt lgkmcnt(0)
	v_cmp_lt_u32_e32 vcc, s34, v1
	v_readfirstlane_b32 s28, v1
	s_cbranch_vccnz .LBB0_1222
	s_cmpk_lt_u32 s28, 0x4a00
	s_cbranch_scc0 .LBB0_1238
	s_cmpk_gt_u32 s28, 0x41ff
	s_cbranch_scc0 .LBB0_1237
	s_cmpk_gt_u32 s28, 0x47ff
	s_cbranch_scc0 .LBB0_1234
	s_add_i32 s22, s28, 0xffffb800
	s_lshr_b32 s26, s22, 4
	s_lshl_b32 s24, s26, 11
	s_lshl_b32 s22, s22, 7
	s_sub_i32 s24, s22, s24
	s_ashr_i32 s25, s24, 31
	s_lshl_b32 s22, s26, 6
	s_lshl_b64 s[26:27], s[24:25], 13
	s_add_u32 s29, s16, s26
	v_mov_b32_e32 v1, v0
	s_addc_u32 s42, s17, s27
	s_lshl_b64 s[26:27], s[22:23], 2
	s_add_u32 s26, s29, s26
	v_lshlrev_b32_e32 v2, 2, v1
	v_ashrrev_i32_e32 v12, 4, v1
	v_and_b32_e32 v24, 60, v2
	s_addc_u32 s27, s42, s27
	v_lshlrev_b32_e32 v10, 2, v24
	v_ashrrev_i32_e32 v13, 31, v12
	v_lshl_add_u64 v[2:3], s[26:27], 0, v[10:11]
	v_lshlrev_b64 v[4:5], 13, v[12:13]
	v_lshl_add_u64 v[14:15], v[2:3], 0, v[4:5]
	v_add_co_u32_e32 v6, vcc, s35, v14
	v_ashrrev_i32_e32 v22, 3, v1
	s_nop 0
	v_addc_co_u32_e32 v7, vcc, 0, v15, vcc
	v_add_co_u32_e32 v16, vcc, s36, v14
	global_load_dwordx4 v[2:5], v[14:15], off nt
	s_nop 0
	global_load_dwordx4 v[6:9], v[6:7], off nt
	v_addc_co_u32_e32 v17, vcc, 0, v15, vcc
	v_add_co_u32_e32 v18, vcc, s37, v14
	v_lshlrev_b32_e32 v1, 4, v1
	s_nop 0
	v_addc_co_u32_e32 v19, vcc, 0, v15, vcc
	global_load_dwordx4 v[14:17], v[16:17], off nt
	s_nop 0
	global_load_dwordx4 v[18:21], v[18:19], off nt
	v_lshlrev_b32_e32 v10, 2, v12
	v_ashrrev_i32_e32 v23, 31, v22
	v_mul_u32_u24_e32 v24, 0x204, v24
	v_mul_lo_u32 v25, v22, s38
	v_lshlrev_b64 v[12:13], 12, v[22:23]
	v_add3_u32 v22, 0, v10, v24
	v_and_b32_e32 v10, 0x70, v1
	v_lshlrev_b32_e32 v1, 2, v10
	v_add3_u32 v1, 0, v25, v1
	v_add_u32_e32 v23, 0x400, v22
	s_lshl_b64 s[26:27], s[22:23], 12
	s_waitcnt vmcnt(63) expcnt(7) lgkmcnt(15)
	s_barrier
	s_add_u32 s22, s3, s26
	s_addc_u32 s26, s4, s27
	s_lshl_b64 s[24:25], s[24:25], 1
	s_add_u32 s24, s22, s24
	s_addc_u32 s25, s26, s25
	v_lshl_add_u64 v[12:13], s[24:25], 0, v[12:13]
	s_mov_b64 s[24:25], 0
	s_waitcnt vmcnt(2)
	ds_write2_b32 v22, v2, v6 offset1:32
	ds_write2_b32 v22, v3, v7 offset0:129 offset1:161
	ds_write2_b32 v23, v4, v8 offset0:2 offset1:34
	ds_write2_b32 v23, v5, v9 offset0:131 offset1:163
	s_waitcnt vmcnt(0)
	ds_write2_b32 v22, v14, v18 offset0:64 offset1:96
	ds_write2_b32 v22, v15, v19 offset0:193 offset1:225
	ds_write2_b32 v23, v16, v20 offset0:66 offset1:98
	ds_write2_b32 v23, v17, v21 offset0:195 offset1:227
	s_waitcnt lgkmcnt(0)
	s_barrier
	ds_read2_b32 v[2:3], v1 offset1:1
	ds_read2_b32 v[4:5], v1 offset0:2 offset1:3
	ds_read2_b32 v[6:7], v1 offset0:4 offset1:5
	ds_read2_b32 v[8:9], v1 offset0:6 offset1:7
	ds_read2_b32 v[14:15], v1 offset0:8 offset1:9
	ds_read2_b32 v[16:17], v1 offset0:10 offset1:11
	ds_read2_b32 v[18:19], v1 offset0:12 offset1:13
	ds_read2_b32 v[20:21], v1 offset0:14 offset1:15
	s_waitcnt lgkmcnt(7)
	v_cvt_pk_bf16_f32 v2, v2, v3
	s_waitcnt lgkmcnt(6)
	v_cvt_pk_bf16_f32 v3, v4, v5
	s_waitcnt lgkmcnt(5)
	v_cvt_pk_bf16_f32 v4, v6, v7
	s_waitcnt lgkmcnt(4)
	v_cvt_pk_bf16_f32 v5, v8, v9
	s_waitcnt lgkmcnt(3)
	v_cvt_pk_bf16_f32 v6, v14, v15
	s_waitcnt lgkmcnt(2)
	v_cvt_pk_bf16_f32 v7, v16, v17
	s_waitcnt lgkmcnt(1)
	v_cvt_pk_bf16_f32 v8, v18, v19
	s_waitcnt lgkmcnt(0)
	v_cvt_pk_bf16_f32 v9, v20, v21
.LBB0_1234:
	s_andn2_b64 vcc, exec, s[24:25]
	s_cbranch_vccnz .LBB0_1236
	s_add_i32 s22, s28, 0xffffbe00
	s_lshr_b32 s26, s22, 4
	s_lshl_b32 s24, s26, 11
	s_lshl_b32 s22, s22, 7
	s_sub_i32 s24, s22, s24
	s_ashr_i32 s25, s24, 31
	s_lshl_b32 s22, s26, 6
	s_mul_i32 s27, s24, 0x6000
	s_mul_hi_i32 s26, s24, 0x6000
	s_add_u32 s29, s14, s27
	v_mov_b32_e32 v1, v0
	s_addc_u32 s42, s15, s26
	s_lshl_b64 s[26:27], s[22:23], 2
	s_add_u32 s26, s29, s26
	v_lshlrev_b32_e32 v2, 2, v1
	v_and_b32_e32 v22, 60, v2
	s_addc_u32 s27, s42, s27
	v_ashrrev_i32_e32 v21, 4, v1
	v_lshlrev_b32_e32 v10, 2, v22
	v_lshl_add_u64 v[12:13], s[26:27], 0, v[10:11]
	v_add_u32_e32 v10, 64, v21
	v_add_u32_e32 v4, 32, v21
	v_mad_i64_i32 v[14:15], s[26:27], v10, s39, v[12:13]
	v_add_u32_e32 v10, 0x60, v21
	v_mad_i64_i32 v[2:3], s[26:27], v21, s39, v[12:13]
	v_mad_i64_i32 v[6:7], s[26:27], v4, s39, v[12:13]
	v_mad_i64_i32 v[16:17], s[26:27], v10, s39, v[12:13]
	global_load_dwordx4 v[2:5], v[2:3], off nt
	s_nop 0
	global_load_dwordx4 v[6:9], v[6:7], off nt
	s_nop 0
	global_load_dwordx4 v[12:15], v[14:15], off nt
	s_nop 0
	global_load_dwordx4 v[16:19], v[16:17], off nt
	v_ashrrev_i32_e32 v20, 3, v1
	v_lshlrev_b32_e32 v1, 4, v1
	v_lshlrev_b32_e32 v10, 2, v21
	v_mul_u32_u24_e32 v22, 0x204, v22
	v_add3_u32 v22, 0, v10, v22
	v_and_b32_e32 v10, 0x70, v1
	v_mul_lo_u32 v23, v20, s38
	v_lshlrev_b32_e32 v1, 2, v10
	s_lshl_b64 s[26:27], s[22:23], 12
	v_add3_u32 v1, 0, v23, v1
	v_add_u32_e32 v24, 0x400, v22
	s_add_u32 s22, s5, s26
	s_waitcnt vmcnt(63) expcnt(7) lgkmcnt(15)
	s_barrier
	s_addc_u32 s26, s30, s27
	s_lshl_b64 s[24:25], s[24:25], 1
	v_ashrrev_i32_e32 v21, 31, v20
	s_add_u32 s24, s22, s24
	v_lshlrev_b64 v[20:21], 12, v[20:21]
	s_addc_u32 s25, s26, s25
	s_waitcnt vmcnt(2)
	ds_write2_b32 v22, v2, v6 offset1:32
	ds_write2_b32 v22, v3, v7 offset0:129 offset1:161
	ds_write2_b32 v24, v4, v8 offset0:2 offset1:34
	ds_write2_b32 v24, v5, v9 offset0:131 offset1:163
	s_waitcnt vmcnt(0)
	ds_write2_b32 v22, v12, v16 offset0:64 offset1:96
	ds_write2_b32 v22, v13, v17 offset0:193 offset1:225
	ds_write2_b32 v24, v14, v18 offset0:66 offset1:98
	ds_write2_b32 v24, v15, v19 offset0:195 offset1:227
	s_waitcnt lgkmcnt(0)
	s_barrier
	ds_read2_b32 v[2:3], v1 offset1:1
	ds_read2_b32 v[4:5], v1 offset0:2 offset1:3
	ds_read2_b32 v[6:7], v1 offset0:4 offset1:5
	ds_read2_b32 v[8:9], v1 offset0:6 offset1:7
	ds_read2_b32 v[12:13], v1 offset0:8 offset1:9
	ds_read2_b32 v[14:15], v1 offset0:10 offset1:11
	ds_read2_b32 v[16:17], v1 offset0:12 offset1:13
	ds_read2_b32 v[18:19], v1 offset0:14 offset1:15
	s_waitcnt lgkmcnt(7)
	v_cvt_pk_bf16_f32 v2, v2, v3
	s_waitcnt lgkmcnt(6)
	v_cvt_pk_bf16_f32 v3, v4, v5
	s_waitcnt lgkmcnt(5)
	v_cvt_pk_bf16_f32 v4, v6, v7
	s_waitcnt lgkmcnt(3)
	v_cvt_pk_bf16_f32 v6, v12, v13
	v_lshl_add_u64 v[12:13], s[24:25], 0, v[20:21]
	v_cvt_pk_bf16_f32 v5, v8, v9
	s_waitcnt lgkmcnt(2)
	v_cvt_pk_bf16_f32 v7, v14, v15
	s_waitcnt lgkmcnt(1)
	v_cvt_pk_bf16_f32 v8, v16, v17
	s_waitcnt lgkmcnt(0)
	v_cvt_pk_bf16_f32 v9, v18, v19

.LBB0_1240:
	s_andn2_b64 vcc, exec, s[24:25]
	s_cbranch_vccnz .LBB0_1221
	s_cmpk_gt_u32 s28, 0x2bff
	s_mov_b64 s[24:25], -1
	s_cbranch_scc0 .LBB0_1243
	s_add_i32 s24, s28, 0xffffd400
	s_mul_i32 s25, s24, 0xba2f
	s_lshr_b32 s25, s25, 24
	s_mul_i32 s26, s25, 0xfffffea0
	s_add_i32 s25, s22, s25
	s_add_i32 s24, s26, s24
	s_mul_i32 s27, s25, 0xb00000
	s_mul_hi_u32 s26, s25, 0xb00000
	s_add_u32 s29, s18, s27
	s_addc_u32 s44, s19, s26
	s_mul_i32 s25, s25, 0x580000
	s_add_u32 s45, s0, s25
	s_mul_i32 s25, s24, 0x1746
	s_addc_u32 s46, s1, 0
	s_lshr_b32 s26, s25, 31
	s_lshr_b32 s25, s25, 16
	s_add_i32 s25, s25, s26
	s_sext_i32_i16 s47, s25
	s_mul_i32 s25, s47, -11
	s_add_i32 s25, s25, s24
	s_lshl_b32 s24, s25, 7
	s_ashr_i32 s25, s24, 31
	s_lshl_b32 s26, s47, 6
	s_ashr_i32 s27, s26, 31
	s_lshl_b64 s[42:43], s[24:25], 13
	s_add_u32 s29, s29, s42
	v_mov_b32_e32 v1, v0
	s_addc_u32 s44, s44, s43
	s_lshl_b64 s[42:43], s[26:27], 2
	s_add_u32 s42, s29, s42
	v_lshlrev_b32_e32 v2, 2, v1
	v_ashrrev_i32_e32 v12, 4, v1
	v_and_b32_e32 v22, 60, v2
	s_addc_u32 s43, s44, s43
	v_lshlrev_b32_e32 v10, 2, v22
	v_ashrrev_i32_e32 v13, 31, v12
	v_lshl_add_u64 v[2:3], s[42:43], 0, v[10:11]
	v_lshlrev_b64 v[4:5], 13, v[12:13]
	v_lshl_add_u64 v[14:15], v[2:3], 0, v[4:5]
	v_add_co_u32_e32 v6, vcc, s35, v14
	v_ashrrev_i32_e32 v23, 3, v1
	s_nop 0
	v_addc_co_u32_e32 v7, vcc, 0, v15, vcc
	v_add_co_u32_e32 v16, vcc, s36, v14
	global_load_dwordx4 v[2:5], v[14:15], off nt
	s_nop 0
	global_load_dwordx4 v[6:9], v[6:7], off nt
	v_addc_co_u32_e32 v17, vcc, 0, v15, vcc
	v_add_co_u32_e32 v18, vcc, s37, v14
	v_lshlrev_b32_e32 v1, 4, v1
	s_nop 0
	v_addc_co_u32_e32 v19, vcc, 0, v15, vcc
	global_load_dwordx4 v[14:17], v[16:17], off nt
	s_nop 0
	global_load_dwordx4 v[18:21], v[18:19], off nt
	v_lshlrev_b32_e32 v10, 2, v12
	v_mul_u32_u24_e32 v13, 0x204, v22
	v_add3_u32 v22, 0, v10, v13
	v_and_b32_e32 v10, 0x70, v1
	v_mul_lo_u32 v12, v23, s38
	s_mul_i32 s47, s47, 0x2c000
	v_lshlrev_b32_e32 v1, 2, v10
	s_mul_hi_i32 s26, s26, 0xb00
	s_add_u32 s27, s45, s47
	v_add3_u32 v1, 0, v12, v1
	v_add_u32_e32 v24, 0x400, v22
	s_addc_u32 s26, s46, s26
	s_lshl_b64 s[24:25], s[24:25], 1
	s_waitcnt vmcnt(63) expcnt(7) lgkmcnt(15)
	s_barrier
	s_add_u32 s24, s27, s24
	s_addc_u32 s25, s26, s25
	v_mov_b64_e32 v[12:13], s[24:25]
	v_mad_i64_i32 v[12:13], s[24:25], v23, s40, v[12:13]
	s_mov_b64 s[24:25], 0
	s_waitcnt vmcnt(2)
	ds_write2_b32 v22, v2, v6 offset1:32
	ds_write2_b32 v22, v3, v7 offset0:129 offset1:161
	ds_write2_b32 v24, v4, v8 offset0:2 offset1:34
	ds_write2_b32 v24, v5, v9 offset0:131 offset1:163
	s_waitcnt vmcnt(0)
	ds_write2_b32 v22, v14, v18 offset0:64 offset1:96
	ds_write2_b32 v22, v15, v19 offset0:193 offset1:225
	ds_write2_b32 v24, v16, v20 offset0:66 offset1:98
	ds_write2_b32 v24, v17, v21 offset0:195 offset1:227
	s_waitcnt lgkmcnt(0)
	s_barrier
	ds_read2_b32 v[2:3], v1 offset1:1
	ds_read2_b32 v[4:5], v1 offset0:2 offset1:3
	ds_read2_b32 v[6:7], v1 offset0:4 offset1:5
	ds_read2_b32 v[8:9], v1 offset0:6 offset1:7
	ds_read2_b32 v[14:15], v1 offset0:8 offset1:9
	ds_read2_b32 v[16:17], v1 offset0:10 offset1:11
	ds_read2_b32 v[18:19], v1 offset0:12 offset1:13
	ds_read2_b32 v[20:21], v1 offset0:14 offset1:15
	s_waitcnt lgkmcnt(7)
	v_cvt_pk_bf16_f32 v2, v2, v3
	s_waitcnt lgkmcnt(6)
	v_cvt_pk_bf16_f32 v3, v4, v5
	s_waitcnt lgkmcnt(5)
	v_cvt_pk_bf16_f32 v4, v6, v7
	s_waitcnt lgkmcnt(4)
	v_cvt_pk_bf16_f32 v5, v8, v9
	s_waitcnt lgkmcnt(3)
	v_cvt_pk_bf16_f32 v6, v14, v15
	s_waitcnt lgkmcnt(2)
	v_cvt_pk_bf16_f32 v7, v16, v17
	s_waitcnt lgkmcnt(1)
	v_cvt_pk_bf16_f32 v8, v18, v19
	s_waitcnt lgkmcnt(0)
	v_cvt_pk_bf16_f32 v9, v20, v21
.LBB0_1243:
	s_andn2_b64 vcc, exec, s[24:25]
	s_cbranch_vccnz .LBB0_1221
	s_mul_i32 s24, s28, 0xba2f
	s_lshr_b32 s24, s24, 25
	s_mul_i32 s25, s24, 0xfffffd40
	s_add_i32 s25, s25, s28
	s_mul_i32 s26, s25, 0xba3
	s_lshr_b32 s27, s26, 31
	s_ashr_i32 s26, s26, 20
	s_add_i32 s26, s26, s27
	s_sext_i32_i16 s27, s26
	s_mul_i32 s26, s27, 0xfffffea0
	s_add_i32 s29, s26, s25
	s_add_i32 s22, s22, s24
	s_addk_i32 s25, 0x15f
	s_cmpk_lt_u32 s25, 0x2bf
	s_cselect_b32 s25, s8, s10
	s_mul_i32 s22, s22, 0xb00000
	s_cselect_b32 s24, s9, s11
	s_add_u32 s25, s25, s22
	s_addc_u32 s42, s24, 0
	s_lshl_b32 s24, s29, 2
	s_lshl_b32 s29, s29, 3
	s_and_b32 s29, s29, 0xffffff00
	s_lshl_b32 s27, s27, 7
	s_and_b32 s26, s24, 0xffffffc0
	s_add_i32 s29, s29, s27
	s_and_b32 s24, s24, 64
	s_or_b32 s24, s29, s24
	s_add_u32 s22, s31, s22
	s_addc_u32 s29, s33, 0
	s_lshl_b32 s27, s28, 7
	s_and_b32 s28, s27, 0x780
	s_mul_i32 s27, s28, 0x1600
	s_add_u32 s25, s25, s27
	s_addc_u32 s42, s42, 0
	s_ashr_i32 s27, s26, 31
	v_mov_b32_e32 v1, v0
	s_lshl_b64 s[26:27], s[26:27], 2
	s_add_u32 s26, s25, s26
	v_lshlrev_b32_e32 v2, 2, v1
	v_and_b32_e32 v22, 60, v2
	s_addc_u32 s27, s42, s27
	v_ashrrev_i32_e32 v21, 4, v1
	v_lshlrev_b32_e32 v10, 2, v22
	v_lshl_add_u64 v[12:13], s[26:27], 0, v[10:11]
	v_add_u32_e32 v10, 64, v21
	v_add_u32_e32 v4, 32, v21
	v_mad_i64_i32 v[14:15], s[26:27], v10, s41, v[12:13]
	v_add_u32_e32 v10, 0x60, v21
	v_mad_i64_i32 v[2:3], s[26:27], v21, s41, v[12:13]
	v_mad_i64_i32 v[6:7], s[26:27], v4, s41, v[12:13]
	v_mad_i64_i32 v[16:17], s[26:27], v10, s41, v[12:13]
	global_load_dwordx4 v[2:5], v[2:3], off nt
	s_nop 0
	global_load_dwordx4 v[6:9], v[6:7], off nt
	s_nop 0
	global_load_dwordx4 v[12:15], v[14:15], off nt
	s_nop 0
	global_load_dwordx4 v[16:19], v[16:17], off nt
	v_ashrrev_i32_e32 v20, 3, v1
	v_lshlrev_b32_e32 v1, 4, v1
	v_lshlrev_b32_e32 v10, 2, v21
	v_mul_u32_u24_e32 v22, 0x204, v22
	v_add3_u32 v22, 0, v10, v22
	v_and_b32_e32 v10, 0x70, v1
	v_mul_lo_u32 v23, v20, s38
	s_ashr_i32 s25, s24, 31
	v_lshlrev_b32_e32 v1, 2, v10
	s_lshl_b64 s[24:25], s[24:25], 12
	v_add3_u32 v1, 0, v23, v1
	v_add_u32_e32 v24, 0x400, v22
	s_add_u32 s22, s22, s24
	s_waitcnt vmcnt(63) expcnt(7) lgkmcnt(15)
	s_barrier
	s_addc_u32 s25, s29, s25
	s_lshl_b32 s24, s28, 1
	v_ashrrev_i32_e32 v21, 31, v20
	s_add_u32 s24, s22, s24
	v_lshlrev_b64 v[20:21], 12, v[20:21]
	s_addc_u32 s25, s25, 0
	s_waitcnt vmcnt(2)
	ds_write2_b32 v22, v2, v6 offset1:32
	ds_write2_b32 v22, v3, v7 offset0:129 offset1:161
	ds_write2_b32 v24, v4, v8 offset0:2 offset1:34
	ds_write2_b32 v24, v5, v9 offset0:131 offset1:163
	s_waitcnt vmcnt(0)
	ds_write2_b32 v22, v12, v16 offset0:64 offset1:96
	ds_write2_b32 v22, v13, v17 offset0:193 offset1:225
	ds_write2_b32 v24, v14, v18 offset0:66 offset1:98
	ds_write2_b32 v24, v15, v19 offset0:195 offset1:227
	s_waitcnt lgkmcnt(0)
	s_barrier
	ds_read2_b32 v[2:3], v1 offset1:1
	ds_read2_b32 v[4:5], v1 offset0:2 offset1:3
	ds_read2_b32 v[6:7], v1 offset0:4 offset1:5
	ds_read2_b32 v[8:9], v1 offset0:6 offset1:7
	ds_read2_b32 v[12:13], v1 offset0:8 offset1:9
	ds_read2_b32 v[14:15], v1 offset0:10 offset1:11
	ds_read2_b32 v[16:17], v1 offset0:12 offset1:13
	ds_read2_b32 v[18:19], v1 offset0:14 offset1:15
	s_waitcnt lgkmcnt(7)
	v_cvt_pk_bf16_f32 v2, v2, v3
	s_waitcnt lgkmcnt(6)
	v_cvt_pk_bf16_f32 v3, v4, v5
	s_waitcnt lgkmcnt(5)
	v_cvt_pk_bf16_f32 v4, v6, v7
	s_waitcnt lgkmcnt(3)
	v_cvt_pk_bf16_f32 v6, v12, v13
	v_lshl_add_u64 v[12:13], s[24:25], 0, v[20:21]
	v_cvt_pk_bf16_f32 v5, v8, v9
	s_waitcnt lgkmcnt(2)
	v_cvt_pk_bf16_f32 v7, v14, v15
	s_waitcnt lgkmcnt(1)
	v_cvt_pk_bf16_f32 v8, v16, v17
	s_waitcnt lgkmcnt(0)
	v_cvt_pk_bf16_f32 v9, v18, v19
	s_branch .LBB0_1221

.LBB0_1325:
	s_or_b64 exec, exec, s[22:23]
	s_waitcnt lgkmcnt(0)
	s_barrier
	ds_read_b32 v1, v11 offset:40960
	s_mov_b64 s[22:23], -1
	s_waitcnt lgkmcnt(0)
	v_cmp_lt_u32_e32 vcc, s31, v1
	v_readfirstlane_b32 s26, v1
	s_cbranch_vccnz .LBB0_1320
	s_cmpk_lt_u32 s26, 0x4a00
	s_cbranch_scc0 .LBB0_1334
	s_cmpk_gt_u32 s26, 0x41ff
	s_cbranch_scc0 .LBB0_1333
	s_cmpk_gt_u32 s26, 0x47ff
	s_cbranch_scc0 .LBB0_1330
	s_add_i32 s20, s26, 0xffffb800
	s_lshr_b32 s24, s20, 4
	s_lshl_b32 s22, s24, 11
	s_lshl_b32 s20, s20, 7
	s_sub_i32 s22, s20, s22
	s_ashr_i32 s23, s22, 31
	s_lshl_b32 s20, s24, 6
	s_lshl_b64 s[24:25], s[22:23], 13
	s_add_u32 s27, s14, s24
	v_mov_b32_e32 v1, v0
	s_addc_u32 s40, s15, s25
	s_lshl_b64 s[24:25], s[20:21], 2
	s_add_u32 s24, s27, s24
	v_lshlrev_b32_e32 v2, 2, v1
	v_ashrrev_i32_e32 v12, 4, v1
	v_and_b32_e32 v24, 60, v2
	s_addc_u32 s25, s40, s25
	v_lshlrev_b32_e32 v10, 2, v24
	v_ashrrev_i32_e32 v13, 31, v12
	v_lshl_add_u64 v[2:3], s[24:25], 0, v[10:11]
	v_lshlrev_b64 v[4:5], 13, v[12:13]
	v_lshl_add_u64 v[14:15], v[2:3], 0, v[4:5]
	v_add_co_u32_e32 v6, vcc, s33, v14
	v_ashrrev_i32_e32 v22, 3, v1
	s_nop 0
	v_addc_co_u32_e32 v7, vcc, 0, v15, vcc
	v_add_co_u32_e32 v16, vcc, s34, v14
	global_load_dwordx4 v[2:5], v[14:15], off nt
	s_nop 0
	global_load_dwordx4 v[6:9], v[6:7], off nt
	v_addc_co_u32_e32 v17, vcc, 0, v15, vcc
	v_add_co_u32_e32 v18, vcc, s35, v14
	v_lshlrev_b32_e32 v1, 4, v1
	s_nop 0
	v_addc_co_u32_e32 v19, vcc, 0, v15, vcc
	global_load_dwordx4 v[14:17], v[16:17], off nt
	s_nop 0
	global_load_dwordx4 v[18:21], v[18:19], off nt
	v_lshlrev_b32_e32 v10, 2, v12
	v_ashrrev_i32_e32 v23, 31, v22
	v_mul_u32_u24_e32 v24, 0x204, v24
	v_mul_lo_u32 v25, v22, s36
	v_lshlrev_b64 v[12:13], 12, v[22:23]
	v_add3_u32 v22, 0, v10, v24
	v_and_b32_e32 v10, 0x70, v1
	v_lshlrev_b32_e32 v1, 2, v10
	v_add3_u32 v1, 0, v25, v1
	v_add_u32_e32 v23, 0x400, v22
	s_lshl_b64 s[24:25], s[20:21], 12
	s_barrier
	s_add_u32 s20, s0, s24
	s_addc_u32 s24, s1, s25
	s_lshl_b64 s[22:23], s[22:23], 1
	s_add_u32 s22, s20, s22
	s_addc_u32 s23, s24, s23
	v_lshl_add_u64 v[12:13], s[22:23], 0, v[12:13]
	s_mov_b64 s[22:23], 0
	s_waitcnt vmcnt(2)
	ds_write2_b32 v22, v2, v6 offset1:32
	ds_write2_b32 v22, v3, v7 offset0:129 offset1:161
	ds_write2_b32 v23, v4, v8 offset0:2 offset1:34
	ds_write2_b32 v23, v5, v9 offset0:131 offset1:163
	s_waitcnt vmcnt(0)
	ds_write2_b32 v22, v14, v18 offset0:64 offset1:96
	ds_write2_b32 v22, v15, v19 offset0:193 offset1:225
	ds_write2_b32 v23, v16, v20 offset0:66 offset1:98
	ds_write2_b32 v23, v17, v21 offset0:195 offset1:227
	s_waitcnt lgkmcnt(0)
	s_barrier
	ds_read2_b32 v[2:3], v1 offset1:1
	ds_read2_b32 v[4:5], v1 offset0:2 offset1:3
	ds_read2_b32 v[6:7], v1 offset0:4 offset1:5
	ds_read2_b32 v[8:9], v1 offset0:6 offset1:7
	ds_read2_b32 v[14:15], v1 offset0:8 offset1:9
	ds_read2_b32 v[16:17], v1 offset0:10 offset1:11
	ds_read2_b32 v[18:19], v1 offset0:12 offset1:13
	ds_read2_b32 v[20:21], v1 offset0:14 offset1:15
	s_waitcnt lgkmcnt(7)
	v_cvt_pk_bf16_f32 v2, v2, v3
	s_waitcnt lgkmcnt(6)
	v_cvt_pk_bf16_f32 v3, v4, v5
	s_waitcnt lgkmcnt(5)
	v_cvt_pk_bf16_f32 v4, v6, v7
	s_waitcnt lgkmcnt(4)
	v_cvt_pk_bf16_f32 v5, v8, v9
	s_waitcnt lgkmcnt(3)
	v_cvt_pk_bf16_f32 v6, v14, v15
	s_waitcnt lgkmcnt(2)
	v_cvt_pk_bf16_f32 v7, v16, v17
	s_waitcnt lgkmcnt(1)
	v_cvt_pk_bf16_f32 v8, v18, v19
	s_waitcnt lgkmcnt(0)
	v_cvt_pk_bf16_f32 v9, v20, v21
.LBB0_1330:
	s_andn2_b64 vcc, exec, s[22:23]
	s_cbranch_vccnz .LBB0_1332
	s_add_i32 s20, s26, 0xffffbe00
	s_lshr_b32 s24, s20, 4
	s_lshl_b32 s22, s24, 11
	s_lshl_b32 s20, s20, 7
	s_sub_i32 s22, s20, s22
	s_ashr_i32 s23, s22, 31
	s_lshl_b32 s20, s24, 6
	s_mul_i32 s25, s22, 0x6000
	s_mul_hi_i32 s24, s22, 0x6000
	s_add_u32 s27, s12, s25
	v_mov_b32_e32 v1, v0
	s_addc_u32 s40, s13, s24
	s_lshl_b64 s[24:25], s[20:21], 2
	s_add_u32 s24, s27, s24
	v_lshlrev_b32_e32 v2, 2, v1
	v_and_b32_e32 v22, 60, v2
	s_addc_u32 s25, s40, s25
	v_ashrrev_i32_e32 v21, 4, v1
	v_lshlrev_b32_e32 v10, 2, v22
	v_lshl_add_u64 v[12:13], s[24:25], 0, v[10:11]
	v_add_u32_e32 v10, 64, v21
	v_add_u32_e32 v4, 32, v21
	v_mad_i64_i32 v[14:15], s[24:25], v10, s37, v[12:13]
	v_add_u32_e32 v10, 0x60, v21
	v_mad_i64_i32 v[2:3], s[24:25], v21, s37, v[12:13]
	v_mad_i64_i32 v[6:7], s[24:25], v4, s37, v[12:13]
	v_mad_i64_i32 v[16:17], s[24:25], v10, s37, v[12:13]
	global_load_dwordx4 v[2:5], v[2:3], off nt
	s_nop 0
	global_load_dwordx4 v[6:9], v[6:7], off nt
	s_nop 0
	global_load_dwordx4 v[12:15], v[14:15], off nt
	s_nop 0
	global_load_dwordx4 v[16:19], v[16:17], off nt
	v_ashrrev_i32_e32 v20, 3, v1
	v_lshlrev_b32_e32 v1, 4, v1
	v_lshlrev_b32_e32 v10, 2, v21
	v_mul_u32_u24_e32 v22, 0x204, v22
	v_add3_u32 v22, 0, v10, v22
	v_and_b32_e32 v10, 0x70, v1
	v_mul_lo_u32 v23, v20, s36
	v_lshlrev_b32_e32 v1, 2, v10
	s_lshl_b64 s[24:25], s[20:21], 12
	v_add3_u32 v1, 0, v23, v1
	v_add_u32_e32 v24, 0x400, v22
	s_add_u32 s20, s3, s24
	s_barrier
	s_addc_u32 s24, s4, s25
	s_lshl_b64 s[22:23], s[22:23], 1
	v_ashrrev_i32_e32 v21, 31, v20
	s_add_u32 s22, s20, s22
	v_lshlrev_b64 v[20:21], 12, v[20:21]
	s_addc_u32 s23, s24, s23
	s_waitcnt vmcnt(2)
	ds_write2_b32 v22, v2, v6 offset1:32
	ds_write2_b32 v22, v3, v7 offset0:129 offset1:161
	ds_write2_b32 v24, v4, v8 offset0:2 offset1:34
	ds_write2_b32 v24, v5, v9 offset0:131 offset1:163
	s_waitcnt vmcnt(0)
	ds_write2_b32 v22, v12, v16 offset0:64 offset1:96
	ds_write2_b32 v22, v13, v17 offset0:193 offset1:225
	ds_write2_b32 v24, v14, v18 offset0:66 offset1:98
	ds_write2_b32 v24, v15, v19 offset0:195 offset1:227
	s_waitcnt lgkmcnt(0)
	s_barrier
	ds_read2_b32 v[2:3], v1 offset1:1
	ds_read2_b32 v[4:5], v1 offset0:2 offset1:3
	ds_read2_b32 v[6:7], v1 offset0:4 offset1:5
	ds_read2_b32 v[8:9], v1 offset0:6 offset1:7
	ds_read2_b32 v[12:13], v1 offset0:8 offset1:9
	ds_read2_b32 v[14:15], v1 offset0:10 offset1:11
	ds_read2_b32 v[16:17], v1 offset0:12 offset1:13
	ds_read2_b32 v[18:19], v1 offset0:14 offset1:15
	s_waitcnt lgkmcnt(7)
	v_cvt_pk_bf16_f32 v2, v2, v3
	s_waitcnt lgkmcnt(6)
	v_cvt_pk_bf16_f32 v3, v4, v5
	s_waitcnt lgkmcnt(5)
	v_cvt_pk_bf16_f32 v4, v6, v7
	s_waitcnt lgkmcnt(3)
	v_cvt_pk_bf16_f32 v6, v12, v13
	v_lshl_add_u64 v[12:13], s[22:23], 0, v[20:21]
	v_cvt_pk_bf16_f32 v5, v8, v9
	s_waitcnt lgkmcnt(2)
	v_cvt_pk_bf16_f32 v7, v14, v15
	s_waitcnt lgkmcnt(1)
	v_cvt_pk_bf16_f32 v8, v16, v17
	s_waitcnt lgkmcnt(0)
	v_cvt_pk_bf16_f32 v9, v18, v19

.LBB0_1336:
	s_andn2_b64 vcc, exec, s[22:23]
	s_cbranch_vccnz .LBB0_1319
	s_cmpk_gt_u32 s20, 0x2bff
	s_mov_b64 s[22:23], -1
	s_cbranch_scc0 .LBB0_1339
	s_add_i32 s22, s20, 0xffffd400
	s_mul_i32 s23, s22, 0xba2f
	s_lshr_b32 s23, s23, 24
	s_mul_i32 s24, s23, 0xfffffea0
	s_add_i32 s23, s27, s23
	s_add_i32 s22, s24, s22
	s_mul_i32 s25, s23, 0xb00000
	s_mul_hi_u32 s24, s23, 0xb00000
	s_add_u32 s42, s16, s25
	s_addc_u32 s43, s17, s24
	s_mul_i32 s23, s23, 0x580000
	s_add_u32 s44, s5, s23
	s_mul_i32 s23, s22, 0x1746
	s_addc_u32 s45, s28, 0
	s_lshr_b32 s24, s23, 31
	s_lshr_b32 s23, s23, 16
	s_add_i32 s23, s23, s24
	s_sext_i32_i16 s46, s23
	s_mul_i32 s23, s46, -11
	s_add_i32 s23, s23, s22
	s_lshl_b32 s22, s23, 7
	s_ashr_i32 s23, s22, 31
	s_lshl_b32 s24, s46, 6
	s_ashr_i32 s25, s24, 31
	s_lshl_b64 s[40:41], s[22:23], 13
	s_add_u32 s42, s42, s40
	v_mov_b32_e32 v1, v0
	s_addc_u32 s43, s43, s41
	s_lshl_b64 s[40:41], s[24:25], 2
	s_add_u32 s40, s42, s40
	v_lshlrev_b32_e32 v2, 2, v1
	v_ashrrev_i32_e32 v12, 4, v1
	v_and_b32_e32 v22, 60, v2
	s_addc_u32 s41, s43, s41
	v_lshlrev_b32_e32 v10, 2, v22
	v_ashrrev_i32_e32 v13, 31, v12
	v_lshl_add_u64 v[2:3], s[40:41], 0, v[10:11]
	v_lshlrev_b64 v[4:5], 13, v[12:13]
	v_lshl_add_u64 v[14:15], v[2:3], 0, v[4:5]
	v_add_co_u32_e32 v6, vcc, s33, v14
	v_ashrrev_i32_e32 v23, 3, v1
	s_nop 0
	v_addc_co_u32_e32 v7, vcc, 0, v15, vcc
	v_add_co_u32_e32 v16, vcc, s34, v14
	global_load_dwordx4 v[2:5], v[14:15], off nt
	s_nop 0
	global_load_dwordx4 v[6:9], v[6:7], off nt
	v_addc_co_u32_e32 v17, vcc, 0, v15, vcc
	v_add_co_u32_e32 v18, vcc, s35, v14
	v_lshlrev_b32_e32 v1, 4, v1
	s_nop 0
	v_addc_co_u32_e32 v19, vcc, 0, v15, vcc
	global_load_dwordx4 v[14:17], v[16:17], off nt
	s_nop 0
	global_load_dwordx4 v[18:21], v[18:19], off nt
	v_lshlrev_b32_e32 v10, 2, v12
	v_mul_u32_u24_e32 v13, 0x204, v22
	v_add3_u32 v22, 0, v10, v13
	v_and_b32_e32 v10, 0x70, v1
	v_mul_lo_u32 v12, v23, s36
	s_mul_i32 s46, s46, 0x2c000
	v_lshlrev_b32_e32 v1, 2, v10
	s_mul_hi_i32 s24, s24, 0xb00
	s_add_u32 s25, s44, s46
	v_add3_u32 v1, 0, v12, v1
	v_add_u32_e32 v24, 0x400, v22
	s_addc_u32 s24, s45, s24
	s_lshl_b64 s[22:23], s[22:23], 1
	s_barrier
	s_add_u32 s22, s25, s22
	s_addc_u32 s23, s24, s23
	v_mov_b64_e32 v[12:13], s[22:23]
	v_mad_i64_i32 v[12:13], s[22:23], v23, s38, v[12:13]
	s_mov_b64 s[22:23], 0
	s_waitcnt vmcnt(2)
	ds_write2_b32 v22, v2, v6 offset1:32
	ds_write2_b32 v22, v3, v7 offset0:129 offset1:161
	ds_write2_b32 v24, v4, v8 offset0:2 offset1:34
	ds_write2_b32 v24, v5, v9 offset0:131 offset1:163
	s_waitcnt vmcnt(0)
	ds_write2_b32 v22, v14, v18 offset0:64 offset1:96
	ds_write2_b32 v22, v15, v19 offset0:193 offset1:225
	ds_write2_b32 v24, v16, v20 offset0:66 offset1:98
	ds_write2_b32 v24, v17, v21 offset0:195 offset1:227
	s_waitcnt lgkmcnt(0)
	s_barrier
	ds_read2_b32 v[2:3], v1 offset1:1
	ds_read2_b32 v[4:5], v1 offset0:2 offset1:3
	ds_read2_b32 v[6:7], v1 offset0:4 offset1:5
	ds_read2_b32 v[8:9], v1 offset0:6 offset1:7
	ds_read2_b32 v[14:15], v1 offset0:8 offset1:9
	ds_read2_b32 v[16:17], v1 offset0:10 offset1:11
	ds_read2_b32 v[18:19], v1 offset0:12 offset1:13
	ds_read2_b32 v[20:21], v1 offset0:14 offset1:15
	s_waitcnt lgkmcnt(7)
	v_cvt_pk_bf16_f32 v2, v2, v3
	s_waitcnt lgkmcnt(6)
	v_cvt_pk_bf16_f32 v3, v4, v5
	s_waitcnt lgkmcnt(5)
	v_cvt_pk_bf16_f32 v4, v6, v7
	s_waitcnt lgkmcnt(4)
	v_cvt_pk_bf16_f32 v5, v8, v9
	s_waitcnt lgkmcnt(3)
	v_cvt_pk_bf16_f32 v6, v14, v15
	s_waitcnt lgkmcnt(2)
	v_cvt_pk_bf16_f32 v7, v16, v17
	s_waitcnt lgkmcnt(1)
	v_cvt_pk_bf16_f32 v8, v18, v19
	s_waitcnt lgkmcnt(0)
	v_cvt_pk_bf16_f32 v9, v20, v21
.LBB0_1339:
	s_andn2_b64 vcc, exec, s[22:23]
	s_cbranch_vccnz .LBB0_1319
	s_mul_i32 s22, s20, 0xba2f
	s_lshr_b32 s22, s22, 25
	s_mul_i32 s23, s22, 0xfffffd40
	s_add_i32 s23, s23, s20
	s_mul_i32 s24, s23, 0xba3
	s_lshr_b32 s25, s24, 31
	s_ashr_i32 s24, s24, 20
	s_add_i32 s24, s24, s25
	s_sext_i32_i16 s25, s24
	s_mul_i32 s24, s25, 0xfffffea0
	s_add_i32 s40, s24, s23
	s_add_i32 s22, s27, s22
	s_addk_i32 s23, 0x15f
	s_cmpk_lt_u32 s23, 0x2bf
	s_cselect_b32 s24, s8, s10
	s_mul_i32 s27, s22, 0xb00000
	s_cselect_b32 s23, s9, s11
	s_add_u32 s41, s24, s27
	s_addc_u32 s23, s23, 0
	s_lshl_b32 s22, s40, 2
	s_lshl_b32 s40, s40, 3
	s_and_b32 s40, s40, 0xffffff00
	s_lshl_b32 s25, s25, 7
	s_and_b32 s24, s22, 0xffffffc0
	s_add_i32 s40, s40, s25
	s_and_b32 s22, s22, 64
	s_or_b32 s22, s40, s22
	s_add_u32 s27, s29, s27
	s_addc_u32 s40, s30, 0
	s_lshl_b32 s20, s20, 7
	s_and_b32 s20, s20, 0x780
	s_mul_i32 s25, s20, 0x1600
	s_add_u32 s41, s41, s25
	s_addc_u32 s23, s23, 0
	s_ashr_i32 s25, s24, 31
	v_mov_b32_e32 v1, v0
	s_lshl_b64 s[24:25], s[24:25], 2
	s_add_u32 s24, s41, s24
	v_lshlrev_b32_e32 v2, 2, v1
	v_and_b32_e32 v22, 60, v2
	s_addc_u32 s25, s23, s25
	v_ashrrev_i32_e32 v21, 4, v1
	v_lshlrev_b32_e32 v10, 2, v22
	v_lshl_add_u64 v[12:13], s[24:25], 0, v[10:11]
	v_add_u32_e32 v10, 64, v21
	v_add_u32_e32 v4, 32, v21
	v_mad_i64_i32 v[14:15], s[24:25], v10, s39, v[12:13]
	v_add_u32_e32 v10, 0x60, v21
	v_mad_i64_i32 v[2:3], s[24:25], v21, s39, v[12:13]
	v_mad_i64_i32 v[6:7], s[24:25], v4, s39, v[12:13]
	v_mad_i64_i32 v[16:17], s[24:25], v10, s39, v[12:13]
	global_load_dwordx4 v[2:5], v[2:3], off nt
	s_nop 0
	global_load_dwordx4 v[6:9], v[6:7], off nt
	s_nop 0
	global_load_dwordx4 v[12:15], v[14:15], off nt
	s_nop 0
	global_load_dwordx4 v[16:19], v[16:17], off nt
	v_ashrrev_i32_e32 v20, 3, v1
	v_lshlrev_b32_e32 v1, 4, v1
	v_lshlrev_b32_e32 v10, 2, v21
	v_mul_u32_u24_e32 v22, 0x204, v22
	v_add3_u32 v22, 0, v10, v22
	v_and_b32_e32 v10, 0x70, v1
	v_mul_lo_u32 v23, v20, s36
	s_ashr_i32 s23, s22, 31
	v_lshlrev_b32_e32 v1, 2, v10
	s_lshl_b64 s[22:23], s[22:23], 12
	v_add3_u32 v1, 0, v23, v1
	v_add_u32_e32 v24, 0x400, v22
	s_add_u32 s22, s27, s22
	s_barrier
	s_addc_u32 s23, s40, s23
	s_lshl_b32 s20, s20, 1
	v_ashrrev_i32_e32 v21, 31, v20
	s_add_u32 s22, s22, s20
	v_lshlrev_b64 v[20:21], 12, v[20:21]
	s_addc_u32 s23, s23, 0
	s_waitcnt vmcnt(2)
	ds_write2_b32 v22, v2, v6 offset1:32
	ds_write2_b32 v22, v3, v7 offset0:129 offset1:161
	ds_write2_b32 v24, v4, v8 offset0:2 offset1:34
	ds_write2_b32 v24, v5, v9 offset0:131 offset1:163
	s_waitcnt vmcnt(0)
	ds_write2_b32 v22, v12, v16 offset0:64 offset1:96
	ds_write2_b32 v22, v13, v17 offset0:193 offset1:225
	ds_write2_b32 v24, v14, v18 offset0:66 offset1:98
	ds_write2_b32 v24, v15, v19 offset0:195 offset1:227
	s_waitcnt lgkmcnt(0)
	s_barrier
	ds_read2_b32 v[2:3], v1 offset1:1
	ds_read2_b32 v[4:5], v1 offset0:2 offset1:3
	ds_read2_b32 v[6:7], v1 offset0:4 offset1:5
	ds_read2_b32 v[8:9], v1 offset0:6 offset1:7
	ds_read2_b32 v[12:13], v1 offset0:8 offset1:9
	ds_read2_b32 v[14:15], v1 offset0:10 offset1:11
	ds_read2_b32 v[16:17], v1 offset0:12 offset1:13
	ds_read2_b32 v[18:19], v1 offset0:14 offset1:15
	s_waitcnt lgkmcnt(7)
	v_cvt_pk_bf16_f32 v2, v2, v3
	s_waitcnt lgkmcnt(6)
	v_cvt_pk_bf16_f32 v3, v4, v5
	s_waitcnt lgkmcnt(5)
	v_cvt_pk_bf16_f32 v4, v6, v7
	s_waitcnt lgkmcnt(3)
	v_cvt_pk_bf16_f32 v6, v12, v13
	v_lshl_add_u64 v[12:13], s[22:23], 0, v[20:21]
	v_cvt_pk_bf16_f32 v5, v8, v9
	s_waitcnt lgkmcnt(2)
	v_cvt_pk_bf16_f32 v7, v14, v15
	s_waitcnt lgkmcnt(1)
	v_cvt_pk_bf16_f32 v8, v16, v17
	s_waitcnt lgkmcnt(0)
	v_cvt_pk_bf16_f32 v9, v18, v19
	s_branch .LBB0_1319

.LBB0_1466:
	s_or_b64 exec, exec, s[24:25]
	s_waitcnt lgkmcnt(0)
	s_barrier
	ds_read_b32 v1, v11 offset:40960
	s_mov_b64 s[24:25], -1
	s_waitcnt lgkmcnt(0)
	v_cmp_lt_u32_e32 vcc, s34, v1
	v_readfirstlane_b32 s28, v1
	s_cbranch_vccnz .LBB0_1459
	s_cmpk_lt_u32 s28, 0x4a00
	s_cbranch_scc0 .LBB0_1475
	s_cmpk_gt_u32 s28, 0x41ff
	s_cbranch_scc0 .LBB0_1474
	s_cmpk_gt_u32 s28, 0x47ff
	s_cbranch_scc0 .LBB0_1471
	s_add_i32 s14, s28, 0xffffb800
	s_lshr_b32 s26, s14, 4
	s_lshl_b32 s24, s26, 11
	s_lshl_b32 s14, s14, 7
	s_sub_i32 s24, s14, s24
	s_ashr_i32 s25, s24, 31
	s_lshl_b32 s14, s26, 6
	s_lshl_b64 s[26:27], s[24:25], 13
	s_add_u32 s29, s22, s26
	v_mov_b32_e32 v1, v0
	s_addc_u32 s42, s23, s27
	s_lshl_b64 s[26:27], s[14:15], 2
	s_add_u32 s26, s29, s26
	v_lshlrev_b32_e32 v2, 2, v1
	v_ashrrev_i32_e32 v12, 4, v1
	v_and_b32_e32 v24, 60, v2
	s_addc_u32 s27, s42, s27
	v_lshlrev_b32_e32 v10, 2, v24
	v_ashrrev_i32_e32 v13, 31, v12
	v_lshl_add_u64 v[2:3], s[26:27], 0, v[10:11]
	v_lshlrev_b64 v[4:5], 13, v[12:13]
	v_lshl_add_u64 v[14:15], v[2:3], 0, v[4:5]
	v_add_co_u32_e32 v6, vcc, s35, v14
	v_ashrrev_i32_e32 v22, 3, v1
	s_nop 0
	v_addc_co_u32_e32 v7, vcc, 0, v15, vcc
	v_add_co_u32_e32 v16, vcc, s36, v14
	global_load_dwordx4 v[2:5], v[14:15], off nt
	s_nop 0
	global_load_dwordx4 v[6:9], v[6:7], off nt
	v_addc_co_u32_e32 v17, vcc, 0, v15, vcc
	v_add_co_u32_e32 v18, vcc, s37, v14
	v_lshlrev_b32_e32 v1, 4, v1
	s_nop 0
	v_addc_co_u32_e32 v19, vcc, 0, v15, vcc
	global_load_dwordx4 v[14:17], v[16:17], off nt
	s_nop 0
	global_load_dwordx4 v[18:21], v[18:19], off nt
	v_lshlrev_b32_e32 v10, 2, v12
	v_ashrrev_i32_e32 v23, 31, v22
	v_mul_u32_u24_e32 v24, 0x204, v24
	v_mul_lo_u32 v25, v22, s38
	v_lshlrev_b64 v[12:13], 12, v[22:23]
	v_add3_u32 v22, 0, v10, v24
	v_and_b32_e32 v10, 0x70, v1
	v_lshlrev_b32_e32 v1, 2, v10
	v_add3_u32 v1, 0, v25, v1
	v_add_u32_e32 v23, 0x400, v22
	s_lshl_b64 s[26:27], s[14:15], 12
	s_barrier
	s_add_u32 s14, s3, s26
	s_addc_u32 s26, s4, s27
	s_lshl_b64 s[24:25], s[24:25], 1
	s_add_u32 s24, s14, s24
	s_addc_u32 s25, s26, s25
	v_lshl_add_u64 v[12:13], s[24:25], 0, v[12:13]
	s_mov_b64 s[24:25], 0
	s_waitcnt vmcnt(2)
	ds_write2_b32 v22, v2, v6 offset1:32
	ds_write2_b32 v22, v3, v7 offset0:129 offset1:161
	ds_write2_b32 v23, v4, v8 offset0:2 offset1:34
	ds_write2_b32 v23, v5, v9 offset0:131 offset1:163
	s_waitcnt vmcnt(0)
	ds_write2_b32 v22, v14, v18 offset0:64 offset1:96
	ds_write2_b32 v22, v15, v19 offset0:193 offset1:225
	ds_write2_b32 v23, v16, v20 offset0:66 offset1:98
	ds_write2_b32 v23, v17, v21 offset0:195 offset1:227
	s_waitcnt lgkmcnt(0)
	s_barrier
	ds_read2_b32 v[2:3], v1 offset1:1
	ds_read2_b32 v[4:5], v1 offset0:2 offset1:3
	ds_read2_b32 v[6:7], v1 offset0:4 offset1:5
	ds_read2_b32 v[8:9], v1 offset0:6 offset1:7
	ds_read2_b32 v[14:15], v1 offset0:8 offset1:9
	ds_read2_b32 v[16:17], v1 offset0:10 offset1:11
	ds_read2_b32 v[18:19], v1 offset0:12 offset1:13
	ds_read2_b32 v[20:21], v1 offset0:14 offset1:15
	s_waitcnt lgkmcnt(7)
	v_cvt_pk_bf16_f32 v2, v2, v3
	s_waitcnt lgkmcnt(6)
	v_cvt_pk_bf16_f32 v3, v4, v5
	s_waitcnt lgkmcnt(5)
	v_cvt_pk_bf16_f32 v4, v6, v7
	s_waitcnt lgkmcnt(4)
	v_cvt_pk_bf16_f32 v5, v8, v9
	s_waitcnt lgkmcnt(3)
	v_cvt_pk_bf16_f32 v6, v14, v15
	s_waitcnt lgkmcnt(2)
	v_cvt_pk_bf16_f32 v7, v16, v17
	s_waitcnt lgkmcnt(1)
	v_cvt_pk_bf16_f32 v8, v18, v19
	s_waitcnt lgkmcnt(0)
	v_cvt_pk_bf16_f32 v9, v20, v21
.LBB0_1471:
	s_andn2_b64 vcc, exec, s[24:25]
	s_cbranch_vccnz .LBB0_1473
	s_add_i32 s14, s28, 0xffffbe00
	s_lshr_b32 s26, s14, 4
	s_lshl_b32 s24, s26, 11
	s_lshl_b32 s14, s14, 7
	s_sub_i32 s24, s14, s24
	s_ashr_i32 s25, s24, 31
	s_lshl_b32 s14, s26, 6
	s_mul_i32 s27, s24, 0x6000
	s_mul_hi_i32 s26, s24, 0x6000
	s_add_u32 s29, s12, s27
	v_mov_b32_e32 v1, v0
	s_addc_u32 s42, s13, s26
	s_lshl_b64 s[26:27], s[14:15], 2
	s_add_u32 s26, s29, s26
	v_lshlrev_b32_e32 v2, 2, v1
	v_and_b32_e32 v22, 60, v2
	s_addc_u32 s27, s42, s27
	v_ashrrev_i32_e32 v21, 4, v1
	v_lshlrev_b32_e32 v10, 2, v22
	v_lshl_add_u64 v[12:13], s[26:27], 0, v[10:11]
	v_add_u32_e32 v10, 64, v21
	v_add_u32_e32 v4, 32, v21
	v_mad_i64_i32 v[14:15], s[26:27], v10, s39, v[12:13]
	v_add_u32_e32 v10, 0x60, v21
	v_mad_i64_i32 v[2:3], s[26:27], v21, s39, v[12:13]
	v_mad_i64_i32 v[6:7], s[26:27], v4, s39, v[12:13]
	v_mad_i64_i32 v[16:17], s[26:27], v10, s39, v[12:13]
	global_load_dwordx4 v[2:5], v[2:3], off nt
	s_nop 0
	global_load_dwordx4 v[6:9], v[6:7], off nt
	s_nop 0
	global_load_dwordx4 v[12:15], v[14:15], off nt
	s_nop 0
	global_load_dwordx4 v[16:19], v[16:17], off nt
	v_ashrrev_i32_e32 v20, 3, v1
	v_lshlrev_b32_e32 v1, 4, v1
	v_lshlrev_b32_e32 v10, 2, v21
	v_mul_u32_u24_e32 v22, 0x204, v22
	v_add3_u32 v22, 0, v10, v22
	v_and_b32_e32 v10, 0x70, v1
	v_mul_lo_u32 v23, v20, s38
	v_lshlrev_b32_e32 v1, 2, v10
	s_lshl_b64 s[26:27], s[14:15], 12
	v_add3_u32 v1, 0, v23, v1
	v_add_u32_e32 v24, 0x400, v22
	s_add_u32 s14, s0, s26
	s_barrier
	s_addc_u32 s26, s1, s27
	s_lshl_b64 s[24:25], s[24:25], 1
	v_ashrrev_i32_e32 v21, 31, v20
	s_add_u32 s24, s14, s24
	v_lshlrev_b64 v[20:21], 12, v[20:21]
	s_addc_u32 s25, s26, s25
	s_waitcnt vmcnt(2)
	ds_write2_b32 v22, v2, v6 offset1:32
	ds_write2_b32 v22, v3, v7 offset0:129 offset1:161
	ds_write2_b32 v24, v4, v8 offset0:2 offset1:34
	ds_write2_b32 v24, v5, v9 offset0:131 offset1:163
	s_waitcnt vmcnt(0)
	ds_write2_b32 v22, v12, v16 offset0:64 offset1:96
	ds_write2_b32 v22, v13, v17 offset0:193 offset1:225
	ds_write2_b32 v24, v14, v18 offset0:66 offset1:98
	ds_write2_b32 v24, v15, v19 offset0:195 offset1:227
	s_waitcnt lgkmcnt(0)
	s_barrier
	ds_read2_b32 v[2:3], v1 offset1:1
	ds_read2_b32 v[4:5], v1 offset0:2 offset1:3
	ds_read2_b32 v[6:7], v1 offset0:4 offset1:5
	ds_read2_b32 v[8:9], v1 offset0:6 offset1:7
	ds_read2_b32 v[12:13], v1 offset0:8 offset1:9
	ds_read2_b32 v[14:15], v1 offset0:10 offset1:11
	ds_read2_b32 v[16:17], v1 offset0:12 offset1:13
	ds_read2_b32 v[18:19], v1 offset0:14 offset1:15
	s_waitcnt lgkmcnt(7)
	v_cvt_pk_bf16_f32 v2, v2, v3
	s_waitcnt lgkmcnt(6)
	v_cvt_pk_bf16_f32 v3, v4, v5
	s_waitcnt lgkmcnt(5)
	v_cvt_pk_bf16_f32 v4, v6, v7
	s_waitcnt lgkmcnt(3)
	v_cvt_pk_bf16_f32 v6, v12, v13
	v_lshl_add_u64 v[12:13], s[24:25], 0, v[20:21]
	v_cvt_pk_bf16_f32 v5, v8, v9
	s_waitcnt lgkmcnt(2)
	v_cvt_pk_bf16_f32 v7, v14, v15
	s_waitcnt lgkmcnt(1)
	v_cvt_pk_bf16_f32 v8, v16, v17
	s_waitcnt lgkmcnt(0)
	v_cvt_pk_bf16_f32 v9, v18, v19

.LBB0_1477:
	s_andn2_b64 vcc, exec, s[24:25]
	s_cbranch_vccnz .LBB0_1458
	s_cmpk_gt_u32 s28, 0x2bff
	s_mov_b64 s[24:25], -1
	s_cbranch_scc0 .LBB0_1480
	s_add_i32 s24, s28, 0xffffd400
	s_mul_i32 s25, s24, 0xba2f
	s_lshr_b32 s25, s25, 24
	s_mul_i32 s26, s25, 0xfffffea0
	s_add_i32 s25, s14, s25
	s_add_i32 s24, s26, s24
	s_mul_i32 s27, s25, 0xb00000
	s_mul_hi_u32 s26, s25, 0xb00000
	s_add_u32 s29, s10, s27
	s_addc_u32 s44, s11, s26
	s_mul_i32 s25, s25, 0x580000
	s_add_u32 s45, s5, s25
	s_mul_i32 s25, s24, 0x1746
	s_addc_u32 s46, s30, 0
	s_lshr_b32 s26, s25, 31
	s_lshr_b32 s25, s25, 16
	s_add_i32 s25, s25, s26
	s_sext_i32_i16 s47, s25
	s_mul_i32 s25, s47, -11
	s_add_i32 s25, s25, s24
	s_lshl_b32 s24, s25, 7
	s_ashr_i32 s25, s24, 31
	s_lshl_b32 s26, s47, 6
	s_ashr_i32 s27, s26, 31
	s_lshl_b64 s[42:43], s[24:25], 13
	s_add_u32 s29, s29, s42
	v_mov_b32_e32 v1, v0
	s_addc_u32 s44, s44, s43
	s_lshl_b64 s[42:43], s[26:27], 2
	s_add_u32 s42, s29, s42
	v_lshlrev_b32_e32 v2, 2, v1
	v_ashrrev_i32_e32 v12, 4, v1
	v_and_b32_e32 v22, 60, v2
	s_addc_u32 s43, s44, s43
	v_lshlrev_b32_e32 v10, 2, v22
	v_ashrrev_i32_e32 v13, 31, v12
	v_lshl_add_u64 v[2:3], s[42:43], 0, v[10:11]
	v_lshlrev_b64 v[4:5], 13, v[12:13]
	v_lshl_add_u64 v[14:15], v[2:3], 0, v[4:5]
	v_add_co_u32_e32 v6, vcc, s35, v14
	v_ashrrev_i32_e32 v23, 3, v1
	s_nop 0
	v_addc_co_u32_e32 v7, vcc, 0, v15, vcc
	v_add_co_u32_e32 v16, vcc, s36, v14
	global_load_dwordx4 v[2:5], v[14:15], off nt
	s_nop 0
	global_load_dwordx4 v[6:9], v[6:7], off nt
	v_addc_co_u32_e32 v17, vcc, 0, v15, vcc
	v_add_co_u32_e32 v18, vcc, s37, v14
	v_lshlrev_b32_e32 v1, 4, v1
	s_nop 0
	v_addc_co_u32_e32 v19, vcc, 0, v15, vcc
	global_load_dwordx4 v[14:17], v[16:17], off nt
	s_nop 0
	global_load_dwordx4 v[18:21], v[18:19], off nt
	v_lshlrev_b32_e32 v10, 2, v12
	v_mul_u32_u24_e32 v13, 0x204, v22
	v_add3_u32 v22, 0, v10, v13
	v_and_b32_e32 v10, 0x70, v1
	v_mul_lo_u32 v12, v23, s38
	s_mul_i32 s47, s47, 0x2c000
	v_lshlrev_b32_e32 v1, 2, v10
	s_mul_hi_i32 s26, s26, 0xb00
	s_add_u32 s27, s45, s47
	v_add3_u32 v1, 0, v12, v1
	v_add_u32_e32 v24, 0x400, v22
	s_addc_u32 s26, s46, s26
	s_lshl_b64 s[24:25], s[24:25], 1
	s_barrier
	s_add_u32 s24, s27, s24
	s_addc_u32 s25, s26, s25
	v_mov_b64_e32 v[12:13], s[24:25]
	v_mad_i64_i32 v[12:13], s[24:25], v23, s40, v[12:13]
	s_mov_b64 s[24:25], 0
	s_waitcnt vmcnt(2)
	ds_write2_b32 v22, v2, v6 offset1:32
	ds_write2_b32 v22, v3, v7 offset0:129 offset1:161
	ds_write2_b32 v24, v4, v8 offset0:2 offset1:34
	ds_write2_b32 v24, v5, v9 offset0:131 offset1:163
	s_waitcnt vmcnt(0)
	ds_write2_b32 v22, v14, v18 offset0:64 offset1:96
	ds_write2_b32 v22, v15, v19 offset0:193 offset1:225
	ds_write2_b32 v24, v16, v20 offset0:66 offset1:98
	ds_write2_b32 v24, v17, v21 offset0:195 offset1:227
	s_waitcnt lgkmcnt(0)
	s_barrier
	ds_read2_b32 v[2:3], v1 offset1:1
	ds_read2_b32 v[4:5], v1 offset0:2 offset1:3
	ds_read2_b32 v[6:7], v1 offset0:4 offset1:5
	ds_read2_b32 v[8:9], v1 offset0:6 offset1:7
	ds_read2_b32 v[14:15], v1 offset0:8 offset1:9
	ds_read2_b32 v[16:17], v1 offset0:10 offset1:11
	ds_read2_b32 v[18:19], v1 offset0:12 offset1:13
	ds_read2_b32 v[20:21], v1 offset0:14 offset1:15
	s_waitcnt lgkmcnt(7)
	v_cvt_pk_bf16_f32 v2, v2, v3
	s_waitcnt lgkmcnt(6)
	v_cvt_pk_bf16_f32 v3, v4, v5
	s_waitcnt lgkmcnt(5)
	v_cvt_pk_bf16_f32 v4, v6, v7
	s_waitcnt lgkmcnt(4)
	v_cvt_pk_bf16_f32 v5, v8, v9
	s_waitcnt lgkmcnt(3)
	v_cvt_pk_bf16_f32 v6, v14, v15
	s_waitcnt lgkmcnt(2)
	v_cvt_pk_bf16_f32 v7, v16, v17
	s_waitcnt lgkmcnt(1)
	v_cvt_pk_bf16_f32 v8, v18, v19
	s_waitcnt lgkmcnt(0)
	v_cvt_pk_bf16_f32 v9, v20, v21
.LBB0_1480:
	s_andn2_b64 vcc, exec, s[24:25]
	s_cbranch_vccnz .LBB0_1458
	s_mul_i32 s24, s28, 0xba2f
	s_lshr_b32 s24, s24, 25
	s_mul_i32 s25, s24, 0xfffffd40
	s_add_i32 s25, s25, s28
	s_mul_i32 s26, s25, 0xba3
	s_lshr_b32 s27, s26, 31
	s_ashr_i32 s26, s26, 20
	s_add_i32 s26, s26, s27
	s_sext_i32_i16 s27, s26
	s_mul_i32 s26, s27, 0xfffffea0
	s_add_i32 s29, s26, s25
	s_add_i32 s14, s14, s24
	s_addk_i32 s25, 0x15f
	s_cmpk_lt_u32 s25, 0x2bf
	s_cselect_b32 s25, s16, s18
	s_mul_i32 s14, s14, 0xb00000
	s_cselect_b32 s24, s17, s19
	s_add_u32 s25, s25, s14
	s_addc_u32 s42, s24, 0
	s_lshl_b32 s24, s29, 2
	s_lshl_b32 s29, s29, 3
	s_and_b32 s29, s29, 0xffffff00
	s_lshl_b32 s27, s27, 7
	s_and_b32 s26, s24, 0xffffffc0
	s_add_i32 s29, s29, s27
	s_and_b32 s24, s24, 64
	s_or_b32 s24, s29, s24
	s_add_u32 s14, s31, s14
	s_addc_u32 s29, s33, 0
	s_lshl_b32 s27, s28, 7
	s_and_b32 s28, s27, 0x780
	s_mul_i32 s27, s28, 0x1600
	s_add_u32 s25, s25, s27
	s_addc_u32 s42, s42, 0
	s_ashr_i32 s27, s26, 31
	v_mov_b32_e32 v1, v0
	s_lshl_b64 s[26:27], s[26:27], 2
	s_add_u32 s26, s25, s26
	v_lshlrev_b32_e32 v2, 2, v1
	v_and_b32_e32 v22, 60, v2
	s_addc_u32 s27, s42, s27
	v_ashrrev_i32_e32 v21, 4, v1
	v_lshlrev_b32_e32 v10, 2, v22
	v_lshl_add_u64 v[12:13], s[26:27], 0, v[10:11]
	v_add_u32_e32 v10, 64, v21
	v_add_u32_e32 v4, 32, v21
	v_mad_i64_i32 v[14:15], s[26:27], v10, s41, v[12:13]
	v_add_u32_e32 v10, 0x60, v21
	v_mad_i64_i32 v[2:3], s[26:27], v21, s41, v[12:13]
	v_mad_i64_i32 v[6:7], s[26:27], v4, s41, v[12:13]
	v_mad_i64_i32 v[16:17], s[26:27], v10, s41, v[12:13]
	global_load_dwordx4 v[2:5], v[2:3], off nt
	s_nop 0
	global_load_dwordx4 v[6:9], v[6:7], off nt
	s_nop 0
	global_load_dwordx4 v[12:15], v[14:15], off nt
	s_nop 0
	global_load_dwordx4 v[16:19], v[16:17], off nt
	v_ashrrev_i32_e32 v20, 3, v1
	v_lshlrev_b32_e32 v1, 4, v1
	v_lshlrev_b32_e32 v10, 2, v21
	v_mul_u32_u24_e32 v22, 0x204, v22
	v_add3_u32 v22, 0, v10, v22
	v_and_b32_e32 v10, 0x70, v1
	v_mul_lo_u32 v23, v20, s38
	s_ashr_i32 s25, s24, 31
	v_lshlrev_b32_e32 v1, 2, v10
	s_lshl_b64 s[24:25], s[24:25], 12
	v_add3_u32 v1, 0, v23, v1
	v_add_u32_e32 v24, 0x400, v22
	s_add_u32 s14, s14, s24
	s_barrier
	s_addc_u32 s25, s29, s25
	s_lshl_b32 s24, s28, 1
	v_ashrrev_i32_e32 v21, 31, v20
	s_add_u32 s24, s14, s24
	v_lshlrev_b64 v[20:21], 12, v[20:21]
	s_addc_u32 s25, s25, 0
	s_waitcnt vmcnt(2)
	ds_write2_b32 v22, v2, v6 offset1:32
	ds_write2_b32 v22, v3, v7 offset0:129 offset1:161
	ds_write2_b32 v24, v4, v8 offset0:2 offset1:34
	ds_write2_b32 v24, v5, v9 offset0:131 offset1:163
	s_waitcnt vmcnt(0)
	ds_write2_b32 v22, v12, v16 offset0:64 offset1:96
	ds_write2_b32 v22, v13, v17 offset0:193 offset1:225
	ds_write2_b32 v24, v14, v18 offset0:66 offset1:98
	ds_write2_b32 v24, v15, v19 offset0:195 offset1:227
	s_waitcnt lgkmcnt(0)
	s_barrier
	ds_read2_b32 v[2:3], v1 offset1:1
	ds_read2_b32 v[4:5], v1 offset0:2 offset1:3
	ds_read2_b32 v[6:7], v1 offset0:4 offset1:5
	ds_read2_b32 v[8:9], v1 offset0:6 offset1:7
	ds_read2_b32 v[12:13], v1 offset0:8 offset1:9
	ds_read2_b32 v[14:15], v1 offset0:10 offset1:11
	ds_read2_b32 v[16:17], v1 offset0:12 offset1:13
	ds_read2_b32 v[18:19], v1 offset0:14 offset1:15
	s_waitcnt lgkmcnt(7)
	v_cvt_pk_bf16_f32 v2, v2, v3
	s_waitcnt lgkmcnt(6)
	v_cvt_pk_bf16_f32 v3, v4, v5
	s_waitcnt lgkmcnt(5)
	v_cvt_pk_bf16_f32 v4, v6, v7
	s_waitcnt lgkmcnt(3)
	v_cvt_pk_bf16_f32 v6, v12, v13
	v_lshl_add_u64 v[12:13], s[24:25], 0, v[20:21]
	v_cvt_pk_bf16_f32 v5, v8, v9
	s_waitcnt lgkmcnt(2)
	v_cvt_pk_bf16_f32 v7, v14, v15
	s_waitcnt lgkmcnt(1)
	v_cvt_pk_bf16_f32 v8, v16, v17
	s_waitcnt lgkmcnt(0)
	v_cvt_pk_bf16_f32 v9, v18, v19
	s_branch .LBB0_1458

.LBB0_1609:
	s_or_b64 exec, exec, s[24:25]
	s_waitcnt lgkmcnt(0)
	s_barrier
	ds_read_b32 v1, v11 offset:40960
	s_mov_b64 s[24:25], -1
	s_waitcnt lgkmcnt(0)
	v_cmp_lt_u32_e32 vcc, s17, v1
	v_readfirstlane_b32 s28, v1
	s_cbranch_vccnz .LBB0_1602
	s_cmpk_lt_u32 s28, 0x4a00
	s_cbranch_scc0 .LBB0_1618
	s_cmpk_gt_u32 s28, 0x41ff
	s_cbranch_scc0 .LBB0_1617
	s_cmpk_gt_u32 s28, 0x47ff
	s_cbranch_scc0 .LBB0_1614
	s_add_i32 s12, s28, 0xffffb800
	s_lshr_b32 s20, s12, 4
	s_lshl_b32 s21, s20, 11
	s_lshl_b32 s12, s12, 7
	s_sub_i32 s24, s12, s21
	s_ashr_i32 s25, s24, 31
	s_lshl_b32 s12, s20, 6
	s_lshl_b64 s[20:21], s[24:25], 13
	s_add_u32 s26, s14, s20
	v_mov_b32_e32 v1, v0
	s_addc_u32 s27, s15, s21
	s_lshl_b64 s[20:21], s[12:13], 2
	s_add_u32 s20, s26, s20
	v_lshlrev_b32_e32 v2, 2, v1
	v_ashrrev_i32_e32 v12, 4, v1
	v_and_b32_e32 v24, 60, v2
	s_addc_u32 s21, s27, s21
	v_lshlrev_b32_e32 v10, 2, v24
	v_ashrrev_i32_e32 v13, 31, v12
	v_lshl_add_u64 v[2:3], s[20:21], 0, v[10:11]
	v_lshlrev_b64 v[4:5], 13, v[12:13]
	v_lshl_add_u64 v[14:15], v[2:3], 0, v[4:5]
	v_add_co_u32_e32 v6, vcc, s18, v14
	v_ashrrev_i32_e32 v22, 3, v1
	s_nop 0
	v_addc_co_u32_e32 v7, vcc, 0, v15, vcc
	v_add_co_u32_e32 v16, vcc, s19, v14
	global_load_dwordx4 v[2:5], v[14:15], off nt
	s_nop 0
	global_load_dwordx4 v[6:9], v[6:7], off nt
	v_addc_co_u32_e32 v17, vcc, 0, v15, vcc
	v_add_co_u32_e32 v18, vcc, s30, v14
	v_lshlrev_b32_e32 v1, 4, v1
	s_nop 0
	v_addc_co_u32_e32 v19, vcc, 0, v15, vcc
	global_load_dwordx4 v[14:17], v[16:17], off nt
	s_nop 0
	global_load_dwordx4 v[18:21], v[18:19], off nt
	v_lshlrev_b32_e32 v10, 2, v12
	v_ashrrev_i32_e32 v23, 31, v22
	v_mul_u32_u24_e32 v24, 0x204, v24
	v_mul_lo_u32 v25, v22, s31
	v_lshlrev_b64 v[12:13], 12, v[22:23]
	v_add3_u32 v22, 0, v10, v24
	v_and_b32_e32 v10, 0x70, v1
	v_lshlrev_b32_e32 v1, 2, v10
	v_add3_u32 v1, 0, v25, v1
	v_add_u32_e32 v23, 0x400, v22
	s_lshl_b64 s[20:21], s[12:13], 12
	s_waitcnt vmcnt(63) expcnt(7) lgkmcnt(15)
	s_barrier
	s_add_u32 s12, s0, s20
	s_addc_u32 s26, s1, s21
	s_lshl_b64 s[20:21], s[24:25], 1
	s_add_u32 s20, s12, s20
	s_addc_u32 s21, s26, s21
	v_lshl_add_u64 v[12:13], s[20:21], 0, v[12:13]
	s_mov_b64 s[24:25], 0
	s_waitcnt vmcnt(2)
	ds_write2_b32 v22, v2, v6 offset1:32
	ds_write2_b32 v22, v3, v7 offset0:129 offset1:161
	ds_write2_b32 v23, v4, v8 offset0:2 offset1:34
	ds_write2_b32 v23, v5, v9 offset0:131 offset1:163
	s_waitcnt vmcnt(0)
	ds_write2_b32 v22, v14, v18 offset0:64 offset1:96
	ds_write2_b32 v22, v15, v19 offset0:193 offset1:225
	ds_write2_b32 v23, v16, v20 offset0:66 offset1:98
	ds_write2_b32 v23, v17, v21 offset0:195 offset1:227
	s_waitcnt lgkmcnt(0)
	s_barrier
	ds_read2_b32 v[2:3], v1 offset1:1
	ds_read2_b32 v[4:5], v1 offset0:2 offset1:3
	ds_read2_b32 v[6:7], v1 offset0:4 offset1:5
	ds_read2_b32 v[8:9], v1 offset0:6 offset1:7
	ds_read2_b32 v[14:15], v1 offset0:8 offset1:9
	ds_read2_b32 v[16:17], v1 offset0:10 offset1:11
	ds_read2_b32 v[18:19], v1 offset0:12 offset1:13
	ds_read2_b32 v[20:21], v1 offset0:14 offset1:15
	s_waitcnt lgkmcnt(7)
	v_cvt_pk_bf16_f32 v2, v2, v3
	s_waitcnt lgkmcnt(6)
	v_cvt_pk_bf16_f32 v3, v4, v5
	s_waitcnt lgkmcnt(5)
	v_cvt_pk_bf16_f32 v4, v6, v7
	s_waitcnt lgkmcnt(4)
	v_cvt_pk_bf16_f32 v5, v8, v9
	s_waitcnt lgkmcnt(3)
	v_cvt_pk_bf16_f32 v6, v14, v15
	s_waitcnt lgkmcnt(2)
	v_cvt_pk_bf16_f32 v7, v16, v17
	s_waitcnt lgkmcnt(1)
	v_cvt_pk_bf16_f32 v8, v18, v19
	s_waitcnt lgkmcnt(0)
	v_cvt_pk_bf16_f32 v9, v20, v21
.LBB0_1614:
	s_andn2_b64 vcc, exec, s[24:25]
	s_cbranch_vccnz .LBB0_1616
	s_add_i32 s12, s28, 0xffffbe00
	s_lshr_b32 s20, s12, 4
	s_lshl_b32 s21, s20, 11
	s_lshl_b32 s12, s12, 7
	s_sub_i32 s24, s12, s21
	s_ashr_i32 s25, s24, 31
	s_lshl_b32 s12, s20, 6
	s_mul_i32 s21, s24, 0x6000
	v_readlane_b32 s26, v253, 17
	s_mul_hi_i32 s20, s24, 0x6000
	v_readlane_b32 s27, v253, 18
	s_add_u32 s26, s26, s21
	v_mov_b32_e32 v1, v0
	s_addc_u32 s27, s27, s20
	s_lshl_b64 s[20:21], s[12:13], 2
	s_add_u32 s20, s26, s20
	v_lshlrev_b32_e32 v2, 2, v1
	v_and_b32_e32 v22, 60, v2
	s_addc_u32 s21, s27, s21
	v_ashrrev_i32_e32 v21, 4, v1
	v_lshlrev_b32_e32 v10, 2, v22
	v_lshl_add_u64 v[12:13], s[20:21], 0, v[10:11]
	v_add_u32_e32 v10, 64, v21
	v_add_u32_e32 v4, 32, v21
	v_mad_i64_i32 v[14:15], s[20:21], v10, s33, v[12:13]
	v_add_u32_e32 v10, 0x60, v21
	v_mad_i64_i32 v[2:3], s[20:21], v21, s33, v[12:13]
	v_mad_i64_i32 v[6:7], s[20:21], v4, s33, v[12:13]
	v_mad_i64_i32 v[16:17], s[20:21], v10, s33, v[12:13]
	global_load_dwordx4 v[2:5], v[2:3], off nt
	s_nop 0
	global_load_dwordx4 v[6:9], v[6:7], off nt
	s_nop 0
	global_load_dwordx4 v[12:15], v[14:15], off nt
	s_nop 0
	global_load_dwordx4 v[16:19], v[16:17], off nt
	v_ashrrev_i32_e32 v20, 3, v1
	v_lshlrev_b32_e32 v1, 4, v1
	v_lshlrev_b32_e32 v10, 2, v21
	v_mul_u32_u24_e32 v22, 0x204, v22
	v_add3_u32 v22, 0, v10, v22
	v_and_b32_e32 v10, 0x70, v1
	v_mul_lo_u32 v23, v20, s31
	v_lshlrev_b32_e32 v1, 2, v10
	s_lshl_b64 s[20:21], s[12:13], 12
	v_add3_u32 v1, 0, v23, v1
	v_add_u32_e32 v24, 0x400, v22
	s_add_u32 s12, s3, s20
	s_waitcnt vmcnt(63) expcnt(7) lgkmcnt(15)
	s_barrier
	s_addc_u32 s26, s4, s21
	s_lshl_b64 s[20:21], s[24:25], 1
	v_ashrrev_i32_e32 v21, 31, v20
	s_add_u32 s20, s12, s20
	v_lshlrev_b64 v[20:21], 12, v[20:21]
	s_addc_u32 s21, s26, s21
	s_waitcnt vmcnt(2)
	ds_write2_b32 v22, v2, v6 offset1:32
	ds_write2_b32 v22, v3, v7 offset0:129 offset1:161
	ds_write2_b32 v24, v4, v8 offset0:2 offset1:34
	ds_write2_b32 v24, v5, v9 offset0:131 offset1:163
	s_waitcnt vmcnt(0)
	ds_write2_b32 v22, v12, v16 offset0:64 offset1:96
	ds_write2_b32 v22, v13, v17 offset0:193 offset1:225
	ds_write2_b32 v24, v14, v18 offset0:66 offset1:98
	ds_write2_b32 v24, v15, v19 offset0:195 offset1:227
	s_waitcnt lgkmcnt(0)
	s_barrier
	ds_read2_b32 v[2:3], v1 offset1:1
	ds_read2_b32 v[4:5], v1 offset0:2 offset1:3
	ds_read2_b32 v[6:7], v1 offset0:4 offset1:5
	ds_read2_b32 v[8:9], v1 offset0:6 offset1:7
	ds_read2_b32 v[12:13], v1 offset0:8 offset1:9
	ds_read2_b32 v[14:15], v1 offset0:10 offset1:11
	ds_read2_b32 v[16:17], v1 offset0:12 offset1:13
	ds_read2_b32 v[18:19], v1 offset0:14 offset1:15
	s_waitcnt lgkmcnt(7)
	v_cvt_pk_bf16_f32 v2, v2, v3
	s_waitcnt lgkmcnt(6)
	v_cvt_pk_bf16_f32 v3, v4, v5
	s_waitcnt lgkmcnt(5)
	v_cvt_pk_bf16_f32 v4, v6, v7
	s_waitcnt lgkmcnt(3)
	v_cvt_pk_bf16_f32 v6, v12, v13
	v_lshl_add_u64 v[12:13], s[20:21], 0, v[20:21]
	v_cvt_pk_bf16_f32 v5, v8, v9
	s_waitcnt lgkmcnt(2)
	v_cvt_pk_bf16_f32 v7, v14, v15
	s_waitcnt lgkmcnt(1)
	v_cvt_pk_bf16_f32 v8, v16, v17
	s_waitcnt lgkmcnt(0)
	v_cvt_pk_bf16_f32 v9, v18, v19

.LBB0_1620:
	s_andn2_b64 vcc, exec, s[24:25]
	s_cbranch_vccnz .LBB0_1601
	s_cmpk_gt_u32 s28, 0x2bff
	s_mov_b64 s[24:25], -1
	s_cbranch_scc0 .LBB0_1623
	s_add_i32 s20, s28, 0xffffd400
	s_mul_i32 s21, s20, 0xba2f
	s_lshr_b32 s21, s21, 24
	s_mul_i32 s24, s21, 0xfffffea0
	s_add_i32 s21, s12, s21
	s_add_i32 s20, s24, s20
	s_mul_i32 s25, s21, 0xb00000
	v_readlane_b32 s26, v253, 19
	s_mul_hi_u32 s24, s21, 0xb00000
	v_readlane_b32 s27, v253, 20
	s_add_u32 s29, s26, s25
	s_addc_u32 s36, s27, s24
	s_mul_i32 s21, s21, 0x580000
	s_add_u32 s37, s5, s21
	s_mul_i32 s21, s20, 0x1746
	s_addc_u32 s38, s10, 0
	s_lshr_b32 s24, s21, 31
	s_lshr_b32 s21, s21, 16
	s_add_i32 s21, s21, s24
	s_sext_i32_i16 s39, s21
	s_mul_i32 s21, s39, -11
	s_add_i32 s21, s21, s20
	s_lshl_b32 s20, s21, 7
	s_ashr_i32 s21, s20, 31
	s_lshl_b32 s24, s39, 6
	s_ashr_i32 s25, s24, 31
	s_lshl_b64 s[26:27], s[20:21], 13
	s_add_u32 s29, s29, s26
	v_mov_b32_e32 v1, v0
	s_addc_u32 s36, s36, s27
	s_lshl_b64 s[26:27], s[24:25], 2
	s_add_u32 s26, s29, s26
	v_lshlrev_b32_e32 v2, 2, v1
	v_ashrrev_i32_e32 v12, 4, v1
	v_and_b32_e32 v22, 60, v2
	s_addc_u32 s27, s36, s27
	v_lshlrev_b32_e32 v10, 2, v22
	v_ashrrev_i32_e32 v13, 31, v12
	v_lshl_add_u64 v[2:3], s[26:27], 0, v[10:11]
	v_lshlrev_b64 v[4:5], 13, v[12:13]
	v_lshl_add_u64 v[14:15], v[2:3], 0, v[4:5]
	v_add_co_u32_e32 v6, vcc, s18, v14
	v_ashrrev_i32_e32 v23, 3, v1
	s_nop 0
	v_addc_co_u32_e32 v7, vcc, 0, v15, vcc
	v_add_co_u32_e32 v16, vcc, s19, v14
	global_load_dwordx4 v[2:5], v[14:15], off nt
	s_nop 0
	global_load_dwordx4 v[6:9], v[6:7], off nt
	v_addc_co_u32_e32 v17, vcc, 0, v15, vcc
	v_add_co_u32_e32 v18, vcc, s30, v14
	v_lshlrev_b32_e32 v1, 4, v1
	s_nop 0
	v_addc_co_u32_e32 v19, vcc, 0, v15, vcc
	global_load_dwordx4 v[14:17], v[16:17], off nt
	s_nop 0
	global_load_dwordx4 v[18:21], v[18:19], off nt
	v_lshlrev_b32_e32 v10, 2, v12
	v_mul_u32_u24_e32 v13, 0x204, v22
	v_add3_u32 v22, 0, v10, v13
	v_and_b32_e32 v10, 0x70, v1
	v_mul_lo_u32 v12, v23, s31
	v_lshlrev_b32_e32 v1, 2, v10
	s_mul_i32 s39, s39, 0x2c000
	v_add3_u32 v1, 0, v12, v1
	v_add_u32_e32 v24, 0x400, v22
	s_mul_hi_i32 s24, s24, 0xb00
	s_add_u32 s25, s37, s39
	s_waitcnt vmcnt(63) expcnt(7) lgkmcnt(15)
	s_barrier
	s_addc_u32 s24, s38, s24
	s_lshl_b64 s[20:21], s[20:21], 1
	s_add_u32 s20, s25, s20
	s_addc_u32 s21, s24, s21
	v_mov_b64_e32 v[12:13], s[20:21]
	v_mad_i64_i32 v[12:13], s[20:21], v23, s34, v[12:13]
	s_mov_b64 s[24:25], 0
	s_waitcnt vmcnt(2)
	ds_write2_b32 v22, v2, v6 offset1:32
	ds_write2_b32 v22, v3, v7 offset0:129 offset1:161
	ds_write2_b32 v24, v4, v8 offset0:2 offset1:34
	ds_write2_b32 v24, v5, v9 offset0:131 offset1:163
	s_waitcnt vmcnt(0)
	ds_write2_b32 v22, v14, v18 offset0:64 offset1:96
	ds_write2_b32 v22, v15, v19 offset0:193 offset1:225
	ds_write2_b32 v24, v16, v20 offset0:66 offset1:98
	ds_write2_b32 v24, v17, v21 offset0:195 offset1:227
	s_waitcnt lgkmcnt(0)
	s_barrier
	ds_read2_b32 v[2:3], v1 offset1:1
	ds_read2_b32 v[4:5], v1 offset0:2 offset1:3
	ds_read2_b32 v[6:7], v1 offset0:4 offset1:5
	ds_read2_b32 v[8:9], v1 offset0:6 offset1:7
	ds_read2_b32 v[14:15], v1 offset0:8 offset1:9
	ds_read2_b32 v[16:17], v1 offset0:10 offset1:11
	ds_read2_b32 v[18:19], v1 offset0:12 offset1:13
	ds_read2_b32 v[20:21], v1 offset0:14 offset1:15
	s_waitcnt lgkmcnt(7)
	v_cvt_pk_bf16_f32 v2, v2, v3
	s_waitcnt lgkmcnt(6)
	v_cvt_pk_bf16_f32 v3, v4, v5
	s_waitcnt lgkmcnt(5)
	v_cvt_pk_bf16_f32 v4, v6, v7
	s_waitcnt lgkmcnt(4)
	v_cvt_pk_bf16_f32 v5, v8, v9
	s_waitcnt lgkmcnt(3)
	v_cvt_pk_bf16_f32 v6, v14, v15
	s_waitcnt lgkmcnt(2)
	v_cvt_pk_bf16_f32 v7, v16, v17
	s_waitcnt lgkmcnt(1)
	v_cvt_pk_bf16_f32 v8, v18, v19
	s_waitcnt lgkmcnt(0)
	v_cvt_pk_bf16_f32 v9, v20, v21
.LBB0_1623:
	s_andn2_b64 vcc, exec, s[24:25]
	s_cbranch_vccnz .LBB0_1601
	s_mul_i32 s20, s28, 0xba2f
	s_lshr_b32 s20, s20, 25
	s_mul_i32 s21, s20, 0xfffffd40
	s_add_i32 s21, s21, s28
	s_mul_i32 s24, s21, 0xba3
	s_lshr_b32 s25, s24, 31
	s_ashr_i32 s24, s24, 20
	s_add_i32 s24, s24, s25
	s_sext_i32_i16 s24, s24
	s_mul_i32 s25, s24, 0xfffffea0
	s_add_i32 s25, s25, s21
	s_add_i32 s12, s12, s20
	s_addk_i32 s21, 0x15f
	v_readlane_b32 s36, v253, 13
	s_cmpk_lt_u32 s21, 0x2bf
	v_readlane_b32 s38, v253, 15
	v_readlane_b32 s37, v253, 14
	v_readlane_b32 s39, v253, 16
	s_cselect_b32 s21, s36, s38
	s_mul_i32 s12, s12, 0xb00000
	s_cselect_b32 s20, s37, s39
	s_add_u32 s21, s21, s12
	s_addc_u32 s26, s20, 0
	s_lshl_b32 s27, s25, 2
	s_lshl_b32 s25, s25, 3
	s_and_b32 s25, s25, 0xffffff00
	s_lshl_b32 s24, s24, 7
	s_add_i32 s25, s25, s24
	s_and_b32 s24, s27, 64
	s_and_b32 s20, s27, 0xffffffc0
	s_or_b32 s24, s25, s24
	s_add_u32 s12, s11, s12
	s_addc_u32 s27, s16, 0
	s_lshl_b32 s25, s28, 7
	s_and_b32 s28, s25, 0x780
	s_mul_i32 s25, s28, 0x1600
	s_add_u32 s25, s21, s25
	s_addc_u32 s26, s26, 0
	s_ashr_i32 s21, s20, 31
	v_mov_b32_e32 v1, v0
	s_lshl_b64 s[20:21], s[20:21], 2
	s_add_u32 s20, s25, s20
	v_lshlrev_b32_e32 v2, 2, v1
	v_and_b32_e32 v22, 60, v2
	s_addc_u32 s21, s26, s21
	v_ashrrev_i32_e32 v21, 4, v1
	v_lshlrev_b32_e32 v10, 2, v22
	v_lshl_add_u64 v[12:13], s[20:21], 0, v[10:11]
	v_add_u32_e32 v10, 64, v21
	v_add_u32_e32 v4, 32, v21
	v_mad_i64_i32 v[14:15], s[20:21], v10, s35, v[12:13]
	v_add_u32_e32 v10, 0x60, v21
	v_mad_i64_i32 v[2:3], s[20:21], v21, s35, v[12:13]
	v_mad_i64_i32 v[6:7], s[20:21], v4, s35, v[12:13]
	v_mad_i64_i32 v[16:17], s[20:21], v10, s35, v[12:13]
	global_load_dwordx4 v[2:5], v[2:3], off nt
	s_nop 0
	global_load_dwordx4 v[6:9], v[6:7], off nt
	s_nop 0
	global_load_dwordx4 v[12:15], v[14:15], off nt
	s_nop 0
	global_load_dwordx4 v[16:19], v[16:17], off nt
	v_ashrrev_i32_e32 v20, 3, v1
	v_lshlrev_b32_e32 v1, 4, v1
	v_lshlrev_b32_e32 v10, 2, v21
	v_mul_u32_u24_e32 v22, 0x204, v22
	v_add3_u32 v22, 0, v10, v22
	v_and_b32_e32 v10, 0x70, v1
	v_mul_lo_u32 v23, v20, s31
	s_ashr_i32 s25, s24, 31
	v_lshlrev_b32_e32 v1, 2, v10
	s_lshl_b64 s[20:21], s[24:25], 12
	v_add3_u32 v1, 0, v23, v1
	v_add_u32_e32 v24, 0x400, v22
	s_add_u32 s12, s12, s20
	s_waitcnt vmcnt(63) expcnt(7) lgkmcnt(15)
	s_barrier
	s_addc_u32 s21, s27, s21
	s_lshl_b32 s20, s28, 1
	v_ashrrev_i32_e32 v21, 31, v20
	s_add_u32 s20, s12, s20
	v_lshlrev_b64 v[20:21], 12, v[20:21]
	s_addc_u32 s21, s21, 0
	s_waitcnt vmcnt(2)
	ds_write2_b32 v22, v2, v6 offset1:32
	ds_write2_b32 v22, v3, v7 offset0:129 offset1:161
	ds_write2_b32 v24, v4, v8 offset0:2 offset1:34
	ds_write2_b32 v24, v5, v9 offset0:131 offset1:163
	s_waitcnt vmcnt(0)
	ds_write2_b32 v22, v12, v16 offset0:64 offset1:96
	ds_write2_b32 v22, v13, v17 offset0:193 offset1:225
	ds_write2_b32 v24, v14, v18 offset0:66 offset1:98
	ds_write2_b32 v24, v15, v19 offset0:195 offset1:227
	s_waitcnt lgkmcnt(0)
	s_barrier
	ds_read2_b32 v[2:3], v1 offset1:1
	ds_read2_b32 v[4:5], v1 offset0:2 offset1:3
	ds_read2_b32 v[6:7], v1 offset0:4 offset1:5
	ds_read2_b32 v[8:9], v1 offset0:6 offset1:7
	ds_read2_b32 v[12:13], v1 offset0:8 offset1:9
	ds_read2_b32 v[14:15], v1 offset0:10 offset1:11
	ds_read2_b32 v[16:17], v1 offset0:12 offset1:13
	ds_read2_b32 v[18:19], v1 offset0:14 offset1:15
	s_waitcnt lgkmcnt(7)
	v_cvt_pk_bf16_f32 v2, v2, v3
	s_waitcnt lgkmcnt(6)
	v_cvt_pk_bf16_f32 v3, v4, v5
	s_waitcnt lgkmcnt(5)
	v_cvt_pk_bf16_f32 v4, v6, v7
	s_waitcnt lgkmcnt(3)
	v_cvt_pk_bf16_f32 v6, v12, v13
	v_lshl_add_u64 v[12:13], s[20:21], 0, v[20:21]
	v_cvt_pk_bf16_f32 v5, v8, v9
	s_waitcnt lgkmcnt(2)
	v_cvt_pk_bf16_f32 v7, v14, v15
	s_waitcnt lgkmcnt(1)
	v_cvt_pk_bf16_f32 v8, v16, v17
	s_waitcnt lgkmcnt(0)
	v_cvt_pk_bf16_f32 v9, v18, v19
	s_branch .LBB0_1601

.LBB0_1718:
	s_or_b64 exec, exec, s[24:25]
	s_waitcnt lgkmcnt(0)
	s_barrier
	ds_read_b32 v1, v11 offset:40960
	s_mov_b64 s[24:25], -1
	s_waitcnt lgkmcnt(0)
	v_cmp_lt_u32_e32 vcc, s34, v1
	v_readfirstlane_b32 s28, v1
	s_cbranch_vccnz .LBB0_1711
	s_cmpk_lt_u32 s28, 0x4a00
	s_cbranch_scc0 .LBB0_1727
	s_cmpk_gt_u32 s28, 0x41ff
	s_cbranch_scc0 .LBB0_1726
	s_cmpk_gt_u32 s28, 0x47ff
	s_cbranch_scc0 .LBB0_1723
	s_add_i32 s22, s28, 0xffffb800
	s_lshr_b32 s26, s22, 4
	s_lshl_b32 s24, s26, 11
	s_lshl_b32 s22, s22, 7
	s_sub_i32 s24, s22, s24
	s_ashr_i32 s25, s24, 31
	s_lshl_b32 s22, s26, 6
	s_lshl_b64 s[26:27], s[24:25], 13
	s_add_u32 s29, s16, s26
	v_mov_b32_e32 v1, v0
	s_addc_u32 s42, s17, s27
	s_lshl_b64 s[26:27], s[22:23], 2
	s_add_u32 s26, s29, s26
	v_lshlrev_b32_e32 v2, 2, v1
	v_ashrrev_i32_e32 v12, 4, v1
	v_and_b32_e32 v24, 60, v2
	s_addc_u32 s27, s42, s27
	v_lshlrev_b32_e32 v10, 2, v24
	v_ashrrev_i32_e32 v13, 31, v12
	v_lshl_add_u64 v[2:3], s[26:27], 0, v[10:11]
	v_lshlrev_b64 v[4:5], 13, v[12:13]
	v_lshl_add_u64 v[14:15], v[2:3], 0, v[4:5]
	v_add_co_u32_e32 v6, vcc, s35, v14
	v_ashrrev_i32_e32 v22, 3, v1
	s_nop 0
	v_addc_co_u32_e32 v7, vcc, 0, v15, vcc
	v_add_co_u32_e32 v16, vcc, s36, v14
	global_load_dwordx4 v[2:5], v[14:15], off nt
	s_nop 0
	global_load_dwordx4 v[6:9], v[6:7], off nt
	v_addc_co_u32_e32 v17, vcc, 0, v15, vcc
	v_add_co_u32_e32 v18, vcc, s37, v14
	v_lshlrev_b32_e32 v1, 4, v1
	s_nop 0
	v_addc_co_u32_e32 v19, vcc, 0, v15, vcc
	global_load_dwordx4 v[14:17], v[16:17], off nt
	s_nop 0
	global_load_dwordx4 v[18:21], v[18:19], off nt
	v_lshlrev_b32_e32 v10, 2, v12
	v_ashrrev_i32_e32 v23, 31, v22
	v_mul_u32_u24_e32 v24, 0x204, v24
	v_mul_lo_u32 v25, v22, s38
	v_lshlrev_b64 v[12:13], 12, v[22:23]
	v_add3_u32 v22, 0, v10, v24
	v_and_b32_e32 v10, 0x70, v1
	v_lshlrev_b32_e32 v1, 2, v10
	v_add3_u32 v1, 0, v25, v1
	v_add_u32_e32 v23, 0x400, v22
	s_lshl_b64 s[26:27], s[22:23], 12
	s_waitcnt vmcnt(63) expcnt(7) lgkmcnt(15)
	s_barrier
	s_add_u32 s22, s0, s26
	s_addc_u32 s26, s1, s27
	s_lshl_b64 s[24:25], s[24:25], 1
	s_add_u32 s24, s22, s24
	s_addc_u32 s25, s26, s25
	v_lshl_add_u64 v[12:13], s[24:25], 0, v[12:13]
	s_mov_b64 s[24:25], 0
	s_waitcnt vmcnt(2)
	ds_write2_b32 v22, v2, v6 offset1:32
	ds_write2_b32 v22, v3, v7 offset0:129 offset1:161
	ds_write2_b32 v23, v4, v8 offset0:2 offset1:34
	ds_write2_b32 v23, v5, v9 offset0:131 offset1:163
	s_waitcnt vmcnt(0)
	ds_write2_b32 v22, v14, v18 offset0:64 offset1:96
	ds_write2_b32 v22, v15, v19 offset0:193 offset1:225
	ds_write2_b32 v23, v16, v20 offset0:66 offset1:98
	ds_write2_b32 v23, v17, v21 offset0:195 offset1:227
	s_waitcnt lgkmcnt(0)
	s_barrier
	ds_read2_b32 v[2:3], v1 offset1:1
	ds_read2_b32 v[4:5], v1 offset0:2 offset1:3
	ds_read2_b32 v[6:7], v1 offset0:4 offset1:5
	ds_read2_b32 v[8:9], v1 offset0:6 offset1:7
	ds_read2_b32 v[14:15], v1 offset0:8 offset1:9
	ds_read2_b32 v[16:17], v1 offset0:10 offset1:11
	ds_read2_b32 v[18:19], v1 offset0:12 offset1:13
	ds_read2_b32 v[20:21], v1 offset0:14 offset1:15
	s_waitcnt lgkmcnt(7)
	v_cvt_pk_bf16_f32 v2, v2, v3
	s_waitcnt lgkmcnt(6)
	v_cvt_pk_bf16_f32 v3, v4, v5
	s_waitcnt lgkmcnt(5)
	v_cvt_pk_bf16_f32 v4, v6, v7
	s_waitcnt lgkmcnt(4)
	v_cvt_pk_bf16_f32 v5, v8, v9
	s_waitcnt lgkmcnt(3)
	v_cvt_pk_bf16_f32 v6, v14, v15
	s_waitcnt lgkmcnt(2)
	v_cvt_pk_bf16_f32 v7, v16, v17
	s_waitcnt lgkmcnt(1)
	v_cvt_pk_bf16_f32 v8, v18, v19
	s_waitcnt lgkmcnt(0)
	v_cvt_pk_bf16_f32 v9, v20, v21
.LBB0_1723:
	s_andn2_b64 vcc, exec, s[24:25]
	s_cbranch_vccnz .LBB0_1725
	s_add_i32 s22, s28, 0xffffbe00
	s_lshr_b32 s26, s22, 4
	s_lshl_b32 s24, s26, 11
	s_lshl_b32 s22, s22, 7
	s_sub_i32 s24, s22, s24
	s_ashr_i32 s25, s24, 31
	s_lshl_b32 s22, s26, 6
	s_mul_i32 s27, s24, 0x6000
	s_mul_hi_i32 s26, s24, 0x6000
	s_add_u32 s29, s14, s27
	v_mov_b32_e32 v1, v0
	s_addc_u32 s42, s15, s26
	s_lshl_b64 s[26:27], s[22:23], 2
	s_add_u32 s26, s29, s26
	v_lshlrev_b32_e32 v2, 2, v1
	v_and_b32_e32 v22, 60, v2
	s_addc_u32 s27, s42, s27
	v_ashrrev_i32_e32 v21, 4, v1
	v_lshlrev_b32_e32 v10, 2, v22
	v_lshl_add_u64 v[12:13], s[26:27], 0, v[10:11]
	v_add_u32_e32 v10, 64, v21
	v_add_u32_e32 v4, 32, v21
	v_mad_i64_i32 v[14:15], s[26:27], v10, s39, v[12:13]
	v_add_u32_e32 v10, 0x60, v21
	v_mad_i64_i32 v[2:3], s[26:27], v21, s39, v[12:13]
	v_mad_i64_i32 v[6:7], s[26:27], v4, s39, v[12:13]
	v_mad_i64_i32 v[16:17], s[26:27], v10, s39, v[12:13]
	global_load_dwordx4 v[2:5], v[2:3], off nt
	s_nop 0
	global_load_dwordx4 v[6:9], v[6:7], off nt
	s_nop 0
	global_load_dwordx4 v[12:15], v[14:15], off nt
	s_nop 0
	global_load_dwordx4 v[16:19], v[16:17], off nt
	v_ashrrev_i32_e32 v20, 3, v1
	v_lshlrev_b32_e32 v1, 4, v1
	v_lshlrev_b32_e32 v10, 2, v21
	v_mul_u32_u24_e32 v22, 0x204, v22
	v_add3_u32 v22, 0, v10, v22
	v_and_b32_e32 v10, 0x70, v1
	v_mul_lo_u32 v23, v20, s38
	v_lshlrev_b32_e32 v1, 2, v10
	s_lshl_b64 s[26:27], s[22:23], 12
	v_add3_u32 v1, 0, v23, v1
	v_add_u32_e32 v24, 0x400, v22
	s_add_u32 s22, s3, s26
	s_waitcnt vmcnt(63) expcnt(7) lgkmcnt(15)
	s_barrier
	s_addc_u32 s26, s4, s27
	s_lshl_b64 s[24:25], s[24:25], 1
	v_ashrrev_i32_e32 v21, 31, v20
	s_add_u32 s24, s22, s24
	v_lshlrev_b64 v[20:21], 12, v[20:21]
	s_addc_u32 s25, s26, s25
	s_waitcnt vmcnt(2)
	ds_write2_b32 v22, v2, v6 offset1:32
	ds_write2_b32 v22, v3, v7 offset0:129 offset1:161
	ds_write2_b32 v24, v4, v8 offset0:2 offset1:34
	ds_write2_b32 v24, v5, v9 offset0:131 offset1:163
	s_waitcnt vmcnt(0)
	ds_write2_b32 v22, v12, v16 offset0:64 offset1:96
	ds_write2_b32 v22, v13, v17 offset0:193 offset1:225
	ds_write2_b32 v24, v14, v18 offset0:66 offset1:98
	ds_write2_b32 v24, v15, v19 offset0:195 offset1:227
	s_waitcnt lgkmcnt(0)
	s_barrier
	ds_read2_b32 v[2:3], v1 offset1:1
	ds_read2_b32 v[4:5], v1 offset0:2 offset1:3
	ds_read2_b32 v[6:7], v1 offset0:4 offset1:5
	ds_read2_b32 v[8:9], v1 offset0:6 offset1:7
	ds_read2_b32 v[12:13], v1 offset0:8 offset1:9
	ds_read2_b32 v[14:15], v1 offset0:10 offset1:11
	ds_read2_b32 v[16:17], v1 offset0:12 offset1:13
	ds_read2_b32 v[18:19], v1 offset0:14 offset1:15
	s_waitcnt lgkmcnt(7)
	v_cvt_pk_bf16_f32 v2, v2, v3
	s_waitcnt lgkmcnt(6)
	v_cvt_pk_bf16_f32 v3, v4, v5
	s_waitcnt lgkmcnt(5)
	v_cvt_pk_bf16_f32 v4, v6, v7
	s_waitcnt lgkmcnt(3)
	v_cvt_pk_bf16_f32 v6, v12, v13
	v_lshl_add_u64 v[12:13], s[24:25], 0, v[20:21]
	v_cvt_pk_bf16_f32 v5, v8, v9
	s_waitcnt lgkmcnt(2)
	v_cvt_pk_bf16_f32 v7, v14, v15
	s_waitcnt lgkmcnt(1)
	v_cvt_pk_bf16_f32 v8, v16, v17
	s_waitcnt lgkmcnt(0)
	v_cvt_pk_bf16_f32 v9, v18, v19

.LBB0_1729:
	s_andn2_b64 vcc, exec, s[24:25]
	s_cbranch_vccnz .LBB0_1710
	s_cmpk_gt_u32 s28, 0x2bff
	s_mov_b64 s[24:25], -1
	s_cbranch_scc0 .LBB0_1732
	s_add_i32 s24, s28, 0xffffd400
	s_mul_i32 s25, s24, 0xba2f
	s_lshr_b32 s25, s25, 24
	s_mul_i32 s26, s25, 0xfffffea0
	s_add_i32 s25, s22, s25
	s_add_i32 s24, s26, s24
	s_mul_i32 s27, s25, 0xb00000
	s_mul_hi_u32 s26, s25, 0xb00000
	s_add_u32 s29, s18, s27
	s_addc_u32 s44, s19, s26
	s_mul_i32 s25, s25, 0x580000
	s_add_u32 s45, s5, s25
	s_mul_i32 s25, s24, 0x1746
	s_addc_u32 s46, s30, 0
	s_lshr_b32 s26, s25, 31
	s_lshr_b32 s25, s25, 16
	s_add_i32 s25, s25, s26
	s_sext_i32_i16 s47, s25
	s_mul_i32 s25, s47, -11
	s_add_i32 s25, s25, s24
	s_lshl_b32 s24, s25, 7
	s_ashr_i32 s25, s24, 31
	s_lshl_b32 s26, s47, 6
	s_ashr_i32 s27, s26, 31
	s_lshl_b64 s[42:43], s[24:25], 13
	s_add_u32 s29, s29, s42
	v_mov_b32_e32 v1, v0
	s_addc_u32 s44, s44, s43
	s_lshl_b64 s[42:43], s[26:27], 2
	s_add_u32 s42, s29, s42
	v_lshlrev_b32_e32 v2, 2, v1
	v_ashrrev_i32_e32 v12, 4, v1
	v_and_b32_e32 v22, 60, v2
	s_addc_u32 s43, s44, s43
	v_lshlrev_b32_e32 v10, 2, v22
	v_ashrrev_i32_e32 v13, 31, v12
	v_lshl_add_u64 v[2:3], s[42:43], 0, v[10:11]
	v_lshlrev_b64 v[4:5], 13, v[12:13]
	v_lshl_add_u64 v[14:15], v[2:3], 0, v[4:5]
	v_add_co_u32_e32 v6, vcc, s35, v14
	v_ashrrev_i32_e32 v23, 3, v1
	s_nop 0
	v_addc_co_u32_e32 v7, vcc, 0, v15, vcc
	v_add_co_u32_e32 v16, vcc, s36, v14
	global_load_dwordx4 v[2:5], v[14:15], off nt
	s_nop 0
	global_load_dwordx4 v[6:9], v[6:7], off nt
	v_addc_co_u32_e32 v17, vcc, 0, v15, vcc
	v_add_co_u32_e32 v18, vcc, s37, v14
	v_lshlrev_b32_e32 v1, 4, v1
	s_nop 0
	v_addc_co_u32_e32 v19, vcc, 0, v15, vcc
	global_load_dwordx4 v[14:17], v[16:17], off nt
	s_nop 0
	global_load_dwordx4 v[18:21], v[18:19], off nt
	v_lshlrev_b32_e32 v10, 2, v12
	v_mul_u32_u24_e32 v13, 0x204, v22
	v_add3_u32 v22, 0, v10, v13
	v_and_b32_e32 v10, 0x70, v1
	v_mul_lo_u32 v12, v23, s38
	s_mul_i32 s47, s47, 0x2c000
	v_lshlrev_b32_e32 v1, 2, v10
	s_mul_hi_i32 s26, s26, 0xb00
	s_add_u32 s27, s45, s47
	v_add3_u32 v1, 0, v12, v1
	v_add_u32_e32 v24, 0x400, v22
	s_addc_u32 s26, s46, s26
	s_lshl_b64 s[24:25], s[24:25], 1
	s_waitcnt vmcnt(63) expcnt(7) lgkmcnt(15)
	s_barrier
	s_add_u32 s24, s27, s24
	s_addc_u32 s25, s26, s25
	v_mov_b64_e32 v[12:13], s[24:25]
	v_mad_i64_i32 v[12:13], s[24:25], v23, s40, v[12:13]
	s_mov_b64 s[24:25], 0
	s_waitcnt vmcnt(2)
	ds_write2_b32 v22, v2, v6 offset1:32
	ds_write2_b32 v22, v3, v7 offset0:129 offset1:161
	ds_write2_b32 v24, v4, v8 offset0:2 offset1:34
	ds_write2_b32 v24, v5, v9 offset0:131 offset1:163
	s_waitcnt vmcnt(0)
	ds_write2_b32 v22, v14, v18 offset0:64 offset1:96
	ds_write2_b32 v22, v15, v19 offset0:193 offset1:225
	ds_write2_b32 v24, v16, v20 offset0:66 offset1:98
	ds_write2_b32 v24, v17, v21 offset0:195 offset1:227
	s_waitcnt lgkmcnt(0)
	s_barrier
	ds_read2_b32 v[2:3], v1 offset1:1
	ds_read2_b32 v[4:5], v1 offset0:2 offset1:3
	ds_read2_b32 v[6:7], v1 offset0:4 offset1:5
	ds_read2_b32 v[8:9], v1 offset0:6 offset1:7
	ds_read2_b32 v[14:15], v1 offset0:8 offset1:9
	ds_read2_b32 v[16:17], v1 offset0:10 offset1:11
	ds_read2_b32 v[18:19], v1 offset0:12 offset1:13
	ds_read2_b32 v[20:21], v1 offset0:14 offset1:15
	s_waitcnt lgkmcnt(7)
	v_cvt_pk_bf16_f32 v2, v2, v3
	s_waitcnt lgkmcnt(6)
	v_cvt_pk_bf16_f32 v3, v4, v5
	s_waitcnt lgkmcnt(5)
	v_cvt_pk_bf16_f32 v4, v6, v7
	s_waitcnt lgkmcnt(4)
	v_cvt_pk_bf16_f32 v5, v8, v9
	s_waitcnt lgkmcnt(3)
	v_cvt_pk_bf16_f32 v6, v14, v15
	s_waitcnt lgkmcnt(2)
	v_cvt_pk_bf16_f32 v7, v16, v17
	s_waitcnt lgkmcnt(1)
	v_cvt_pk_bf16_f32 v8, v18, v19
	s_waitcnt lgkmcnt(0)
	v_cvt_pk_bf16_f32 v9, v20, v21

.LBB0_1986:
	s_or_b64 exec, exec, s[12:13]
	s_waitcnt lgkmcnt(0)
	s_barrier
	ds_read_b32 v1, v11 offset:40960
	s_mov_b64 s[12:13], -1
	s_waitcnt lgkmcnt(0)
	v_cmp_lt_u32_e32 vcc, s21, v1
	v_readfirstlane_b32 s16, v1
	s_cbranch_vccnz .LBB0_1979
	s_cmpk_lt_u32 s16, 0x4a00
	s_cbranch_scc0 .LBB0_1995
	s_cmpk_gt_u32 s16, 0x41ff
	s_cbranch_scc0 .LBB0_1994
	s_cmpk_gt_u32 s16, 0x47ff
	s_cbranch_scc0 .LBB0_1991
	s_add_i32 s10, s16, 0xffffb800
	s_lshr_b32 s14, s10, 4
	s_lshl_b32 s12, s14, 11
	s_lshl_b32 s10, s10, 7
	s_sub_i32 s12, s10, s12
	s_ashr_i32 s13, s12, 31
	s_lshl_b32 s10, s14, 6
	s_lshl_b64 s[14:15], s[12:13], 13
	s_add_u32 s17, s72, s14
	v_mov_b32_e32 v1, v0
	s_addc_u32 s29, s73, s15
	s_lshl_b64 s[14:15], s[10:11], 2
	s_add_u32 s14, s17, s14
	v_lshlrev_b32_e32 v2, 2, v1
	v_ashrrev_i32_e32 v12, 4, v1
	v_and_b32_e32 v24, 60, v2
	s_addc_u32 s15, s29, s15
	v_lshlrev_b32_e32 v10, 2, v24
	v_ashrrev_i32_e32 v13, 31, v12
	v_lshl_add_u64 v[2:3], s[14:15], 0, v[10:11]
	v_lshlrev_b64 v[4:5], 13, v[12:13]
	v_lshl_add_u64 v[14:15], v[2:3], 0, v[4:5]
	v_add_co_u32_e32 v6, vcc, s22, v14
	v_ashrrev_i32_e32 v22, 3, v1
	s_nop 0
	v_addc_co_u32_e32 v7, vcc, 0, v15, vcc
	v_add_co_u32_e32 v16, vcc, s23, v14
	global_load_dwordx4 v[2:5], v[14:15], off nt
	s_nop 0
	global_load_dwordx4 v[6:9], v[6:7], off nt
	v_addc_co_u32_e32 v17, vcc, 0, v15, vcc
	v_add_co_u32_e32 v18, vcc, s24, v14
	v_lshlrev_b32_e32 v1, 4, v1
	s_nop 0
	v_addc_co_u32_e32 v19, vcc, 0, v15, vcc
	global_load_dwordx4 v[14:17], v[16:17], off nt
	s_nop 0
	global_load_dwordx4 v[18:21], v[18:19], off nt
	v_lshlrev_b32_e32 v10, 2, v12
	v_ashrrev_i32_e32 v23, 31, v22
	v_mul_u32_u24_e32 v24, 0x204, v24
	v_mul_lo_u32 v25, v22, s25
	v_lshlrev_b64 v[12:13], 12, v[22:23]
	v_add3_u32 v22, 0, v10, v24
	v_and_b32_e32 v10, 0x70, v1
	v_lshlrev_b32_e32 v1, 2, v10
	v_add3_u32 v1, 0, v25, v1
	v_add_u32_e32 v23, 0x400, v22
	s_lshl_b64 s[14:15], s[10:11], 12
	s_waitcnt vmcnt(63) expcnt(7) lgkmcnt(15)
	s_barrier
	s_add_u32 s10, s0, s14
	s_addc_u32 s14, s1, s15
	s_lshl_b64 s[12:13], s[12:13], 1
	s_add_u32 s12, s10, s12
	s_addc_u32 s13, s14, s13
	v_lshl_add_u64 v[12:13], s[12:13], 0, v[12:13]
	s_mov_b64 s[12:13], 0
	s_waitcnt vmcnt(2)
	ds_write2_b32 v22, v2, v6 offset1:32
	ds_write2_b32 v22, v3, v7 offset0:129 offset1:161
	ds_write2_b32 v23, v4, v8 offset0:2 offset1:34
	ds_write2_b32 v23, v5, v9 offset0:131 offset1:163
	s_waitcnt vmcnt(0)
	ds_write2_b32 v22, v14, v18 offset0:64 offset1:96
	ds_write2_b32 v22, v15, v19 offset0:193 offset1:225
	ds_write2_b32 v23, v16, v20 offset0:66 offset1:98
	ds_write2_b32 v23, v17, v21 offset0:195 offset1:227
	s_waitcnt lgkmcnt(0)
	s_barrier
	ds_read2_b32 v[2:3], v1 offset1:1
	ds_read2_b32 v[4:5], v1 offset0:2 offset1:3
	ds_read2_b32 v[6:7], v1 offset0:4 offset1:5
	ds_read2_b32 v[8:9], v1 offset0:6 offset1:7
	ds_read2_b32 v[14:15], v1 offset0:8 offset1:9
	ds_read2_b32 v[16:17], v1 offset0:10 offset1:11
	ds_read2_b32 v[18:19], v1 offset0:12 offset1:13
	ds_read2_b32 v[20:21], v1 offset0:14 offset1:15
	s_waitcnt lgkmcnt(7)
	v_cvt_pk_bf16_f32 v2, v2, v3
	s_waitcnt lgkmcnt(6)
	v_cvt_pk_bf16_f32 v3, v4, v5
	s_waitcnt lgkmcnt(5)
	v_cvt_pk_bf16_f32 v4, v6, v7
	s_waitcnt lgkmcnt(4)
	v_cvt_pk_bf16_f32 v5, v8, v9
	s_waitcnt lgkmcnt(3)
	v_cvt_pk_bf16_f32 v6, v14, v15
	s_waitcnt lgkmcnt(2)
	v_cvt_pk_bf16_f32 v7, v16, v17
	s_waitcnt lgkmcnt(1)
	v_cvt_pk_bf16_f32 v8, v18, v19
	s_waitcnt lgkmcnt(0)
	v_cvt_pk_bf16_f32 v9, v20, v21
.LBB0_1991:
	s_andn2_b64 vcc, exec, s[12:13]
	s_cbranch_vccnz .LBB0_1993
	s_add_i32 s10, s16, 0xffffbe00
	s_lshr_b32 s14, s10, 4
	s_lshl_b32 s12, s14, 11
	s_lshl_b32 s10, s10, 7
	s_sub_i32 s12, s10, s12
	s_ashr_i32 s13, s12, 31
	s_lshl_b32 s10, s14, 6
	s_mul_i32 s15, s12, 0x6000
	s_mul_hi_i32 s14, s12, 0x6000
	s_add_u32 s17, s70, s15
	v_mov_b32_e32 v1, v0
	s_addc_u32 s29, s71, s14
	s_lshl_b64 s[14:15], s[10:11], 2
	s_add_u32 s14, s17, s14
	v_lshlrev_b32_e32 v2, 2, v1
	v_and_b32_e32 v22, 60, v2
	s_addc_u32 s15, s29, s15
	v_ashrrev_i32_e32 v21, 4, v1
	v_lshlrev_b32_e32 v10, 2, v22
	v_lshl_add_u64 v[12:13], s[14:15], 0, v[10:11]
	v_add_u32_e32 v10, 64, v21
	v_add_u32_e32 v4, 32, v21
	v_mad_i64_i32 v[14:15], s[14:15], v10, s26, v[12:13]
	v_add_u32_e32 v10, 0x60, v21
	v_mad_i64_i32 v[2:3], s[14:15], v21, s26, v[12:13]
	v_mad_i64_i32 v[6:7], s[14:15], v4, s26, v[12:13]
	v_mad_i64_i32 v[16:17], s[14:15], v10, s26, v[12:13]
	global_load_dwordx4 v[2:5], v[2:3], off nt
	s_nop 0
	global_load_dwordx4 v[6:9], v[6:7], off nt
	s_nop 0
	global_load_dwordx4 v[12:15], v[14:15], off nt
	s_nop 0
	global_load_dwordx4 v[16:19], v[16:17], off nt
	v_ashrrev_i32_e32 v20, 3, v1
	v_lshlrev_b32_e32 v1, 4, v1
	v_lshlrev_b32_e32 v10, 2, v21
	v_mul_u32_u24_e32 v22, 0x204, v22
	v_add3_u32 v22, 0, v10, v22
	v_and_b32_e32 v10, 0x70, v1
	v_mul_lo_u32 v23, v20, s25
	v_lshlrev_b32_e32 v1, 2, v10
	s_lshl_b64 s[14:15], s[10:11], 12
	v_add3_u32 v1, 0, v23, v1
	v_add_u32_e32 v24, 0x400, v22
	s_add_u32 s10, s3, s14
	s_waitcnt vmcnt(63) expcnt(7) lgkmcnt(15)
	s_barrier
	s_addc_u32 s14, s4, s15
	s_lshl_b64 s[12:13], s[12:13], 1
	v_ashrrev_i32_e32 v21, 31, v20
	s_add_u32 s12, s10, s12
	v_lshlrev_b64 v[20:21], 12, v[20:21]
	s_addc_u32 s13, s14, s13
	s_waitcnt vmcnt(2)
	ds_write2_b32 v22, v2, v6 offset1:32
	ds_write2_b32 v22, v3, v7 offset0:129 offset1:161
	ds_write2_b32 v24, v4, v8 offset0:2 offset1:34
	ds_write2_b32 v24, v5, v9 offset0:131 offset1:163
	s_waitcnt vmcnt(0)
	ds_write2_b32 v22, v12, v16 offset0:64 offset1:96
	ds_write2_b32 v22, v13, v17 offset0:193 offset1:225
	ds_write2_b32 v24, v14, v18 offset0:66 offset1:98
	ds_write2_b32 v24, v15, v19 offset0:195 offset1:227
	s_waitcnt lgkmcnt(0)
	s_barrier
	ds_read2_b32 v[2:3], v1 offset1:1
	ds_read2_b32 v[4:5], v1 offset0:2 offset1:3
	ds_read2_b32 v[6:7], v1 offset0:4 offset1:5
	ds_read2_b32 v[8:9], v1 offset0:6 offset1:7
	ds_read2_b32 v[12:13], v1 offset0:8 offset1:9
	ds_read2_b32 v[14:15], v1 offset0:10 offset1:11
	ds_read2_b32 v[16:17], v1 offset0:12 offset1:13
	ds_read2_b32 v[18:19], v1 offset0:14 offset1:15
	s_waitcnt lgkmcnt(7)
	v_cvt_pk_bf16_f32 v2, v2, v3
	s_waitcnt lgkmcnt(6)
	v_cvt_pk_bf16_f32 v3, v4, v5
	s_waitcnt lgkmcnt(5)
	v_cvt_pk_bf16_f32 v4, v6, v7
	s_waitcnt lgkmcnt(3)
	v_cvt_pk_bf16_f32 v6, v12, v13
	v_lshl_add_u64 v[12:13], s[12:13], 0, v[20:21]
	v_cvt_pk_bf16_f32 v5, v8, v9
	s_waitcnt lgkmcnt(2)
	v_cvt_pk_bf16_f32 v7, v14, v15
	s_waitcnt lgkmcnt(1)
	v_cvt_pk_bf16_f32 v8, v16, v17
	s_waitcnt lgkmcnt(0)
	v_cvt_pk_bf16_f32 v9, v18, v19

.LBB0_1997:
	s_andn2_b64 vcc, exec, s[12:13]
	s_cbranch_vccnz .LBB0_1978
	s_cmpk_gt_u32 s16, 0x2bff
	s_mov_b64 s[12:13], -1
	s_cbranch_scc0 .LBB0_2000
	s_add_i32 s12, s16, 0xffffd400
	s_mul_i32 s13, s12, 0xba2f
	s_lshr_b32 s13, s13, 24
	s_mul_i32 s14, s13, 0xfffffea0
	s_add_i32 s13, s10, s13
	s_add_i32 s12, s14, s12
	s_mul_i32 s15, s13, 0xb00000
	s_mul_hi_u32 s14, s13, 0xb00000
	s_add_u32 s17, s74, s15
	s_addc_u32 s29, s75, s14
	s_mul_i32 s13, s13, 0x580000
	s_add_u32 s33, s5, s13
	s_mul_i32 s13, s12, 0x1746
	s_addc_u32 s34, s18, 0
	s_lshr_b32 s14, s13, 31
	s_lshr_b32 s13, s13, 16
	s_add_i32 s13, s13, s14
	s_sext_i32_i16 s35, s13
	s_mul_i32 s13, s35, -11
	s_add_i32 s13, s13, s12
	s_lshl_b32 s12, s13, 7
	s_ashr_i32 s13, s12, 31
	s_lshl_b32 s14, s35, 6
	s_ashr_i32 s15, s14, 31
	s_lshl_b64 s[30:31], s[12:13], 13
	s_add_u32 s17, s17, s30
	v_mov_b32_e32 v1, v0
	s_addc_u32 s29, s29, s31
	s_lshl_b64 s[30:31], s[14:15], 2
	s_add_u32 s30, s17, s30
	v_lshlrev_b32_e32 v2, 2, v1
	v_ashrrev_i32_e32 v12, 4, v1
	v_and_b32_e32 v22, 60, v2
	s_addc_u32 s31, s29, s31
	v_lshlrev_b32_e32 v10, 2, v22
	v_ashrrev_i32_e32 v13, 31, v12
	v_lshl_add_u64 v[2:3], s[30:31], 0, v[10:11]
	v_lshlrev_b64 v[4:5], 13, v[12:13]
	v_lshl_add_u64 v[14:15], v[2:3], 0, v[4:5]
	v_add_co_u32_e32 v6, vcc, s22, v14
	v_ashrrev_i32_e32 v23, 3, v1
	s_nop 0
	v_addc_co_u32_e32 v7, vcc, 0, v15, vcc
	v_add_co_u32_e32 v16, vcc, s23, v14
	global_load_dwordx4 v[2:5], v[14:15], off nt
	s_nop 0
	global_load_dwordx4 v[6:9], v[6:7], off nt
	v_addc_co_u32_e32 v17, vcc, 0, v15, vcc
	v_add_co_u32_e32 v18, vcc, s24, v14
	v_lshlrev_b32_e32 v1, 4, v1
	s_nop 0
	v_addc_co_u32_e32 v19, vcc, 0, v15, vcc
	global_load_dwordx4 v[14:17], v[16:17], off nt
	s_nop 0
	global_load_dwordx4 v[18:21], v[18:19], off nt
	v_lshlrev_b32_e32 v10, 2, v12
	v_mul_u32_u24_e32 v13, 0x204, v22
	v_add3_u32 v22, 0, v10, v13
	v_and_b32_e32 v10, 0x70, v1
	v_mul_lo_u32 v12, v23, s25
	s_mul_i32 s35, s35, 0x2c000
	v_lshlrev_b32_e32 v1, 2, v10
	s_mul_hi_i32 s14, s14, 0xb00
	s_add_u32 s15, s33, s35
	v_add3_u32 v1, 0, v12, v1
	v_add_u32_e32 v24, 0x400, v22
	s_addc_u32 s14, s34, s14
	s_lshl_b64 s[12:13], s[12:13], 1
	s_waitcnt vmcnt(63) expcnt(7) lgkmcnt(15)
	s_barrier
	s_add_u32 s12, s15, s12
	s_addc_u32 s13, s14, s13
	v_mov_b64_e32 v[12:13], s[12:13]
	v_mad_i64_i32 v[12:13], s[12:13], v23, s27, v[12:13]
	s_mov_b64 s[12:13], 0
	s_waitcnt vmcnt(2)
	ds_write2_b32 v22, v2, v6 offset1:32
	ds_write2_b32 v22, v3, v7 offset0:129 offset1:161
	ds_write2_b32 v24, v4, v8 offset0:2 offset1:34
	ds_write2_b32 v24, v5, v9 offset0:131 offset1:163
	s_waitcnt vmcnt(0)
	ds_write2_b32 v22, v14, v18 offset0:64 offset1:96
	ds_write2_b32 v22, v15, v19 offset0:193 offset1:225
	ds_write2_b32 v24, v16, v20 offset0:66 offset1:98
	ds_write2_b32 v24, v17, v21 offset0:195 offset1:227
	s_waitcnt lgkmcnt(0)
	s_barrier
	ds_read2_b32 v[2:3], v1 offset1:1
	ds_read2_b32 v[4:5], v1 offset0:2 offset1:3
	ds_read2_b32 v[6:7], v1 offset0:4 offset1:5
	ds_read2_b32 v[8:9], v1 offset0:6 offset1:7
	ds_read2_b32 v[14:15], v1 offset0:8 offset1:9
	ds_read2_b32 v[16:17], v1 offset0:10 offset1:11
	ds_read2_b32 v[18:19], v1 offset0:12 offset1:13
	ds_read2_b32 v[20:21], v1 offset0:14 offset1:15
	s_waitcnt lgkmcnt(7)
	v_cvt_pk_bf16_f32 v2, v2, v3
	s_waitcnt lgkmcnt(6)
	v_cvt_pk_bf16_f32 v3, v4, v5
	s_waitcnt lgkmcnt(5)
	v_cvt_pk_bf16_f32 v4, v6, v7
	s_waitcnt lgkmcnt(4)
	v_cvt_pk_bf16_f32 v5, v8, v9
	s_waitcnt lgkmcnt(3)
	v_cvt_pk_bf16_f32 v6, v14, v15
	s_waitcnt lgkmcnt(2)
	v_cvt_pk_bf16_f32 v7, v16, v17
	s_waitcnt lgkmcnt(1)
	v_cvt_pk_bf16_f32 v8, v18, v19
	s_waitcnt lgkmcnt(0)
	v_cvt_pk_bf16_f32 v9, v20, v21
.LBB0_2000:
	s_andn2_b64 vcc, exec, s[12:13]
	s_cbranch_vccnz .LBB0_1978
	s_mul_i32 s12, s16, 0xba2f
	s_lshr_b32 s12, s12, 25
	s_mul_i32 s13, s12, 0xfffffd40
	s_add_i32 s13, s13, s16
	s_mul_i32 s14, s13, 0xba3
	s_lshr_b32 s15, s14, 31
	s_ashr_i32 s14, s14, 20
	s_add_i32 s14, s14, s15
	s_sext_i32_i16 s15, s14
	s_mul_i32 s14, s15, 0xfffffea0
	s_add_i32 s17, s14, s13
	s_add_i32 s10, s10, s12
	s_addk_i32 s13, 0x15f
	s_cmpk_lt_u32 s13, 0x2bf
	s_cselect_b32 s13, s56, s58
	s_mul_i32 s10, s10, 0xb00000
	s_cselect_b32 s12, s57, s59
	s_add_u32 s13, s13, s10
	s_addc_u32 s29, s12, 0
	s_lshl_b32 s12, s17, 2
	s_lshl_b32 s17, s17, 3
	s_and_b32 s17, s17, 0xffffff00
	s_lshl_b32 s15, s15, 7
	s_and_b32 s14, s12, 0xffffffc0
	s_add_i32 s17, s17, s15
	s_and_b32 s12, s12, 64
	s_or_b32 s12, s17, s12
	s_add_u32 s10, s19, s10
	s_addc_u32 s17, s20, 0
	s_lshl_b32 s15, s16, 7
	s_and_b32 s16, s15, 0x780
	s_mul_i32 s15, s16, 0x1600
	s_add_u32 s13, s13, s15
	s_addc_u32 s29, s29, 0
	s_ashr_i32 s15, s14, 31
	v_mov_b32_e32 v1, v0
	s_lshl_b64 s[14:15], s[14:15], 2
	s_add_u32 s14, s13, s14
	v_lshlrev_b32_e32 v2, 2, v1
	v_and_b32_e32 v22, 60, v2
	s_addc_u32 s15, s29, s15
	v_ashrrev_i32_e32 v21, 4, v1
	v_lshlrev_b32_e32 v10, 2, v22
	v_lshl_add_u64 v[12:13], s[14:15], 0, v[10:11]
	v_add_u32_e32 v10, 64, v21
	v_add_u32_e32 v4, 32, v21
	v_mad_i64_i32 v[14:15], s[14:15], v10, s28, v[12:13]
	v_add_u32_e32 v10, 0x60, v21
	v_mad_i64_i32 v[2:3], s[14:15], v21, s28, v[12:13]
	v_mad_i64_i32 v[6:7], s[14:15], v4, s28, v[12:13]
	v_mad_i64_i32 v[16:17], s[14:15], v10, s28, v[12:13]
	global_load_dwordx4 v[2:5], v[2:3], off nt
	s_nop 0
	global_load_dwordx4 v[6:9], v[6:7], off nt
	s_nop 0
	global_load_dwordx4 v[12:15], v[14:15], off nt
	s_nop 0
	global_load_dwordx4 v[16:19], v[16:17], off nt
	v_ashrrev_i32_e32 v20, 3, v1
	v_lshlrev_b32_e32 v1, 4, v1
	v_lshlrev_b32_e32 v10, 2, v21
	v_mul_u32_u24_e32 v22, 0x204, v22
	v_add3_u32 v22, 0, v10, v22
	v_and_b32_e32 v10, 0x70, v1
	v_mul_lo_u32 v23, v20, s25
	s_ashr_i32 s13, s12, 31
	v_lshlrev_b32_e32 v1, 2, v10
	s_lshl_b64 s[12:13], s[12:13], 12
	v_add3_u32 v1, 0, v23, v1
	v_add_u32_e32 v24, 0x400, v22
	s_add_u32 s10, s10, s12
	s_waitcnt vmcnt(63) expcnt(7) lgkmcnt(15)
	s_barrier
	s_addc_u32 s13, s17, s13
	s_lshl_b32 s12, s16, 1
	v_ashrrev_i32_e32 v21, 31, v20
	s_add_u32 s12, s10, s12
	v_lshlrev_b64 v[20:21], 12, v[20:21]
	s_addc_u32 s13, s13, 0
	s_waitcnt vmcnt(2)
	ds_write2_b32 v22, v2, v6 offset1:32
	ds_write2_b32 v22, v3, v7 offset0:129 offset1:161
	ds_write2_b32 v24, v4, v8 offset0:2 offset1:34
	ds_write2_b32 v24, v5, v9 offset0:131 offset1:163
	s_waitcnt vmcnt(0)
	ds_write2_b32 v22, v12, v16 offset0:64 offset1:96
	ds_write2_b32 v22, v13, v17 offset0:193 offset1:225
	ds_write2_b32 v24, v14, v18 offset0:66 offset1:98
	ds_write2_b32 v24, v15, v19 offset0:195 offset1:227
	s_waitcnt lgkmcnt(0)
	s_barrier
	ds_read2_b32 v[2:3], v1 offset1:1
	ds_read2_b32 v[4:5], v1 offset0:2 offset1:3
	ds_read2_b32 v[6:7], v1 offset0:4 offset1:5
	ds_read2_b32 v[8:9], v1 offset0:6 offset1:7
	ds_read2_b32 v[12:13], v1 offset0:8 offset1:9
	ds_read2_b32 v[14:15], v1 offset0:10 offset1:11
	ds_read2_b32 v[16:17], v1 offset0:12 offset1:13
	ds_read2_b32 v[18:19], v1 offset0:14 offset1:15
	s_waitcnt lgkmcnt(7)
	v_cvt_pk_bf16_f32 v2, v2, v3
	s_waitcnt lgkmcnt(6)
	v_cvt_pk_bf16_f32 v3, v4, v5
	s_waitcnt lgkmcnt(5)
	v_cvt_pk_bf16_f32 v4, v6, v7
	s_waitcnt lgkmcnt(3)
	v_cvt_pk_bf16_f32 v6, v12, v13
	v_lshl_add_u64 v[12:13], s[12:13], 0, v[20:21]
	v_cvt_pk_bf16_f32 v5, v8, v9
	s_waitcnt lgkmcnt(2)
	v_cvt_pk_bf16_f32 v7, v14, v15
	s_waitcnt lgkmcnt(1)
	v_cvt_pk_bf16_f32 v8, v16, v17
	s_waitcnt lgkmcnt(0)
	v_cvt_pk_bf16_f32 v9, v18, v19
	s_branch .LBB0_1978

.LBB0_2009:
	s_or_b64 exec, exec, s[10:11]
	s_waitcnt lgkmcnt(0)
	s_barrier
	ds_read_b32 v1, v11 offset:40960
	s_mov_b64 s[10:11], -1
	s_waitcnt lgkmcnt(0)
	v_cmp_lt_u32_e32 vcc, s16, v1
	v_readfirstlane_b32 s14, v1
	s_cbranch_vccnz .LBB0_2004
	s_cmpk_lt_u32 s14, 0x4a00
	s_cbranch_scc0 .LBB0_2018
	s_cmpk_gt_u32 s14, 0x41ff
	s_cbranch_scc0 .LBB0_2017
	s_cmpk_gt_u32 s14, 0x47ff
	s_cbranch_scc0 .LBB0_2014
	s_add_i32 s8, s14, 0xffffb800
	s_lshr_b32 s12, s8, 4
	s_lshl_b32 s10, s12, 11
	s_lshl_b32 s8, s8, 7
	s_sub_i32 s10, s8, s10
	s_ashr_i32 s11, s10, 31
	s_lshl_b32 s8, s12, 6
	s_lshl_b64 s[12:13], s[10:11], 13
	s_add_u32 s15, s72, s12
	v_mov_b32_e32 v1, v0
	s_addc_u32 s27, s73, s13
	s_lshl_b64 s[12:13], s[8:9], 2
	s_add_u32 s12, s15, s12
	v_lshlrev_b32_e32 v2, 2, v1
	v_ashrrev_i32_e32 v12, 4, v1
	v_and_b32_e32 v24, 60, v2
	s_addc_u32 s13, s27, s13
	v_lshlrev_b32_e32 v10, 2, v24
	v_ashrrev_i32_e32 v13, 31, v12
	v_lshl_add_u64 v[2:3], s[12:13], 0, v[10:11]
	v_lshlrev_b64 v[4:5], 13, v[12:13]
	v_lshl_add_u64 v[14:15], v[2:3], 0, v[4:5]
	v_add_co_u32_e32 v6, vcc, s17, v14
	v_ashrrev_i32_e32 v22, 3, v1
	s_nop 0
	v_addc_co_u32_e32 v7, vcc, 0, v15, vcc
	v_add_co_u32_e32 v16, vcc, s21, v14
	global_load_dwordx4 v[2:5], v[14:15], off nt
	s_nop 0
	global_load_dwordx4 v[6:9], v[6:7], off nt
	v_addc_co_u32_e32 v17, vcc, 0, v15, vcc
	v_add_co_u32_e32 v18, vcc, s22, v14
	v_lshlrev_b32_e32 v1, 4, v1
	s_nop 0
	v_addc_co_u32_e32 v19, vcc, 0, v15, vcc
	global_load_dwordx4 v[14:17], v[16:17], off nt
	s_nop 0
	global_load_dwordx4 v[18:21], v[18:19], off nt
	v_lshlrev_b32_e32 v10, 2, v12
	v_ashrrev_i32_e32 v23, 31, v22
	v_mul_u32_u24_e32 v24, 0x204, v24
	v_mul_lo_u32 v25, v22, s23
	v_lshlrev_b64 v[12:13], 12, v[22:23]
	v_add3_u32 v22, 0, v10, v24
	v_and_b32_e32 v10, 0x70, v1
	v_lshlrev_b32_e32 v1, 2, v10
	v_add3_u32 v1, 0, v25, v1
	v_add_u32_e32 v23, 0x400, v22
	s_lshl_b64 s[12:13], s[8:9], 12
	s_waitcnt vmcnt(63) expcnt(7) lgkmcnt(15)
	s_barrier
	s_add_u32 s8, s0, s12
	s_addc_u32 s12, s1, s13
	s_lshl_b64 s[10:11], s[10:11], 1
	s_add_u32 s10, s8, s10
	s_addc_u32 s11, s12, s11
	v_lshl_add_u64 v[12:13], s[10:11], 0, v[12:13]
	s_mov_b64 s[10:11], 0
	s_waitcnt vmcnt(2)
	ds_write2_b32 v22, v2, v6 offset1:32
	ds_write2_b32 v22, v3, v7 offset0:129 offset1:161
	ds_write2_b32 v23, v4, v8 offset0:2 offset1:34
	ds_write2_b32 v23, v5, v9 offset0:131 offset1:163
	s_waitcnt vmcnt(0)
	ds_write2_b32 v22, v14, v18 offset0:64 offset1:96
	ds_write2_b32 v22, v15, v19 offset0:193 offset1:225
	ds_write2_b32 v23, v16, v20 offset0:66 offset1:98
	ds_write2_b32 v23, v17, v21 offset0:195 offset1:227
	s_waitcnt lgkmcnt(0)
	s_barrier
	ds_read2_b32 v[2:3], v1 offset1:1
	ds_read2_b32 v[4:5], v1 offset0:2 offset1:3
	ds_read2_b32 v[6:7], v1 offset0:4 offset1:5
	ds_read2_b32 v[8:9], v1 offset0:6 offset1:7
	ds_read2_b32 v[14:15], v1 offset0:8 offset1:9
	ds_read2_b32 v[16:17], v1 offset0:10 offset1:11
	ds_read2_b32 v[18:19], v1 offset0:12 offset1:13
	ds_read2_b32 v[20:21], v1 offset0:14 offset1:15
	s_waitcnt lgkmcnt(7)
	v_cvt_pk_bf16_f32 v2, v2, v3
	s_waitcnt lgkmcnt(6)
	v_cvt_pk_bf16_f32 v3, v4, v5
	s_waitcnt lgkmcnt(5)
	v_cvt_pk_bf16_f32 v4, v6, v7
	s_waitcnt lgkmcnt(4)
	v_cvt_pk_bf16_f32 v5, v8, v9
	s_waitcnt lgkmcnt(3)
	v_cvt_pk_bf16_f32 v6, v14, v15
	s_waitcnt lgkmcnt(2)
	v_cvt_pk_bf16_f32 v7, v16, v17
	s_waitcnt lgkmcnt(1)
	v_cvt_pk_bf16_f32 v8, v18, v19
	s_waitcnt lgkmcnt(0)
	v_cvt_pk_bf16_f32 v9, v20, v21

.LBB0_2020:
	s_andn2_b64 vcc, exec, s[10:11]
	s_cbranch_vccnz .LBB0_2003
	s_cmpk_gt_u32 s8, 0x2bff
	s_mov_b64 s[10:11], -1
	s_cbranch_scc0 .LBB0_2023
	s_add_i32 s10, s8, 0xffffd400
	s_mul_i32 s11, s10, 0xba2f
	s_lshr_b32 s11, s11, 24
	s_mul_i32 s12, s11, 0xfffffea0
	s_add_i32 s11, s15, s11
	s_add_i32 s10, s12, s10
	s_mul_i32 s13, s11, 0xb00000
	s_mul_hi_u32 s12, s11, 0xb00000
	s_add_u32 s27, s74, s13
	s_addc_u32 s30, s75, s12
	s_mul_i32 s11, s11, 0x580000
	s_add_u32 s31, s5, s11
	s_mul_i32 s11, s10, 0x1746
	s_addc_u32 s33, s18, 0
	s_lshr_b32 s12, s11, 31
	s_lshr_b32 s11, s11, 16
	s_add_i32 s11, s11, s12
	s_sext_i32_i16 s34, s11
	s_mul_i32 s11, s34, -11
	s_add_i32 s11, s11, s10
	s_lshl_b32 s10, s11, 7
	s_ashr_i32 s11, s10, 31
	s_lshl_b32 s12, s34, 6
	s_ashr_i32 s13, s12, 31
	s_lshl_b64 s[28:29], s[10:11], 13
	s_add_u32 s27, s27, s28
	v_mov_b32_e32 v1, v0
	s_addc_u32 s30, s30, s29
	s_lshl_b64 s[28:29], s[12:13], 2
	s_add_u32 s28, s27, s28
	v_lshlrev_b32_e32 v2, 2, v1
	v_ashrrev_i32_e32 v12, 4, v1
	v_and_b32_e32 v22, 60, v2
	s_addc_u32 s29, s30, s29
	v_lshlrev_b32_e32 v10, 2, v22
	v_ashrrev_i32_e32 v13, 31, v12
	v_lshl_add_u64 v[2:3], s[28:29], 0, v[10:11]
	v_lshlrev_b64 v[4:5], 13, v[12:13]
	v_lshl_add_u64 v[14:15], v[2:3], 0, v[4:5]
	v_add_co_u32_e32 v6, vcc, s17, v14
	v_ashrrev_i32_e32 v23, 3, v1
	s_nop 0
	v_addc_co_u32_e32 v7, vcc, 0, v15, vcc
	v_add_co_u32_e32 v16, vcc, s21, v14
	global_load_dwordx4 v[2:5], v[14:15], off nt
	s_nop 0
	global_load_dwordx4 v[6:9], v[6:7], off nt
	v_addc_co_u32_e32 v17, vcc, 0, v15, vcc
	v_add_co_u32_e32 v18, vcc, s22, v14
	v_lshlrev_b32_e32 v1, 4, v1
	s_nop 0
	v_addc_co_u32_e32 v19, vcc, 0, v15, vcc
	global_load_dwordx4 v[14:17], v[16:17], off nt
	s_nop 0
	global_load_dwordx4 v[18:21], v[18:19], off nt
	v_lshlrev_b32_e32 v10, 2, v12
	v_mul_u32_u24_e32 v13, 0x204, v22
	v_add3_u32 v22, 0, v10, v13
	v_and_b32_e32 v10, 0x70, v1
	v_mul_lo_u32 v12, v23, s23
	s_mul_i32 s34, s34, 0x2c000
	v_lshlrev_b32_e32 v1, 2, v10
	s_mul_hi_i32 s12, s12, 0xb00
	s_add_u32 s13, s31, s34
	v_add3_u32 v1, 0, v12, v1
	v_add_u32_e32 v24, 0x400, v22
	s_addc_u32 s12, s33, s12
	s_lshl_b64 s[10:11], s[10:11], 1
	s_waitcnt vmcnt(63) expcnt(7) lgkmcnt(15)
	s_barrier
	s_add_u32 s10, s13, s10
	s_addc_u32 s11, s12, s11
	v_mov_b64_e32 v[12:13], s[10:11]
	v_mad_i64_i32 v[12:13], s[10:11], v23, s25, v[12:13]
	s_mov_b64 s[10:11], 0
	s_waitcnt vmcnt(2)
	ds_write2_b32 v22, v2, v6 offset1:32
	ds_write2_b32 v22, v3, v7 offset0:129 offset1:161
	ds_write2_b32 v24, v4, v8 offset0:2 offset1:34
	ds_write2_b32 v24, v5, v9 offset0:131 offset1:163
	s_waitcnt vmcnt(0)
	ds_write2_b32 v22, v14, v18 offset0:64 offset1:96
	ds_write2_b32 v22, v15, v19 offset0:193 offset1:225
	ds_write2_b32 v24, v16, v20 offset0:66 offset1:98
	ds_write2_b32 v24, v17, v21 offset0:195 offset1:227
	s_waitcnt lgkmcnt(0)
	s_barrier
	ds_read2_b32 v[2:3], v1 offset1:1
	ds_read2_b32 v[4:5], v1 offset0:2 offset1:3
	ds_read2_b32 v[6:7], v1 offset0:4 offset1:5
	ds_read2_b32 v[8:9], v1 offset0:6 offset1:7
	ds_read2_b32 v[14:15], v1 offset0:8 offset1:9
	ds_read2_b32 v[16:17], v1 offset0:10 offset1:11
	ds_read2_b32 v[18:19], v1 offset0:12 offset1:13
	ds_read2_b32 v[20:21], v1 offset0:14 offset1:15
	s_waitcnt lgkmcnt(7)
	v_cvt_pk_bf16_f32 v2, v2, v3
	s_waitcnt lgkmcnt(6)
	v_cvt_pk_bf16_f32 v3, v4, v5
	s_waitcnt lgkmcnt(5)
	v_cvt_pk_bf16_f32 v4, v6, v7
	s_waitcnt lgkmcnt(4)
	v_cvt_pk_bf16_f32 v5, v8, v9
	s_waitcnt lgkmcnt(3)
	v_cvt_pk_bf16_f32 v6, v14, v15
	s_waitcnt lgkmcnt(2)
	v_cvt_pk_bf16_f32 v7, v16, v17
	s_waitcnt lgkmcnt(1)
	v_cvt_pk_bf16_f32 v8, v18, v19
	s_waitcnt lgkmcnt(0)
	v_cvt_pk_bf16_f32 v9, v20, v21
.LBB0_2023:
	s_andn2_b64 vcc, exec, s[10:11]
	s_cbranch_vccnz .LBB0_2003
	s_mul_i32 s10, s8, 0xba2f
	s_lshr_b32 s10, s10, 25
	s_mul_i32 s11, s10, 0xfffffd40
	s_add_i32 s11, s11, s8
	s_mul_i32 s12, s11, 0xba3
	s_lshr_b32 s13, s12, 31
	s_ashr_i32 s12, s12, 20
	s_add_i32 s12, s12, s13
	s_sext_i32_i16 s13, s12
	s_mul_i32 s12, s13, 0xfffffea0
	s_add_i32 s27, s12, s11
	s_add_i32 s10, s15, s10
	s_addk_i32 s11, 0x15f
	s_cmpk_lt_u32 s11, 0x2bf
	s_cselect_b32 s12, s56, s58
	s_mul_i32 s15, s10, 0xb00000
	s_cselect_b32 s11, s57, s59
	s_add_u32 s28, s12, s15
	s_addc_u32 s11, s11, 0
	s_lshl_b32 s10, s27, 2
	s_lshl_b32 s27, s27, 3
	s_and_b32 s27, s27, 0xffffff00
	s_lshl_b32 s13, s13, 7
	s_and_b32 s12, s10, 0xffffffc0
	s_add_i32 s27, s27, s13
	s_and_b32 s10, s10, 64
	s_or_b32 s10, s27, s10
	s_add_u32 s15, s19, s15
	s_addc_u32 s27, s20, 0
	s_lshl_b32 s8, s8, 7
	s_and_b32 s8, s8, 0x780
	s_mul_i32 s13, s8, 0x1600
	s_add_u32 s28, s28, s13
	s_addc_u32 s11, s11, 0
	s_ashr_i32 s13, s12, 31
	v_mov_b32_e32 v1, v0
	s_lshl_b64 s[12:13], s[12:13], 2
	s_add_u32 s12, s28, s12
	v_lshlrev_b32_e32 v2, 2, v1
	v_and_b32_e32 v22, 60, v2
	s_addc_u32 s13, s11, s13
	v_ashrrev_i32_e32 v21, 4, v1
	v_lshlrev_b32_e32 v10, 2, v22
	v_lshl_add_u64 v[12:13], s[12:13], 0, v[10:11]
	v_add_u32_e32 v10, 64, v21
	v_add_u32_e32 v4, 32, v21
	v_mad_i64_i32 v[14:15], s[12:13], v10, s26, v[12:13]
	v_add_u32_e32 v10, 0x60, v21
	v_mad_i64_i32 v[2:3], s[12:13], v21, s26, v[12:13]
	v_mad_i64_i32 v[6:7], s[12:13], v4, s26, v[12:13]
	v_mad_i64_i32 v[16:17], s[12:13], v10, s26, v[12:13]
	global_load_dwordx4 v[2:5], v[2:3], off nt
	s_nop 0
	global_load_dwordx4 v[6:9], v[6:7], off nt
	s_nop 0
	global_load_dwordx4 v[12:15], v[14:15], off nt
	s_nop 0
	global_load_dwordx4 v[16:19], v[16:17], off nt
	v_ashrrev_i32_e32 v20, 3, v1
	v_lshlrev_b32_e32 v1, 4, v1
	v_lshlrev_b32_e32 v10, 2, v21
	v_mul_u32_u24_e32 v22, 0x204, v22
	v_add3_u32 v22, 0, v10, v22
	v_and_b32_e32 v10, 0x70, v1
	v_mul_lo_u32 v23, v20, s23
	s_ashr_i32 s11, s10, 31
	v_lshlrev_b32_e32 v1, 2, v10
	s_lshl_b64 s[10:11], s[10:11], 12
	v_add3_u32 v1, 0, v23, v1
	v_add_u32_e32 v24, 0x400, v22
	s_add_u32 s10, s15, s10
	s_waitcnt vmcnt(63) expcnt(7) lgkmcnt(15)
	s_barrier
	s_addc_u32 s11, s27, s11
	s_lshl_b32 s8, s8, 1
	v_ashrrev_i32_e32 v21, 31, v20
	s_add_u32 s10, s10, s8
	v_lshlrev_b64 v[20:21], 12, v[20:21]
	s_addc_u32 s11, s11, 0
	s_waitcnt vmcnt(2)
	ds_write2_b32 v22, v2, v6 offset1:32
	ds_write2_b32 v22, v3, v7 offset0:129 offset1:161
	ds_write2_b32 v24, v4, v8 offset0:2 offset1:34
	ds_write2_b32 v24, v5, v9 offset0:131 offset1:163
	s_waitcnt vmcnt(0)
	ds_write2_b32 v22, v12, v16 offset0:64 offset1:96
	ds_write2_b32 v22, v13, v17 offset0:193 offset1:225
	ds_write2_b32 v24, v14, v18 offset0:66 offset1:98
	ds_write2_b32 v24, v15, v19 offset0:195 offset1:227
	s_waitcnt lgkmcnt(0)
	s_barrier
	ds_read2_b32 v[2:3], v1 offset1:1
	ds_read2_b32 v[4:5], v1 offset0:2 offset1:3
	ds_read2_b32 v[6:7], v1 offset0:4 offset1:5
	ds_read2_b32 v[8:9], v1 offset0:6 offset1:7
	ds_read2_b32 v[12:13], v1 offset0:8 offset1:9
	ds_read2_b32 v[14:15], v1 offset0:10 offset1:11
	ds_read2_b32 v[16:17], v1 offset0:12 offset1:13
	ds_read2_b32 v[18:19], v1 offset0:14 offset1:15
	s_waitcnt lgkmcnt(7)
	v_cvt_pk_bf16_f32 v2, v2, v3
	s_waitcnt lgkmcnt(6)
	v_cvt_pk_bf16_f32 v3, v4, v5
	s_waitcnt lgkmcnt(5)
	v_cvt_pk_bf16_f32 v4, v6, v7
	s_waitcnt lgkmcnt(3)
	v_cvt_pk_bf16_f32 v6, v12, v13
	v_lshl_add_u64 v[12:13], s[10:11], 0, v[20:21]
	v_cvt_pk_bf16_f32 v5, v8, v9
	s_waitcnt lgkmcnt(2)
	v_cvt_pk_bf16_f32 v7, v14, v15
	s_waitcnt lgkmcnt(1)
	v_cvt_pk_bf16_f32 v8, v16, v17
	s_waitcnt lgkmcnt(0)
	v_cvt_pk_bf16_f32 v9, v18, v19
	s_branch .LBB0_2003

.LBB0_2116:
	s_or_b64 exec, exec, s[24:25]
	s_waitcnt lgkmcnt(0)
	s_barrier
	ds_read_b32 v1, v11 offset:40960
	s_mov_b64 s[24:25], -1
	s_waitcnt lgkmcnt(0)
	v_cmp_lt_u32_e32 vcc, s34, v1
	v_readfirstlane_b32 s28, v1
	s_cbranch_vccnz .LBB0_2109
	s_cmpk_lt_u32 s28, 0x4a00
	s_cbranch_scc0 .LBB0_2125
	s_cmpk_gt_u32 s28, 0x41ff
	s_cbranch_scc0 .LBB0_2124
	s_cmpk_gt_u32 s28, 0x47ff
	s_cbranch_scc0 .LBB0_2121
	s_add_i32 s22, s28, 0xffffb800
	s_lshr_b32 s26, s22, 4
	s_lshl_b32 s24, s26, 11
	s_lshl_b32 s22, s22, 7
	s_sub_i32 s24, s22, s24
	s_ashr_i32 s25, s24, 31
	s_lshl_b32 s22, s26, 6
	s_lshl_b64 s[26:27], s[24:25], 13
	s_add_u32 s29, s14, s26
	v_mov_b32_e32 v1, v0
	s_addc_u32 s42, s15, s27
	s_lshl_b64 s[26:27], s[22:23], 2
	s_add_u32 s26, s29, s26
	v_lshlrev_b32_e32 v2, 2, v1
	v_ashrrev_i32_e32 v12, 4, v1
	v_and_b32_e32 v24, 60, v2
	s_addc_u32 s27, s42, s27
	v_lshlrev_b32_e32 v10, 2, v24
	v_ashrrev_i32_e32 v13, 31, v12
	v_lshl_add_u64 v[2:3], s[26:27], 0, v[10:11]
	v_lshlrev_b64 v[4:5], 13, v[12:13]
	v_lshl_add_u64 v[14:15], v[2:3], 0, v[4:5]
	v_add_co_u32_e32 v6, vcc, s35, v14
	v_ashrrev_i32_e32 v22, 3, v1
	s_nop 0
	v_addc_co_u32_e32 v7, vcc, 0, v15, vcc
	v_add_co_u32_e32 v16, vcc, s36, v14
	global_load_dwordx4 v[2:5], v[14:15], off nt
	s_nop 0
	global_load_dwordx4 v[6:9], v[6:7], off nt
	v_addc_co_u32_e32 v17, vcc, 0, v15, vcc
	v_add_co_u32_e32 v18, vcc, s37, v14
	v_lshlrev_b32_e32 v1, 4, v1
	s_nop 0
	v_addc_co_u32_e32 v19, vcc, 0, v15, vcc
	global_load_dwordx4 v[14:17], v[16:17], off nt
	s_nop 0
	global_load_dwordx4 v[18:21], v[18:19], off nt
	v_lshlrev_b32_e32 v10, 2, v12
	v_ashrrev_i32_e32 v23, 31, v22
	v_mul_u32_u24_e32 v24, 0x204, v24
	v_mul_lo_u32 v25, v22, s38
	v_lshlrev_b64 v[12:13], 12, v[22:23]
	v_add3_u32 v22, 0, v10, v24
	v_and_b32_e32 v10, 0x70, v1
	v_lshlrev_b32_e32 v1, 2, v10
	v_add3_u32 v1, 0, v25, v1
	v_add_u32_e32 v23, 0x400, v22
	s_lshl_b64 s[26:27], s[22:23], 12
	s_barrier
	s_add_u32 s22, s0, s26
	s_addc_u32 s26, s1, s27
	s_lshl_b64 s[24:25], s[24:25], 1
	s_add_u32 s24, s22, s24
	s_addc_u32 s25, s26, s25
	v_lshl_add_u64 v[12:13], s[24:25], 0, v[12:13]
	s_mov_b64 s[24:25], 0
	s_waitcnt vmcnt(2)
	ds_write2_b32 v22, v2, v6 offset1:32
	ds_write2_b32 v22, v3, v7 offset0:129 offset1:161
	ds_write2_b32 v23, v4, v8 offset0:2 offset1:34
	ds_write2_b32 v23, v5, v9 offset0:131 offset1:163
	s_waitcnt vmcnt(0)
	ds_write2_b32 v22, v14, v18 offset0:64 offset1:96
	ds_write2_b32 v22, v15, v19 offset0:193 offset1:225
	ds_write2_b32 v23, v16, v20 offset0:66 offset1:98
	ds_write2_b32 v23, v17, v21 offset0:195 offset1:227
	s_waitcnt lgkmcnt(0)
	s_barrier
	ds_read2_b32 v[2:3], v1 offset1:1
	ds_read2_b32 v[4:5], v1 offset0:2 offset1:3
	ds_read2_b32 v[6:7], v1 offset0:4 offset1:5
	ds_read2_b32 v[8:9], v1 offset0:6 offset1:7
	ds_read2_b32 v[14:15], v1 offset0:8 offset1:9
	ds_read2_b32 v[16:17], v1 offset0:10 offset1:11
	ds_read2_b32 v[18:19], v1 offset0:12 offset1:13
	ds_read2_b32 v[20:21], v1 offset0:14 offset1:15
	s_waitcnt lgkmcnt(7)
	v_cvt_pk_bf16_f32 v2, v2, v3
	s_waitcnt lgkmcnt(6)
	v_cvt_pk_bf16_f32 v3, v4, v5
	s_waitcnt lgkmcnt(5)
	v_cvt_pk_bf16_f32 v4, v6, v7
	s_waitcnt lgkmcnt(4)
	v_cvt_pk_bf16_f32 v5, v8, v9
	s_waitcnt lgkmcnt(3)
	v_cvt_pk_bf16_f32 v6, v14, v15
	s_waitcnt lgkmcnt(2)
	v_cvt_pk_bf16_f32 v7, v16, v17
	s_waitcnt lgkmcnt(1)
	v_cvt_pk_bf16_f32 v8, v18, v19
	s_waitcnt lgkmcnt(0)
	v_cvt_pk_bf16_f32 v9, v20, v21
.LBB0_2121:
	s_andn2_b64 vcc, exec, s[24:25]
	s_cbranch_vccnz .LBB0_2123
	s_add_i32 s22, s28, 0xffffbe00
	s_lshr_b32 s26, s22, 4
	s_lshl_b32 s24, s26, 11
	s_lshl_b32 s22, s22, 7
	s_sub_i32 s24, s22, s24
	s_ashr_i32 s25, s24, 31
	s_lshl_b32 s22, s26, 6
	s_mul_i32 s27, s24, 0x6000
	s_mul_hi_i32 s26, s24, 0x6000
	s_add_u32 s29, s12, s27
	v_mov_b32_e32 v1, v0
	s_addc_u32 s42, s13, s26
	s_lshl_b64 s[26:27], s[22:23], 2
	s_add_u32 s26, s29, s26
	v_lshlrev_b32_e32 v2, 2, v1
	v_and_b32_e32 v22, 60, v2
	s_addc_u32 s27, s42, s27
	v_ashrrev_i32_e32 v21, 4, v1
	v_lshlrev_b32_e32 v10, 2, v22
	v_lshl_add_u64 v[12:13], s[26:27], 0, v[10:11]
	v_add_u32_e32 v10, 64, v21
	v_add_u32_e32 v4, 32, v21
	v_mad_i64_i32 v[14:15], s[26:27], v10, s39, v[12:13]
	v_add_u32_e32 v10, 0x60, v21
	v_mad_i64_i32 v[2:3], s[26:27], v21, s39, v[12:13]
	v_mad_i64_i32 v[6:7], s[26:27], v4, s39, v[12:13]
	v_mad_i64_i32 v[16:17], s[26:27], v10, s39, v[12:13]
	global_load_dwordx4 v[2:5], v[2:3], off nt
	s_nop 0
	global_load_dwordx4 v[6:9], v[6:7], off nt
	s_nop 0
	global_load_dwordx4 v[12:15], v[14:15], off nt
	s_nop 0
	global_load_dwordx4 v[16:19], v[16:17], off nt
	v_ashrrev_i32_e32 v20, 3, v1
	v_lshlrev_b32_e32 v1, 4, v1
	v_lshlrev_b32_e32 v10, 2, v21
	v_mul_u32_u24_e32 v22, 0x204, v22
	v_add3_u32 v22, 0, v10, v22
	v_and_b32_e32 v10, 0x70, v1
	v_mul_lo_u32 v23, v20, s38
	v_lshlrev_b32_e32 v1, 2, v10
	s_lshl_b64 s[26:27], s[22:23], 12
	v_add3_u32 v1, 0, v23, v1
	v_add_u32_e32 v24, 0x400, v22
	s_add_u32 s22, s3, s26
	s_barrier
	s_addc_u32 s26, s4, s27
	s_lshl_b64 s[24:25], s[24:25], 1
	v_ashrrev_i32_e32 v21, 31, v20
	s_add_u32 s24, s22, s24
	v_lshlrev_b64 v[20:21], 12, v[20:21]
	s_addc_u32 s25, s26, s25
	s_waitcnt vmcnt(2)
	ds_write2_b32 v22, v2, v6 offset1:32
	ds_write2_b32 v22, v3, v7 offset0:129 offset1:161
	ds_write2_b32 v24, v4, v8 offset0:2 offset1:34
	ds_write2_b32 v24, v5, v9 offset0:131 offset1:163
	s_waitcnt vmcnt(0)
	ds_write2_b32 v22, v12, v16 offset0:64 offset1:96
	ds_write2_b32 v22, v13, v17 offset0:193 offset1:225
	ds_write2_b32 v24, v14, v18 offset0:66 offset1:98
	ds_write2_b32 v24, v15, v19 offset0:195 offset1:227
	s_waitcnt lgkmcnt(0)
	s_barrier
	ds_read2_b32 v[2:3], v1 offset1:1
	ds_read2_b32 v[4:5], v1 offset0:2 offset1:3
	ds_read2_b32 v[6:7], v1 offset0:4 offset1:5
	ds_read2_b32 v[8:9], v1 offset0:6 offset1:7
	ds_read2_b32 v[12:13], v1 offset0:8 offset1:9
	ds_read2_b32 v[14:15], v1 offset0:10 offset1:11
	ds_read2_b32 v[16:17], v1 offset0:12 offset1:13
	ds_read2_b32 v[18:19], v1 offset0:14 offset1:15
	s_waitcnt lgkmcnt(7)
	v_cvt_pk_bf16_f32 v2, v2, v3
	s_waitcnt lgkmcnt(6)
	v_cvt_pk_bf16_f32 v3, v4, v5
	s_waitcnt lgkmcnt(5)
	v_cvt_pk_bf16_f32 v4, v6, v7
	s_waitcnt lgkmcnt(3)
	v_cvt_pk_bf16_f32 v6, v12, v13
	v_lshl_add_u64 v[12:13], s[24:25], 0, v[20:21]
	v_cvt_pk_bf16_f32 v5, v8, v9
	s_waitcnt lgkmcnt(2)
	v_cvt_pk_bf16_f32 v7, v14, v15
	s_waitcnt lgkmcnt(1)
	v_cvt_pk_bf16_f32 v8, v16, v17
	s_waitcnt lgkmcnt(0)
	v_cvt_pk_bf16_f32 v9, v18, v19

.LBB0_2127:
	s_andn2_b64 vcc, exec, s[24:25]
	s_cbranch_vccnz .LBB0_2108
	s_cmpk_gt_u32 s28, 0x2bff
	s_mov_b64 s[24:25], -1
	s_cbranch_scc0 .LBB0_2130
	s_add_i32 s24, s28, 0xffffd400
	s_mul_i32 s25, s24, 0xba2f
	s_lshr_b32 s25, s25, 24
	s_mul_i32 s26, s25, 0xfffffea0
	s_add_i32 s25, s22, s25
	s_add_i32 s24, s26, s24
	s_mul_i32 s27, s25, 0xb00000
	s_mul_hi_u32 s26, s25, 0xb00000
	s_add_u32 s29, s16, s27
	s_addc_u32 s44, s17, s26
	s_mul_i32 s25, s25, 0x580000
	s_add_u32 s45, s5, s25
	s_mul_i32 s25, s24, 0x1746
	s_addc_u32 s46, s30, 0
	s_lshr_b32 s26, s25, 31
	s_lshr_b32 s25, s25, 16
	s_add_i32 s25, s25, s26
	s_sext_i32_i16 s47, s25
	s_mul_i32 s25, s47, -11
	s_add_i32 s25, s25, s24
	s_lshl_b32 s24, s25, 7
	s_ashr_i32 s25, s24, 31
	s_lshl_b32 s26, s47, 6
	s_ashr_i32 s27, s26, 31
	s_lshl_b64 s[42:43], s[24:25], 13
	s_add_u32 s29, s29, s42
	v_mov_b32_e32 v1, v0
	s_addc_u32 s44, s44, s43
	s_lshl_b64 s[42:43], s[26:27], 2
	s_add_u32 s42, s29, s42
	v_lshlrev_b32_e32 v2, 2, v1
	v_ashrrev_i32_e32 v12, 4, v1
	v_and_b32_e32 v22, 60, v2
	s_addc_u32 s43, s44, s43
	v_lshlrev_b32_e32 v10, 2, v22
	v_ashrrev_i32_e32 v13, 31, v12
	v_lshl_add_u64 v[2:3], s[42:43], 0, v[10:11]
	v_lshlrev_b64 v[4:5], 13, v[12:13]
	v_lshl_add_u64 v[14:15], v[2:3], 0, v[4:5]
	v_add_co_u32_e32 v6, vcc, s35, v14
	v_ashrrev_i32_e32 v23, 3, v1
	s_nop 0
	v_addc_co_u32_e32 v7, vcc, 0, v15, vcc
	v_add_co_u32_e32 v16, vcc, s36, v14
	global_load_dwordx4 v[2:5], v[14:15], off nt
	s_nop 0
	global_load_dwordx4 v[6:9], v[6:7], off nt
	v_addc_co_u32_e32 v17, vcc, 0, v15, vcc
	v_add_co_u32_e32 v18, vcc, s37, v14
	v_lshlrev_b32_e32 v1, 4, v1
	s_nop 0
	v_addc_co_u32_e32 v19, vcc, 0, v15, vcc
	global_load_dwordx4 v[14:17], v[16:17], off nt
	s_nop 0
	global_load_dwordx4 v[18:21], v[18:19], off nt
	v_lshlrev_b32_e32 v10, 2, v12
	v_mul_u32_u24_e32 v13, 0x204, v22
	v_add3_u32 v22, 0, v10, v13
	v_and_b32_e32 v10, 0x70, v1
	v_mul_lo_u32 v12, v23, s38
	s_mul_i32 s47, s47, 0x2c000
	v_lshlrev_b32_e32 v1, 2, v10
	s_mul_hi_i32 s26, s26, 0xb00
	s_add_u32 s27, s45, s47
	v_add3_u32 v1, 0, v12, v1
	v_add_u32_e32 v24, 0x400, v22
	s_addc_u32 s26, s46, s26
	s_lshl_b64 s[24:25], s[24:25], 1
	s_barrier
	s_add_u32 s24, s27, s24
	s_addc_u32 s25, s26, s25
	v_mov_b64_e32 v[12:13], s[24:25]
	v_mad_i64_i32 v[12:13], s[24:25], v23, s40, v[12:13]
	s_mov_b64 s[24:25], 0
	s_waitcnt vmcnt(2)
	ds_write2_b32 v22, v2, v6 offset1:32
	ds_write2_b32 v22, v3, v7 offset0:129 offset1:161
	ds_write2_b32 v24, v4, v8 offset0:2 offset1:34
	ds_write2_b32 v24, v5, v9 offset0:131 offset1:163
	s_waitcnt vmcnt(0)
	ds_write2_b32 v22, v14, v18 offset0:64 offset1:96
	ds_write2_b32 v22, v15, v19 offset0:193 offset1:225
	ds_write2_b32 v24, v16, v20 offset0:66 offset1:98
	ds_write2_b32 v24, v17, v21 offset0:195 offset1:227
	s_waitcnt lgkmcnt(0)
	s_barrier
	ds_read2_b32 v[2:3], v1 offset1:1
	ds_read2_b32 v[4:5], v1 offset0:2 offset1:3
	ds_read2_b32 v[6:7], v1 offset0:4 offset1:5
	ds_read2_b32 v[8:9], v1 offset0:6 offset1:7
	ds_read2_b32 v[14:15], v1 offset0:8 offset1:9
	ds_read2_b32 v[16:17], v1 offset0:10 offset1:11
	ds_read2_b32 v[18:19], v1 offset0:12 offset1:13
	ds_read2_b32 v[20:21], v1 offset0:14 offset1:15
	s_waitcnt lgkmcnt(7)
	v_cvt_pk_bf16_f32 v2, v2, v3
	s_waitcnt lgkmcnt(6)
	v_cvt_pk_bf16_f32 v3, v4, v5
	s_waitcnt lgkmcnt(5)
	v_cvt_pk_bf16_f32 v4, v6, v7
	s_waitcnt lgkmcnt(4)
	v_cvt_pk_bf16_f32 v5, v8, v9
	s_waitcnt lgkmcnt(3)
	v_cvt_pk_bf16_f32 v6, v14, v15
	s_waitcnt lgkmcnt(2)
	v_cvt_pk_bf16_f32 v7, v16, v17
	s_waitcnt lgkmcnt(1)
	v_cvt_pk_bf16_f32 v8, v18, v19
	s_waitcnt lgkmcnt(0)
	v_cvt_pk_bf16_f32 v9, v20, v21
.LBB0_2130:
	s_andn2_b64 vcc, exec, s[24:25]
	s_cbranch_vccnz .LBB0_2108
	s_mul_i32 s24, s28, 0xba2f
	s_lshr_b32 s24, s24, 25
	s_mul_i32 s25, s24, 0xfffffd40
	s_add_i32 s25, s25, s28
	s_mul_i32 s26, s25, 0xba3
	s_lshr_b32 s27, s26, 31
	s_ashr_i32 s26, s26, 20
	s_add_i32 s26, s26, s27
	s_sext_i32_i16 s27, s26
	s_mul_i32 s26, s27, 0xfffffea0
	s_add_i32 s29, s26, s25
	s_add_i32 s22, s22, s24
	s_addk_i32 s25, 0x15f
	s_cmpk_lt_u32 s25, 0x2bf
	s_cselect_b32 s25, s8, s10
	s_mul_i32 s22, s22, 0xb00000
	s_cselect_b32 s24, s9, s11
	s_add_u32 s25, s25, s22
	s_addc_u32 s42, s24, 0
	s_lshl_b32 s24, s29, 2
	s_lshl_b32 s29, s29, 3
	s_and_b32 s29, s29, 0xffffff00
	s_lshl_b32 s27, s27, 7
	s_and_b32 s26, s24, 0xffffffc0
	s_add_i32 s29, s29, s27
	s_and_b32 s24, s24, 64
	s_or_b32 s24, s29, s24
	s_add_u32 s22, s31, s22
	s_addc_u32 s29, s33, 0
	s_lshl_b32 s27, s28, 7
	s_and_b32 s28, s27, 0x780
	s_mul_i32 s27, s28, 0x1600
	s_add_u32 s25, s25, s27
	s_addc_u32 s42, s42, 0
	s_ashr_i32 s27, s26, 31
	v_mov_b32_e32 v1, v0
	s_lshl_b64 s[26:27], s[26:27], 2
	s_add_u32 s26, s25, s26
	v_lshlrev_b32_e32 v2, 2, v1
	v_and_b32_e32 v22, 60, v2
	s_addc_u32 s27, s42, s27
	v_ashrrev_i32_e32 v21, 4, v1
	v_lshlrev_b32_e32 v10, 2, v22
	v_lshl_add_u64 v[12:13], s[26:27], 0, v[10:11]
	v_add_u32_e32 v10, 64, v21
	v_add_u32_e32 v4, 32, v21
	v_mad_i64_i32 v[14:15], s[26:27], v10, s41, v[12:13]
	v_add_u32_e32 v10, 0x60, v21
	v_mad_i64_i32 v[2:3], s[26:27], v21, s41, v[12:13]
	v_mad_i64_i32 v[6:7], s[26:27], v4, s41, v[12:13]
	v_mad_i64_i32 v[16:17], s[26:27], v10, s41, v[12:13]
	global_load_dwordx4 v[2:5], v[2:3], off nt
	s_nop 0
	global_load_dwordx4 v[6:9], v[6:7], off nt
	s_nop 0
	global_load_dwordx4 v[12:15], v[14:15], off nt
	s_nop 0
	global_load_dwordx4 v[16:19], v[16:17], off nt
	v_ashrrev_i32_e32 v20, 3, v1
	v_lshlrev_b32_e32 v1, 4, v1
	v_lshlrev_b32_e32 v10, 2, v21
	v_mul_u32_u24_e32 v22, 0x204, v22
	v_add3_u32 v22, 0, v10, v22
	v_and_b32_e32 v10, 0x70, v1
	v_mul_lo_u32 v23, v20, s38
	s_ashr_i32 s25, s24, 31
	v_lshlrev_b32_e32 v1, 2, v10
	s_lshl_b64 s[24:25], s[24:25], 12
	v_add3_u32 v1, 0, v23, v1
	v_add_u32_e32 v24, 0x400, v22
	s_add_u32 s22, s22, s24
	s_barrier
	s_addc_u32 s25, s29, s25
	s_lshl_b32 s24, s28, 1
	v_ashrrev_i32_e32 v21, 31, v20
	s_add_u32 s24, s22, s24
	v_lshlrev_b64 v[20:21], 12, v[20:21]
	s_addc_u32 s25, s25, 0
	s_waitcnt vmcnt(2)
	ds_write2_b32 v22, v2, v6 offset1:32
	ds_write2_b32 v22, v3, v7 offset0:129 offset1:161
	ds_write2_b32 v24, v4, v8 offset0:2 offset1:34
	ds_write2_b32 v24, v5, v9 offset0:131 offset1:163
	s_waitcnt vmcnt(0)
	ds_write2_b32 v22, v12, v16 offset0:64 offset1:96
	ds_write2_b32 v22, v13, v17 offset0:193 offset1:225
	ds_write2_b32 v24, v14, v18 offset0:66 offset1:98
	ds_write2_b32 v24, v15, v19 offset0:195 offset1:227
	s_waitcnt lgkmcnt(0)
	s_barrier
	ds_read2_b32 v[2:3], v1 offset1:1
	ds_read2_b32 v[4:5], v1 offset0:2 offset1:3
	ds_read2_b32 v[6:7], v1 offset0:4 offset1:5
	ds_read2_b32 v[8:9], v1 offset0:6 offset1:7
	ds_read2_b32 v[12:13], v1 offset0:8 offset1:9
	ds_read2_b32 v[14:15], v1 offset0:10 offset1:11
	ds_read2_b32 v[16:17], v1 offset0:12 offset1:13
	ds_read2_b32 v[18:19], v1 offset0:14 offset1:15
	s_waitcnt lgkmcnt(7)
	v_cvt_pk_bf16_f32 v2, v2, v3
	s_waitcnt lgkmcnt(6)
	v_cvt_pk_bf16_f32 v3, v4, v5
	s_waitcnt lgkmcnt(5)
	v_cvt_pk_bf16_f32 v4, v6, v7
	s_waitcnt lgkmcnt(3)
	v_cvt_pk_bf16_f32 v6, v12, v13
	v_lshl_add_u64 v[12:13], s[24:25], 0, v[20:21]
	v_cvt_pk_bf16_f32 v5, v8, v9
	s_waitcnt lgkmcnt(2)
	v_cvt_pk_bf16_f32 v7, v14, v15
	s_waitcnt lgkmcnt(1)
	v_cvt_pk_bf16_f32 v8, v16, v17
	s_waitcnt lgkmcnt(0)
	v_cvt_pk_bf16_f32 v9, v18, v19
	s_branch .LBB0_2108

.LBB0_2139:
	s_or_b64 exec, exec, s[22:23]
	s_waitcnt lgkmcnt(0)
	s_barrier
	ds_read_b32 v1, v11 offset:40960
	s_mov_b64 s[22:23], -1
	s_waitcnt lgkmcnt(0)
	v_cmp_lt_u32_e32 vcc, s28, v1
	v_readfirstlane_b32 s26, v1
	s_cbranch_vccnz .LBB0_2134
	s_cmpk_lt_u32 s26, 0x4a00
	s_cbranch_scc0 .LBB0_2148
	s_cmpk_gt_u32 s26, 0x41ff
	s_cbranch_scc0 .LBB0_2147
	s_cmpk_gt_u32 s26, 0x47ff
	s_cbranch_scc0 .LBB0_2144
	s_add_i32 s20, s26, 0xffffb800
	s_lshr_b32 s24, s20, 4
	s_lshl_b32 s22, s24, 11
	s_lshl_b32 s20, s20, 7
	s_sub_i32 s22, s20, s22
	s_ashr_i32 s23, s22, 31
	s_lshl_b32 s20, s24, 6
	s_lshl_b64 s[24:25], s[22:23], 13
	s_add_u32 s27, s14, s24
	v_mov_b32_e32 v1, v0
	s_addc_u32 s40, s15, s25
	s_lshl_b64 s[24:25], s[20:21], 2
	s_add_u32 s24, s27, s24
	v_lshlrev_b32_e32 v2, 2, v1
	v_ashrrev_i32_e32 v12, 4, v1
	v_and_b32_e32 v24, 60, v2
	s_addc_u32 s25, s40, s25
	v_lshlrev_b32_e32 v10, 2, v24
	v_ashrrev_i32_e32 v13, 31, v12
	v_lshl_add_u64 v[2:3], s[24:25], 0, v[10:11]
	v_lshlrev_b64 v[4:5], 13, v[12:13]
	v_lshl_add_u64 v[14:15], v[2:3], 0, v[4:5]
	v_add_co_u32_e32 v6, vcc, s29, v14
	v_ashrrev_i32_e32 v22, 3, v1
	s_nop 0
	v_addc_co_u32_e32 v7, vcc, 0, v15, vcc
	v_add_co_u32_e32 v16, vcc, s34, v14
	global_load_dwordx4 v[2:5], v[14:15], off nt
	s_nop 0
	global_load_dwordx4 v[6:9], v[6:7], off nt
	v_addc_co_u32_e32 v17, vcc, 0, v15, vcc
	v_add_co_u32_e32 v18, vcc, s35, v14
	v_lshlrev_b32_e32 v1, 4, v1
	s_nop 0
	v_addc_co_u32_e32 v19, vcc, 0, v15, vcc
	global_load_dwordx4 v[14:17], v[16:17], off nt
	s_nop 0
	global_load_dwordx4 v[18:21], v[18:19], off nt
	v_lshlrev_b32_e32 v10, 2, v12
	v_ashrrev_i32_e32 v23, 31, v22
	v_mul_u32_u24_e32 v24, 0x204, v24
	v_mul_lo_u32 v25, v22, s36
	v_lshlrev_b64 v[12:13], 12, v[22:23]
	v_add3_u32 v22, 0, v10, v24
	v_and_b32_e32 v10, 0x70, v1
	v_lshlrev_b32_e32 v1, 2, v10
	v_add3_u32 v1, 0, v25, v1
	v_add_u32_e32 v23, 0x400, v22
	s_lshl_b64 s[24:25], s[20:21], 12
	s_barrier
	s_add_u32 s20, s0, s24
	s_addc_u32 s24, s1, s25
	s_lshl_b64 s[22:23], s[22:23], 1
	s_add_u32 s22, s20, s22
	s_addc_u32 s23, s24, s23
	v_lshl_add_u64 v[12:13], s[22:23], 0, v[12:13]
	s_mov_b64 s[22:23], 0
	s_waitcnt vmcnt(2)
	ds_write2_b32 v22, v2, v6 offset1:32
	ds_write2_b32 v22, v3, v7 offset0:129 offset1:161
	ds_write2_b32 v23, v4, v8 offset0:2 offset1:34
	ds_write2_b32 v23, v5, v9 offset0:131 offset1:163
	s_waitcnt vmcnt(0)
	ds_write2_b32 v22, v14, v18 offset0:64 offset1:96
	ds_write2_b32 v22, v15, v19 offset0:193 offset1:225
	ds_write2_b32 v23, v16, v20 offset0:66 offset1:98
	ds_write2_b32 v23, v17, v21 offset0:195 offset1:227
	s_waitcnt lgkmcnt(0)
	s_barrier
	ds_read2_b32 v[2:3], v1 offset1:1
	ds_read2_b32 v[4:5], v1 offset0:2 offset1:3
	ds_read2_b32 v[6:7], v1 offset0:4 offset1:5
	ds_read2_b32 v[8:9], v1 offset0:6 offset1:7
	ds_read2_b32 v[14:15], v1 offset0:8 offset1:9
	ds_read2_b32 v[16:17], v1 offset0:10 offset1:11
	ds_read2_b32 v[18:19], v1 offset0:12 offset1:13
	ds_read2_b32 v[20:21], v1 offset0:14 offset1:15
	s_waitcnt lgkmcnt(7)
	v_cvt_pk_bf16_f32 v2, v2, v3
	s_waitcnt lgkmcnt(6)
	v_cvt_pk_bf16_f32 v3, v4, v5
	s_waitcnt lgkmcnt(5)
	v_cvt_pk_bf16_f32 v4, v6, v7
	s_waitcnt lgkmcnt(4)
	v_cvt_pk_bf16_f32 v5, v8, v9
	s_waitcnt lgkmcnt(3)
	v_cvt_pk_bf16_f32 v6, v14, v15
	s_waitcnt lgkmcnt(2)
	v_cvt_pk_bf16_f32 v7, v16, v17
	s_waitcnt lgkmcnt(1)
	v_cvt_pk_bf16_f32 v8, v18, v19
	s_waitcnt lgkmcnt(0)
	v_cvt_pk_bf16_f32 v9, v20, v21

.LBB0_2150:
	s_andn2_b64 vcc, exec, s[22:23]
	s_cbranch_vccnz .LBB0_2133
	s_cmpk_gt_u32 s26, 0x2bff
	s_mov_b64 s[22:23], -1
	s_cbranch_scc0 .LBB0_2153
	s_add_i32 s22, s26, 0xffffd400
	s_mul_i32 s23, s22, 0xba2f
	s_lshr_b32 s23, s23, 24
	s_mul_i32 s24, s23, 0xfffffea0
	s_add_i32 s23, s20, s23
	s_add_i32 s22, s24, s22
	s_mul_i32 s25, s23, 0xb00000
	s_mul_hi_u32 s24, s23, 0xb00000
	s_add_u32 s27, s16, s25
	s_addc_u32 s42, s17, s24
	s_mul_i32 s23, s23, 0x580000
	s_add_u32 s43, s5, s23
	s_mul_i32 s23, s22, 0x1746
	s_addc_u32 s44, s30, 0
	s_lshr_b32 s24, s23, 31
	s_lshr_b32 s23, s23, 16
	s_add_i32 s23, s23, s24
	s_sext_i32_i16 s45, s23
	s_mul_i32 s23, s45, -11
	s_add_i32 s23, s23, s22
	s_lshl_b32 s22, s23, 7
	s_ashr_i32 s23, s22, 31
	s_lshl_b32 s24, s45, 6
	s_ashr_i32 s25, s24, 31
	s_lshl_b64 s[40:41], s[22:23], 13
	s_add_u32 s27, s27, s40
	v_mov_b32_e32 v1, v0
	s_addc_u32 s42, s42, s41
	s_lshl_b64 s[40:41], s[24:25], 2
	s_add_u32 s40, s27, s40
	v_lshlrev_b32_e32 v2, 2, v1
	v_ashrrev_i32_e32 v12, 4, v1
	v_and_b32_e32 v22, 60, v2
	s_addc_u32 s41, s42, s41
	v_lshlrev_b32_e32 v10, 2, v22
	v_ashrrev_i32_e32 v13, 31, v12
	v_lshl_add_u64 v[2:3], s[40:41], 0, v[10:11]
	v_lshlrev_b64 v[4:5], 13, v[12:13]
	v_lshl_add_u64 v[14:15], v[2:3], 0, v[4:5]
	v_add_co_u32_e32 v6, vcc, s29, v14
	v_ashrrev_i32_e32 v23, 3, v1
	s_nop 0
	v_addc_co_u32_e32 v7, vcc, 0, v15, vcc
	v_add_co_u32_e32 v16, vcc, s34, v14
	global_load_dwordx4 v[2:5], v[14:15], off nt
	s_nop 0
	global_load_dwordx4 v[6:9], v[6:7], off nt
	v_addc_co_u32_e32 v17, vcc, 0, v15, vcc
	v_add_co_u32_e32 v18, vcc, s35, v14
	v_lshlrev_b32_e32 v1, 4, v1
	s_nop 0
	v_addc_co_u32_e32 v19, vcc, 0, v15, vcc
	global_load_dwordx4 v[14:17], v[16:17], off nt
	s_nop 0
	global_load_dwordx4 v[18:21], v[18:19], off nt
	v_lshlrev_b32_e32 v10, 2, v12
	v_mul_u32_u24_e32 v13, 0x204, v22
	v_add3_u32 v22, 0, v10, v13
	v_and_b32_e32 v10, 0x70, v1
	v_mul_lo_u32 v12, v23, s36
	s_mul_i32 s45, s45, 0x2c000
	v_lshlrev_b32_e32 v1, 2, v10
	s_mul_hi_i32 s24, s24, 0xb00
	s_add_u32 s25, s43, s45
	v_add3_u32 v1, 0, v12, v1
	v_add_u32_e32 v24, 0x400, v22
	s_addc_u32 s24, s44, s24
	s_lshl_b64 s[22:23], s[22:23], 1
	s_barrier
	s_add_u32 s22, s25, s22
	s_addc_u32 s23, s24, s23
	v_mov_b64_e32 v[12:13], s[22:23]
	v_mad_i64_i32 v[12:13], s[22:23], v23, s38, v[12:13]
	s_mov_b64 s[22:23], 0
	s_waitcnt vmcnt(2)
	ds_write2_b32 v22, v2, v6 offset1:32
	ds_write2_b32 v22, v3, v7 offset0:129 offset1:161
	ds_write2_b32 v24, v4, v8 offset0:2 offset1:34
	ds_write2_b32 v24, v5, v9 offset0:131 offset1:163
	s_waitcnt vmcnt(0)
	ds_write2_b32 v22, v14, v18 offset0:64 offset1:96
	ds_write2_b32 v22, v15, v19 offset0:193 offset1:225
	ds_write2_b32 v24, v16, v20 offset0:66 offset1:98
	ds_write2_b32 v24, v17, v21 offset0:195 offset1:227
	s_waitcnt lgkmcnt(0)
	s_barrier
	ds_read2_b32 v[2:3], v1 offset1:1
	ds_read2_b32 v[4:5], v1 offset0:2 offset1:3
	ds_read2_b32 v[6:7], v1 offset0:4 offset1:5
	ds_read2_b32 v[8:9], v1 offset0:6 offset1:7
	ds_read2_b32 v[14:15], v1 offset0:8 offset1:9
	ds_read2_b32 v[16:17], v1 offset0:10 offset1:11
	ds_read2_b32 v[18:19], v1 offset0:12 offset1:13
	ds_read2_b32 v[20:21], v1 offset0:14 offset1:15
	s_waitcnt lgkmcnt(7)
	v_cvt_pk_bf16_f32 v2, v2, v3
	s_waitcnt lgkmcnt(6)
	v_cvt_pk_bf16_f32 v3, v4, v5
	s_waitcnt lgkmcnt(5)
	v_cvt_pk_bf16_f32 v4, v6, v7
	s_waitcnt lgkmcnt(4)
	v_cvt_pk_bf16_f32 v5, v8, v9
	s_waitcnt lgkmcnt(3)
	v_cvt_pk_bf16_f32 v6, v14, v15
	s_waitcnt lgkmcnt(2)
	v_cvt_pk_bf16_f32 v7, v16, v17
	s_waitcnt lgkmcnt(1)
	v_cvt_pk_bf16_f32 v8, v18, v19
	s_waitcnt lgkmcnt(0)
	v_cvt_pk_bf16_f32 v9, v20, v21
.LBB0_2153:
	s_andn2_b64 vcc, exec, s[22:23]
	s_cbranch_vccnz .LBB0_2133
	s_mul_i32 s22, s26, 0xba2f
	s_lshr_b32 s22, s22, 25
	s_mul_i32 s23, s22, 0xfffffd40
	s_add_i32 s23, s23, s26
	s_mul_i32 s24, s23, 0xba3
	s_lshr_b32 s25, s24, 31
	s_ashr_i32 s24, s24, 20
	s_add_i32 s24, s24, s25
	s_sext_i32_i16 s25, s24
	s_mul_i32 s24, s25, 0xfffffea0
	s_add_i32 s27, s24, s23
	s_add_i32 s20, s20, s22
	s_addk_i32 s23, 0x15f
	s_cmpk_lt_u32 s23, 0x2bf
	s_cselect_b32 s23, s8, s10
	s_mul_i32 s20, s20, 0xb00000
	s_cselect_b32 s22, s9, s11
	s_add_u32 s23, s23, s20
	s_addc_u32 s40, s22, 0
	s_lshl_b32 s22, s27, 2
	s_lshl_b32 s27, s27, 3
	s_and_b32 s27, s27, 0xffffff00
	s_lshl_b32 s25, s25, 7
	s_and_b32 s24, s22, 0xffffffc0
	s_add_i32 s27, s27, s25
	s_and_b32 s22, s22, 64
	s_or_b32 s22, s27, s22
	s_add_u32 s20, s31, s20
	s_addc_u32 s27, s33, 0
	s_lshl_b32 s25, s26, 7
	s_and_b32 s26, s25, 0x780
	s_mul_i32 s25, s26, 0x1600
	s_add_u32 s23, s23, s25
	s_addc_u32 s40, s40, 0
	s_ashr_i32 s25, s24, 31
	v_mov_b32_e32 v1, v0
	s_lshl_b64 s[24:25], s[24:25], 2
	s_add_u32 s24, s23, s24
	v_lshlrev_b32_e32 v2, 2, v1
	v_and_b32_e32 v22, 60, v2
	s_addc_u32 s25, s40, s25
	v_ashrrev_i32_e32 v21, 4, v1
	v_lshlrev_b32_e32 v10, 2, v22
	v_lshl_add_u64 v[12:13], s[24:25], 0, v[10:11]
	v_add_u32_e32 v10, 64, v21
	v_add_u32_e32 v4, 32, v21
	v_mad_i64_i32 v[14:15], s[24:25], v10, s39, v[12:13]
	v_add_u32_e32 v10, 0x60, v21
	v_mad_i64_i32 v[2:3], s[24:25], v21, s39, v[12:13]
	v_mad_i64_i32 v[6:7], s[24:25], v4, s39, v[12:13]
	v_mad_i64_i32 v[16:17], s[24:25], v10, s39, v[12:13]
	global_load_dwordx4 v[2:5], v[2:3], off nt
	s_nop 0
	global_load_dwordx4 v[6:9], v[6:7], off nt
	s_nop 0
	global_load_dwordx4 v[12:15], v[14:15], off nt
	s_nop 0
	global_load_dwordx4 v[16:19], v[16:17], off nt
	v_ashrrev_i32_e32 v20, 3, v1
	v_lshlrev_b32_e32 v1, 4, v1
	v_lshlrev_b32_e32 v10, 2, v21
	v_mul_u32_u24_e32 v22, 0x204, v22
	v_add3_u32 v22, 0, v10, v22
	v_and_b32_e32 v10, 0x70, v1
	v_mul_lo_u32 v23, v20, s36
	s_ashr_i32 s23, s22, 31
	v_lshlrev_b32_e32 v1, 2, v10
	s_lshl_b64 s[22:23], s[22:23], 12
	v_add3_u32 v1, 0, v23, v1
	v_add_u32_e32 v24, 0x400, v22
	s_add_u32 s20, s20, s22
	s_barrier
	s_addc_u32 s23, s27, s23
	s_lshl_b32 s22, s26, 1
	v_ashrrev_i32_e32 v21, 31, v20
	s_add_u32 s22, s20, s22
	v_lshlrev_b64 v[20:21], 12, v[20:21]
	s_addc_u32 s23, s23, 0
	s_waitcnt vmcnt(2)
	ds_write2_b32 v22, v2, v6 offset1:32
	ds_write2_b32 v22, v3, v7 offset0:129 offset1:161
	ds_write2_b32 v24, v4, v8 offset0:2 offset1:34
	ds_write2_b32 v24, v5, v9 offset0:131 offset1:163
	s_waitcnt vmcnt(0)
	ds_write2_b32 v22, v12, v16 offset0:64 offset1:96
	ds_write2_b32 v22, v13, v17 offset0:193 offset1:225
	ds_write2_b32 v24, v14, v18 offset0:66 offset1:98
	ds_write2_b32 v24, v15, v19 offset0:195 offset1:227
	s_waitcnt lgkmcnt(0)
	s_barrier
	ds_read2_b32 v[2:3], v1 offset1:1
	ds_read2_b32 v[4:5], v1 offset0:2 offset1:3
	ds_read2_b32 v[6:7], v1 offset0:4 offset1:5
	ds_read2_b32 v[8:9], v1 offset0:6 offset1:7
	ds_read2_b32 v[12:13], v1 offset0:8 offset1:9
	ds_read2_b32 v[14:15], v1 offset0:10 offset1:11
	ds_read2_b32 v[16:17], v1 offset0:12 offset1:13
	ds_read2_b32 v[18:19], v1 offset0:14 offset1:15
	s_waitcnt lgkmcnt(7)
	v_cvt_pk_bf16_f32 v2, v2, v3
	s_waitcnt lgkmcnt(6)
	v_cvt_pk_bf16_f32 v3, v4, v5
	s_waitcnt lgkmcnt(5)
	v_cvt_pk_bf16_f32 v4, v6, v7
	s_waitcnt lgkmcnt(3)
	v_cvt_pk_bf16_f32 v6, v12, v13
	v_lshl_add_u64 v[12:13], s[22:23], 0, v[20:21]
	v_cvt_pk_bf16_f32 v5, v8, v9
	s_waitcnt lgkmcnt(2)
	v_cvt_pk_bf16_f32 v7, v14, v15
	s_waitcnt lgkmcnt(1)
	v_cvt_pk_bf16_f32 v8, v16, v17
	s_waitcnt lgkmcnt(0)
	v_cvt_pk_bf16_f32 v9, v18, v19
	s_branch .LBB0_2133
